# weight converters: 304 dead zero-inits in front of lo/hi v_cvt_pk_fp8 pairs removed (less VALU per converted tile), P1 GEMM share 144
# baseline (speedup 1.0000x reference)
; __device__ __forceinline__ unsigned pk4_fp8(float a, float b, float c, float d) { unsigned w = 0u; w = __builtin_amdgcn_cvt_pk_fp8_f32(a, b, w, false); w = __builtin_amdgcn_cvt_pk_fp8_f32(c, d, w, true); return w; }
; #define LAS __attribute__((address_space(3)))
; #define CVT_LOAD(v, c, s_) do { _Pragma("unroll") for (int i_ = 0; i_ < 16; ++i_) v[i_] = *(const f32x4*)((c).src + (size_t)(64 * (s_) + i_) * (c).N); } while (0)
; __device__ __forceinline__ void cvt_pack8(const f32x4 (&v)[16], const CvtItem& c, LAS unsigned char* blk, int s4, int lane) {
;     const float w = c.wscale; const int cb = lane & 15, j = 4 * s4 + (lane >> 4);
; #pragma unroll
;     for (int jn = 0; jn < 4; ++jn) {
;         v4u o; o.x = pg8::pk4_fp8(v[0][jn] * w, v[1][jn] * w, v[2][jn] * w, v[3][jn] * w); o.y = pg8::pk4_fp8(v[4][jn] * w, v[5][jn] * w, v[6][jn] * w, v[7][jn] * w);
;         o.z = pg8::pk4_fp8(v[8][jn] * w, v[9][jn] * w, v[10][jn] * w, v[11][jn] * w); o.w = pg8::pk4_fp8(v[12][jn] * w, v[13][jn] * w, v[14][jn] * w, v[15][jn] * w);
;         *(LAS v4u*)(blk + (4 * cb + jn) * 256 + ((j ^ cb) * 16)) = o; }
; }
; __device__ __forceinline__ void cvt_moe_pipe2(const CvtSrc& A, const CvtSrc& B, LAS float* scr, int gw, int NGW, int lane) {
;     LAS unsigned char* blk = (LAS unsigned char*)scr;
;     f32x4 va[16], vb[16]; CvtItem c, cn;
;     const int it1 = A.n + B.n; int it = gw;
;     if (it < it1) { c = cvt_moe_item2(it, A, B, lane); CVT_LOAD(va, c, 0); }
;     while (it < it1) {
;         const int i1 = it + NGW; const bool more = i1 < it1;
;         CVT_LOAD(vb, c, 1); cvt_pack8(va, c, blk, 0, lane);
;         CVT_LOAD(va, c, 2); cvt_pack8(vb, c, blk, 1, lane);
;         CVT_LOAD(vb, c, 3); cvt_pack8(va, c, blk, 2, lane);
;         if (more) { cn = cvt_moe_item2(i1, A, B, lane); CVT_LOAD(va, cn, 0); }
;         cvt_pack8(vb, c, blk, 3, lane);
.LBB0_111:
	s_ashr_i32 s5, s4, 31
	s_lshl_b64 s[0:1], s[4:5], 8
	v_lshl_add_u64 v[66:67], v[136:137], 0, s[0:1]
	s_lshl_b64 s[24:25], s[4:5], 2
	global_load_dwordx4 v[70:73], v[66:67], off nt
	v_lshl_add_u64 v[66:67], v[66:67], 0, s[24:25]
	global_load_dwordx4 v[98:101], v[66:67], off nt
	v_lshl_add_u64 v[66:67], v[66:67], 0, s[24:25]
	global_load_dwordx4 v[110:113], v[66:67], off nt
	v_lshl_add_u64 v[66:67], v[66:67], 0, s[24:25]
	global_load_dwordx4 v[118:121], v[66:67], off nt
	v_lshl_add_u64 v[66:67], v[66:67], 0, s[24:25]
	global_load_dwordx4 v[102:105], v[66:67], off nt
	v_lshl_add_u64 v[66:67], v[66:67], 0, s[24:25]
	global_load_dwordx4 v[114:117], v[66:67], off nt
	v_lshl_add_u64 v[66:67], v[66:67], 0, s[24:25]
	global_load_dwordx4 v[122:125], v[66:67], off nt
	v_lshl_add_u64 v[66:67], v[66:67], 0, s[24:25]
	v_lshl_add_u64 v[74:75], v[66:67], 0, s[24:25]
	global_load_dwordx4 v[126:129], v[66:67], off nt
	s_waitcnt vmcnt(8)
	v_mul_f32_e32 v62, v62, v195
	global_load_dwordx4 v[66:69], v[74:75], off nt
	v_lshl_add_u64 v[74:75], v[74:75], 0, s[24:25]
	global_load_dwordx4 v[90:93], v[74:75], off nt
	v_lshl_add_u64 v[74:75], v[74:75], 0, s[24:25]
	global_load_dwordx4 v[94:97], v[74:75], off nt
	v_lshl_add_u64 v[74:75], v[74:75], 0, s[24:25]
	v_lshl_add_u64 v[78:79], v[74:75], 0, s[24:25]
	v_lshl_add_u64 v[82:83], v[78:79], 0, s[24:25]
	global_load_dwordx4 v[106:109], v[74:75], off nt
	v_lshl_add_u64 v[86:87], v[82:83], 0, s[24:25]
	global_load_dwordx4 v[74:77], v[78:79], off nt
	v_lshl_add_u64 v[138:139], v[86:87], 0, s[24:25]
	global_load_dwordx4 v[78:81], v[82:83], off nt
	v_mul_f32_e32 v46, v46, v195
	global_load_dwordx4 v[82:85], v[86:87], off nt
	global_load_dwordx4 v[86:89], v[138:139], off nt
	v_cvt_pk_fp8_f32 v198, v62, v46
	v_mul_f32_e32 v42, v42, v195
	v_mul_f32_e32 v58, v58, v195
	v_mul_f32_e32 v10, v10, v195
	v_mul_f32_e32 v26, v26, v195
	v_cvt_pk_fp8_f32 v198, v42, v58 op_sel:[0,0,1]
	v_mul_f32_e32 v34, v34, v195
	v_mul_f32_e32 v42, v50, v195
	v_cvt_pk_fp8_f32 v200, v10, v26
	v_mul_f32_e32 v2, v2, v195
	v_mul_f32_e32 v10, v22, v195
	v_cvt_pk_fp8_f32 v199, v34, v42
	v_cvt_pk_fp8_f32 v201, v2, v10
	v_mul_f32_e32 v14, v14, v195
	v_mul_f32_e32 v30, v30, v195
	v_mul_f32_e32 v38, v38, v195
	v_mul_f32_e32 v46, v54, v195
	v_cvt_pk_fp8_f32 v200, v14, v30 op_sel:[0,0,1]
	v_mul_f32_e32 v6, v6, v195
	v_mul_f32_e32 v14, v18, v195
	v_cvt_pk_fp8_f32 v199, v38, v46 op_sel:[0,0,1]
	v_cvt_pk_fp8_f32 v201, v6, v14 op_sel:[0,0,1]
	v_mul_f32_e32 v2, v63, v195
	v_mul_f32_e32 v6, v47, v195
	v_mul_f32_e32 v10, v43, v195
	ds_write_b128 v156, v[198:201]
	v_cvt_pk_fp8_f32 v198, v2, v6
	v_mul_f32_e32 v2, v35, v195
	v_mul_f32_e32 v6, v51, v195
	v_cvt_pk_fp8_f32 v199, v2, v6
	v_mul_f32_e32 v2, v11, v195
	v_mul_f32_e32 v6, v27, v195
	v_cvt_pk_fp8_f32 v200, v2, v6
	v_mul_f32_e32 v2, v3, v195
	v_mul_f32_e32 v3, v23, v195
	v_cvt_pk_fp8_f32 v201, v2, v3
	v_mul_f32_e32 v14, v59, v195
	v_cvt_pk_fp8_f32 v198, v10, v14 op_sel:[0,0,1]
	v_mul_f32_e32 v10, v39, v195
	v_mul_f32_e32 v14, v55, v195
	v_cvt_pk_fp8_f32 v199, v10, v14 op_sel:[0,0,1]
	v_mul_f32_e32 v10, v15, v195
	v_mul_f32_e32 v11, v31, v195
	v_mul_f32_e32 v6, v7, v195
	v_mul_f32_e32 v7, v19, v195
	v_cvt_pk_fp8_f32 v200, v10, v11 op_sel:[0,0,1]
	v_cvt_pk_fp8_f32 v201, v6, v7 op_sel:[0,0,1]
	v_mul_f32_e32 v2, v64, v195
	v_mul_f32_e32 v3, v48, v195
	v_mul_f32_e32 v6, v44, v195
	ds_write_b128 v156, v[198:201] offset:256
	v_cvt_pk_fp8_f32 v198, v2, v3
	v_mul_f32_e32 v2, v36, v195
	v_mul_f32_e32 v3, v52, v195
	v_cvt_pk_fp8_f32 v199, v2, v3
	v_mul_f32_e32 v2, v12, v195
	v_mul_f32_e32 v3, v28, v195
	v_cvt_pk_fp8_f32 v200, v2, v3
	v_mul_f32_e32 v2, v4, v195
	v_mul_f32_e32 v3, v24, v195
	v_mul_f32_e32 v7, v60, v195
	v_cvt_pk_fp8_f32 v201, v2, v3
	v_cvt_pk_fp8_f32 v198, v6, v7 op_sel:[0,0,1]
	v_mul_f32_e32 v6, v40, v195
	v_mul_f32_e32 v7, v56, v195
	v_cvt_pk_fp8_f32 v199, v6, v7 op_sel:[0,0,1]
	v_mul_f32_e32 v6, v16, v195
	v_mul_f32_e32 v7, v32, v195
	v_cvt_pk_fp8_f32 v200, v6, v7 op_sel:[0,0,1]
	v_mul_f32_e32 v4, v8, v195
	v_mul_f32_e32 v6, v20, v195
	v_cvt_pk_fp8_f32 v201, v4, v6 op_sel:[0,0,1]
	v_mul_f32_e32 v3, v65, v195
	v_mul_f32_e32 v4, v49, v195
	v_cvt_pk_fp8_f32 v2, v3, v4
	v_mul_f32_e32 v6, v45, v195
	v_mul_f32_e32 v7, v61, v195
	v_mul_f32_e32 v4, v37, v195
	v_cvt_pk_fp8_f32 v2, v6, v7 op_sel:[0,0,1]
	v_mul_f32_e32 v6, v53, v195
	v_cvt_pk_fp8_f32 v3, v4, v6
	v_mul_f32_e32 v7, v41, v195
	v_mul_f32_e32 v8, v57, v195
	v_mul_f32_e32 v6, v13, v195
	v_cvt_pk_fp8_f32 v3, v7, v8 op_sel:[0,0,1]
	v_mul_f32_e32 v7, v29, v195
	ds_write_b128 v156, v[198:201] offset:512
	v_cvt_pk_fp8_f32 v4, v6, v7
	v_mul_f32_e32 v6, v5, v195
	v_mul_f32_e32 v7, v25, v195
	s_waitcnt vmcnt(15)
	v_mul_f32_e32 v70, v195, v70
	s_waitcnt vmcnt(14)
	v_mul_f32_e32 v98, v195, v98
	v_cvt_pk_fp8_f32 v5, v6, v7
	v_cvt_pk_fp8_f32 v198, v70, v98
	s_waitcnt vmcnt(11)
	v_mul_f32_e32 v70, v195, v102
	s_waitcnt vmcnt(10)
	v_mul_f32_e32 v98, v195, v114
	v_cvt_pk_fp8_f32 v199, v70, v98
	s_waitcnt vmcnt(7)
	v_mul_f32_e32 v66, v195, v66
	s_waitcnt vmcnt(6)
	v_mul_f32_e32 v70, v195, v90
	v_mul_f32_e32 v8, v17, v195
	v_mul_f32_e32 v10, v33, v195
	v_cvt_pk_fp8_f32 v200, v66, v70
	s_waitcnt vmcnt(3)
	v_mul_f32_e32 v66, v195, v74
	s_waitcnt vmcnt(2)
	v_mul_f32_e32 v70, v195, v78
	v_cvt_pk_fp8_f32 v4, v8, v10 op_sel:[0,0,1]
	v_mul_f32_e32 v8, v9, v195
	v_mul_f32_e32 v9, v21, v195
	v_cvt_pk_fp8_f32 v201, v66, v70
	v_cvt_pk_fp8_f32 v5, v8, v9 op_sel:[0,0,1]
	v_mul_f32_e32 v110, v195, v110
	v_mul_f32_e32 v118, v195, v118
	v_cvt_pk_fp8_f32 v198, v110, v118 op_sel:[0,0,1]
	v_mul_f32_e32 v102, v195, v122
	v_mul_f32_e32 v110, v195, v126
	v_mul_f32_e32 v90, v195, v94
	v_mul_f32_e32 v94, v195, v106
	s_waitcnt vmcnt(1)
; __device__ __forceinline__ unsigned pk4_fp8(float a, float b, float c, float d) { unsigned w = 0u; w = __builtin_amdgcn_cvt_pk_fp8_f32(a, b, w, false); w = __builtin_amdgcn_cvt_pk_fp8_f32(c, d, w, true); return w; }
; #define LAS __attribute__((address_space(3)))
; #define CVT_LOAD(v, c, s_) do { _Pragma("unroll") for (int i_ = 0; i_ < 16; ++i_) v[i_] = *(const f32x4*)((c).src + (size_t)(64 * (s_) + i_) * (c).N); } while (0)
; __device__ __forceinline__ void cvt_pack8(const f32x4 (&v)[16], const CvtItem& c, LAS unsigned char* blk, int s4, int lane) {
;     const float w = c.wscale; const int cb = lane & 15, j = 4 * s4 + (lane >> 4);
; #pragma unroll
;     for (int jn = 0; jn < 4; ++jn) {
;         v4u o; o.x = pg8::pk4_fp8(v[0][jn] * w, v[1][jn] * w, v[2][jn] * w, v[3][jn] * w); o.y = pg8::pk4_fp8(v[4][jn] * w, v[5][jn] * w, v[6][jn] * w, v[7][jn] * w);
;         o.z = pg8::pk4_fp8(v[8][jn] * w, v[9][jn] * w, v[10][jn] * w, v[11][jn] * w); o.w = pg8::pk4_fp8(v[12][jn] * w, v[13][jn] * w, v[14][jn] * w, v[15][jn] * w);
;         *(LAS v4u*)(blk + (4 * cb + jn) * 256 + ((j ^ cb) * 16)) = o; }
; }
; __device__ __forceinline__ void cvt_moe_pipe2(const CvtSrc& A, const CvtSrc& B, LAS float* scr, int gw, int NGW, int lane) {
;     LAS unsigned char* blk = (LAS unsigned char*)scr;
;     f32x4 va[16], vb[16]; CvtItem c, cn;
;     const int it1 = A.n + B.n; int it = gw;
;     if (it < it1) { c = cvt_moe_item2(it, A, B, lane); CVT_LOAD(va, c, 0); }
;     while (it < it1) {
;         const int i1 = it + NGW; const bool more = i1 < it1;
;         CVT_LOAD(vb, c, 1); cvt_pack8(va, c, blk, 0, lane);
;         CVT_LOAD(va, c, 2); cvt_pack8(vb, c, blk, 1, lane);
;         CVT_LOAD(vb, c, 3); cvt_pack8(va, c, blk, 2, lane);
;         if (more) { cn = cvt_moe_item2(i1, A, B, lane); CVT_LOAD(va, cn, 0); }
;         cvt_pack8(vb, c, blk, 3, lane);
	v_mul_f32_e32 v74, v195, v82
	s_waitcnt vmcnt(0)
	v_mul_f32_e32 v78, v195, v86
	v_cvt_pk_fp8_f32 v199, v102, v110 op_sel:[0,0,1]
	v_cvt_pk_fp8_f32 v200, v90, v94 op_sel:[0,0,1]
	v_cvt_pk_fp8_f32 v201, v74, v78 op_sel:[0,0,1]
	ds_write_b128 v156, v[2:5] offset:768
	v_mad_i64_i32 v[2:3], s[0:1], s4, v176, v[138:139]
	global_load_dwordx4 v[62:65], v[2:3], off nt
	v_lshl_add_u64 v[2:3], v[2:3], 0, s[24:25]
	global_load_dwordx4 v[46:49], v[2:3], off nt
	v_lshl_add_u64 v[2:3], v[2:3], 0, s[24:25]
	global_load_dwordx4 v[42:45], v[2:3], off nt
	v_lshl_add_u64 v[2:3], v[2:3], 0, s[24:25]
	ds_write_b128 v157, v[198:201]
	v_mul_f32_e32 v66, v195, v71
	v_mul_f32_e32 v70, v195, v99
	global_load_dwordx4 v[58:61], v[2:3], off nt
	v_lshl_add_u64 v[2:3], v[2:3], 0, s[24:25]
	v_cvt_pk_fp8_f32 v198, v66, v70
	v_mul_f32_e32 v66, v195, v103
	v_mul_f32_e32 v70, v195, v115
	global_load_dwordx4 v[34:37], v[2:3], off nt
	v_lshl_add_u64 v[2:3], v[2:3], 0, s[24:25]
	v_cvt_pk_fp8_f32 v199, v66, v70
	v_mul_f32_e32 v66, v195, v67
	v_mul_f32_e32 v67, v195, v91
	global_load_dwordx4 v[50:53], v[2:3], off nt
	v_lshl_add_u64 v[2:3], v[2:3], 0, s[24:25]
	v_cvt_pk_fp8_f32 v200, v66, v67
	v_mul_f32_e32 v66, v195, v75
	v_mul_f32_e32 v67, v195, v79
	global_load_dwordx4 v[38:41], v[2:3], off nt
	v_lshl_add_u64 v[2:3], v[2:3], 0, s[24:25]
	v_mul_f32_e32 v71, v195, v111
	v_mul_f32_e32 v74, v195, v119
	v_cvt_pk_fp8_f32 v201, v66, v67
	global_load_dwordx4 v[54:57], v[2:3], off nt
	v_lshl_add_u64 v[2:3], v[2:3], 0, s[24:25]
	v_cvt_pk_fp8_f32 v198, v71, v74 op_sel:[0,0,1]
	v_mul_f32_e32 v71, v195, v123
	v_mul_f32_e32 v74, v195, v127
	global_load_dwordx4 v[10:13], v[2:3], off nt
	v_lshl_add_u64 v[2:3], v[2:3], 0, s[24:25]
	v_cvt_pk_fp8_f32 v199, v71, v74 op_sel:[0,0,1]
	v_mul_f32_e32 v70, v195, v95
	v_mul_f32_e32 v71, v195, v107
	global_load_dwordx4 v[26:29], v[2:3], off nt
	v_lshl_add_u64 v[2:3], v[2:3], 0, s[24:25]
	v_cvt_pk_fp8_f32 v200, v70, v71 op_sel:[0,0,1]
	v_mul_f32_e32 v70, v195, v83
	v_mul_f32_e32 v71, v195, v87
	global_load_dwordx4 v[14:17], v[2:3], off nt
	v_lshl_add_u64 v[2:3], v[2:3], 0, s[24:25]
	v_cvt_pk_fp8_f32 v201, v70, v71 op_sel:[0,0,1]
	v_lshl_add_u64 v[6:7], v[2:3], 0, s[24:25]
	global_load_dwordx4 v[30:33], v[2:3], off nt
	v_mul_f32_e32 v66, v195, v72
	global_load_dwordx4 v[2:5], v[6:7], off nt
	v_lshl_add_u64 v[6:7], v[6:7], 0, s[24:25]
	global_load_dwordx4 v[22:25], v[6:7], off nt
	ds_write_b128 v157, v[198:201] offset:256
	v_mul_f32_e32 v67, v195, v100
	v_lshl_add_u64 v[18:19], v[6:7], 0, s[24:25]
	v_cvt_pk_fp8_f32 v198, v66, v67
	v_mul_f32_e32 v66, v195, v104
	v_mul_f32_e32 v67, v195, v116
	v_lshl_add_u64 v[138:139], v[18:19], 0, s[24:25]
	v_cvt_pk_fp8_f32 v199, v66, v67
	v_mul_f32_e32 v66, v195, v68
	v_mul_f32_e32 v67, v195, v92
	global_load_dwordx4 v[6:9], v[18:19], off nt
	v_cvt_pk_fp8_f32 v200, v66, v67
	global_load_dwordx4 v[18:21], v[138:139], off nt
	v_mul_f32_e32 v66, v195, v76
	v_mul_f32_e32 v67, v195, v80
	v_mul_f32_e32 v70, v195, v112
	v_mul_f32_e32 v71, v195, v120
	v_cvt_pk_fp8_f32 v201, v66, v67
	v_cvt_pk_fp8_f32 v198, v70, v71 op_sel:[0,0,1]
	v_mul_f32_e32 v70, v195, v124
	v_mul_f32_e32 v71, v195, v128
	v_cvt_pk_fp8_f32 v199, v70, v71 op_sel:[0,0,1]
	v_mul_f32_e32 v68, v195, v96
	v_mul_f32_e32 v70, v195, v108
	v_cvt_pk_fp8_f32 v200, v68, v70 op_sel:[0,0,1]
	v_mul_f32_e32 v68, v195, v84
	v_mul_f32_e32 v70, v195, v88
	v_cvt_pk_fp8_f32 v201, v68, v70 op_sel:[0,0,1]
	v_mul_f32_e32 v67, v195, v73
	v_mul_f32_e32 v68, v195, v101
	v_cvt_pk_fp8_f32 v66, v67, v68
	v_mul_f32_e32 v70, v195, v113
	v_mul_f32_e32 v71, v195, v121
	v_mul_f32_e32 v68, v195, v105
	v_cvt_pk_fp8_f32 v66, v70, v71 op_sel:[0,0,1]
	v_mul_f32_e32 v70, v195, v117
	v_cvt_pk_fp8_f32 v67, v68, v70
	v_mul_f32_e32 v69, v195, v69
	v_mul_f32_e32 v70, v195, v93
	v_cvt_pk_fp8_f32 v68, v69, v70
	v_mul_f32_e32 v71, v195, v125
	v_mul_f32_e32 v72, v195, v129
	v_cvt_pk_fp8_f32 v67, v71, v72 op_sel:[0,0,1]
	v_mul_f32_e32 v71, v195, v97
	v_mul_f32_e32 v72, v195, v109
	v_cvt_pk_fp8_f32 v68, v71, v72 op_sel:[0,0,1]
	v_mul_f32_e32 v70, v195, v77
	v_mul_f32_e32 v71, v195, v81
	v_cvt_pk_fp8_f32 v69, v70, v71
	v_mul_f32_e32 v72, v195, v85
	v_mul_f32_e32 v73, v195, v89
	ds_write_b128 v157, v[198:201] offset:512
	v_cvt_pk_fp8_f32 v69, v72, v73 op_sel:[0,0,1]
	s_waitcnt vmcnt(15)
	v_mul_f32_e32 v130, v195, v62
	s_waitcnt vmcnt(14)
	v_mul_f32_e32 v135, v195, v46
	ds_write_b128 v157, v[66:69] offset:768
	v_mad_i64_i32 v[66:67], s[0:1], s4, v176, v[138:139]
	global_load_dwordx4 v[110:113], v[66:67], off nt
	v_lshl_add_u64 v[66:67], v[66:67], 0, s[24:25]
	global_load_dwordx4 v[118:121], v[66:67], off nt
	v_lshl_add_u64 v[66:67], v[66:67], 0, s[24:25]
	global_load_dwordx4 v[122:125], v[66:67], off nt
	v_lshl_add_u64 v[66:67], v[66:67], 0, s[24:25]
	global_load_dwordx4 v[126:129], v[66:67], off nt
	v_lshl_add_u64 v[66:67], v[66:67], 0, s[24:25]
	global_load_dwordx4 v[98:101], v[66:67], off nt
	v_lshl_add_u64 v[66:67], v[66:67], 0, s[24:25]
	global_load_dwordx4 v[102:105], v[66:67], off nt
	v_lshl_add_u64 v[66:67], v[66:67], 0, s[24:25]
	global_load_dwordx4 v[106:109], v[66:67], off nt
	v_lshl_add_u64 v[66:67], v[66:67], 0, s[24:25]
	global_load_dwordx4 v[114:117], v[66:67], off nt
	v_lshl_add_u64 v[66:67], v[66:67], 0, s[24:25]
	global_load_dwordx4 v[78:81], v[66:67], off nt
	v_lshl_add_u64 v[66:67], v[66:67], 0, s[24:25]
	global_load_dwordx4 v[86:89], v[66:67], off nt
	v_lshl_add_u64 v[66:67], v[66:67], 0, s[24:25]
	global_load_dwordx4 v[90:93], v[66:67], off nt
	v_lshl_add_u64 v[66:67], v[66:67], 0, s[24:25]
	v_lshl_add_u64 v[70:71], v[66:67], 0, s[24:25]
	v_lshl_add_u64 v[74:75], v[70:71], 0, s[24:25]
	v_lshl_add_u64 v[82:83], v[74:75], 0, s[24:25]
	global_load_dwordx4 v[94:97], v[66:67], off nt
	v_cvt_pk_fp8_f32 v198, v130, v135
	global_load_dwordx4 v[66:69], v[70:71], off nt
	s_waitcnt vmcnt(24)
; __device__ __forceinline__ unsigned pk4_fp8(float a, float b, float c, float d) { unsigned w = 0u; w = __builtin_amdgcn_cvt_pk_fp8_f32(a, b, w, false); w = __builtin_amdgcn_cvt_pk_fp8_f32(c, d, w, true); return w; }
; #define LAS __attribute__((address_space(3)))
; #define CVT_LOAD(v, c, s_) do { _Pragma("unroll") for (int i_ = 0; i_ < 16; ++i_) v[i_] = *(const f32x4*)((c).src + (size_t)(64 * (s_) + i_) * (c).N); } while (0)
; __device__ __forceinline__ void cvt_pack8(const f32x4 (&v)[16], const CvtItem& c, LAS unsigned char* blk, int s4, int lane) {
;     const float w = c.wscale; const int cb = lane & 15, j = 4 * s4 + (lane >> 4);
; #pragma unroll
;     for (int jn = 0; jn < 4; ++jn) {
;         v4u o; o.x = pg8::pk4_fp8(v[0][jn] * w, v[1][jn] * w, v[2][jn] * w, v[3][jn] * w); o.y = pg8::pk4_fp8(v[4][jn] * w, v[5][jn] * w, v[6][jn] * w, v[7][jn] * w);
;         o.z = pg8::pk4_fp8(v[8][jn] * w, v[9][jn] * w, v[10][jn] * w, v[11][jn] * w); o.w = pg8::pk4_fp8(v[12][jn] * w, v[13][jn] * w, v[14][jn] * w, v[15][jn] * w);
;         *(LAS v4u*)(blk + (4 * cb + jn) * 256 + ((j ^ cb) * 16)) = o; }
; }
; __device__ __forceinline__ CvtItem cvt_moe_item2(int j, const CvtSrc& A, const CvtSrc& B, int lane) {
;     return (j < A.n) ? cvt_moe_item(A.it0 + j, A.wg, A.wu, A.wd, A.WGU, A.WDN, lane) : cvt_moe_item(B.it0 + (j - A.n), B.wg, B.wu, B.wd, B.WGU, B.WDN, lane);
; }
; __device__ __forceinline__ void cvt_moe_pipe2(const CvtSrc& A, const CvtSrc& B, LAS float* scr, int gw, int NGW, int lane) {
;     LAS unsigned char* blk = (LAS unsigned char*)scr;
;     f32x4 va[16], vb[16]; CvtItem c, cn;
;     const int it1 = A.n + B.n; int it = gw;
;     if (it < it1) { c = cvt_moe_item2(it, A, B, lane); CVT_LOAD(va, c, 0); }
;     while (it < it1) {
;         const int i1 = it + NGW; const bool more = i1 < it1;
;         CVT_LOAD(vb, c, 1); cvt_pack8(va, c, blk, 0, lane);
;         CVT_LOAD(va, c, 2); cvt_pack8(vb, c, blk, 1, lane);
;         CVT_LOAD(vb, c, 3); cvt_pack8(va, c, blk, 2, lane);
;         if (more) { cn = cvt_moe_item2(i1, A, B, lane); CVT_LOAD(va, cn, 0); }
;         cvt_pack8(vb, c, blk, 3, lane);
;         cvt_flush8(c, blk, lane);
;         if (more) c = cn;
;         it = i1;
	v_mul_f32_e32 v130, v195, v34
	global_load_dwordx4 v[70:73], v[74:75], off nt
	s_waitcnt vmcnt(24)
	v_mul_f32_e32 v135, v195, v50
	global_load_dwordx4 v[74:77], v[82:83], off nt
	v_lshl_add_u64 v[82:83], v[82:83], 0, s[24:25]
	global_load_dwordx4 v[82:85], v[82:83], off nt
	v_cvt_pk_fp8_f32 v199, v130, v135
	s_waitcnt vmcnt(23)
	v_mul_f32_e32 v130, v195, v10
	s_waitcnt vmcnt(22)
	v_mul_f32_e32 v135, v195, v26
	v_cvt_pk_fp8_f32 v200, v130, v135
	s_waitcnt vmcnt(19)
	v_mul_f32_e32 v130, v195, v2
	s_waitcnt vmcnt(18)
	v_mul_f32_e32 v135, v195, v22
	v_mul_f32_e32 v138, v195, v42
	v_mul_f32_e32 v139, v195, v58
	v_cvt_pk_fp8_f32 v201, v130, v135
	v_cvt_pk_fp8_f32 v198, v138, v139 op_sel:[0,0,1]
	v_mul_f32_e32 v138, v195, v38
	v_mul_f32_e32 v139, v195, v54
	v_cvt_pk_fp8_f32 v199, v138, v139 op_sel:[0,0,1]
	v_mul_f32_e32 v138, v195, v14
	v_mul_f32_e32 v139, v195, v30
	v_cvt_pk_fp8_f32 v200, v138, v139 op_sel:[0,0,1]
	s_waitcnt vmcnt(17)
	v_mul_f32_e32 v138, v195, v6
	s_waitcnt vmcnt(16)
	v_mul_f32_e32 v139, v195, v18
	v_cvt_pk_fp8_f32 v201, v138, v139 op_sel:[0,0,1]
	v_mul_f32_e32 v130, v195, v63
	v_mul_f32_e32 v135, v195, v47
	v_mul_f32_e32 v138, v195, v43
	ds_write_b128 v158, v[198:201]
	v_cvt_pk_fp8_f32 v198, v130, v135
	v_mul_f32_e32 v130, v195, v35
	v_mul_f32_e32 v135, v195, v51
	v_cvt_pk_fp8_f32 v199, v130, v135
	v_mul_f32_e32 v130, v195, v11
	v_mul_f32_e32 v135, v195, v27
	v_cvt_pk_fp8_f32 v200, v130, v135
	v_mul_f32_e32 v130, v195, v3
	v_mul_f32_e32 v135, v195, v23
	v_mul_f32_e32 v139, v195, v59
	v_cvt_pk_fp8_f32 v201, v130, v135
	v_cvt_pk_fp8_f32 v198, v138, v139 op_sel:[0,0,1]
	v_mul_f32_e32 v138, v195, v39
	v_mul_f32_e32 v139, v195, v55
	v_cvt_pk_fp8_f32 v199, v138, v139 op_sel:[0,0,1]
	v_mul_f32_e32 v138, v195, v15
	v_mul_f32_e32 v139, v195, v31
	v_cvt_pk_fp8_f32 v200, v138, v139 op_sel:[0,0,1]
	v_mul_f32_e32 v138, v195, v7
	v_mul_f32_e32 v139, v195, v19
	v_cvt_pk_fp8_f32 v201, v138, v139 op_sel:[0,0,1]
	v_mul_f32_e32 v130, v195, v64
	v_mul_f32_e32 v135, v195, v48
	v_mul_f32_e32 v138, v195, v44
	ds_write_b128 v158, v[198:201] offset:256
	v_cvt_pk_fp8_f32 v198, v130, v135
	v_mul_f32_e32 v130, v195, v36
	v_mul_f32_e32 v135, v195, v52
	v_cvt_pk_fp8_f32 v199, v130, v135
	v_mul_f32_e32 v130, v195, v12
	v_mul_f32_e32 v135, v195, v28
	v_cvt_pk_fp8_f32 v200, v130, v135
	v_mul_f32_e32 v130, v195, v4
	v_mul_f32_e32 v135, v195, v24
	v_mul_f32_e32 v139, v195, v60
	v_cvt_pk_fp8_f32 v201, v130, v135
	v_cvt_pk_fp8_f32 v198, v138, v139 op_sel:[0,0,1]
	v_mul_f32_e32 v138, v195, v40
	v_mul_f32_e32 v139, v195, v56
	v_cvt_pk_fp8_f32 v199, v138, v139 op_sel:[0,0,1]
	v_mul_f32_e32 v138, v195, v16
	v_mul_f32_e32 v139, v195, v32
	v_cvt_pk_fp8_f32 v200, v138, v139 op_sel:[0,0,1]
	v_mul_f32_e32 v138, v195, v8
	v_mul_f32_e32 v139, v195, v20
	v_cvt_pk_fp8_f32 v201, v138, v139 op_sel:[0,0,1]
	v_mul_f32_e32 v130, v195, v65
	v_mul_f32_e32 v135, v195, v49
	v_mul_f32_e32 v138, v195, v45
	ds_write_b128 v158, v[198:201] offset:512
	v_cvt_pk_fp8_f32 v198, v130, v135
	v_mul_f32_e32 v130, v195, v37
	v_mul_f32_e32 v135, v195, v53
	v_cvt_pk_fp8_f32 v199, v130, v135
	v_mul_f32_e32 v130, v195, v13
	v_mul_f32_e32 v135, v195, v29
	v_cvt_pk_fp8_f32 v200, v130, v135
	v_mul_f32_e32 v130, v195, v5
	v_mul_f32_e32 v135, v195, v25
	v_mul_f32_e32 v139, v195, v61
	v_cvt_pk_fp8_f32 v201, v130, v135
	v_cvt_pk_fp8_f32 v198, v138, v139 op_sel:[0,0,1]
	v_mul_f32_e32 v138, v195, v41
	v_mul_f32_e32 v139, v195, v57
	v_cvt_pk_fp8_f32 v199, v138, v139 op_sel:[0,0,1]
	v_mul_f32_e32 v138, v195, v17
	v_mul_f32_e32 v139, v195, v33
	v_cvt_pk_fp8_f32 v200, v138, v139 op_sel:[0,0,1]
	v_mul_f32_e32 v138, v195, v9
	v_mul_f32_e32 v139, v195, v21
	s_add_i32 s36, s36, s38
	v_cvt_pk_fp8_f32 v201, v138, v139 op_sel:[0,0,1]
	s_cmpk_gt_i32 s36, 0x25df
	s_cselect_b64 s[24:25], -1, 0
	s_and_b64 vcc, exec, s[24:25]
	ds_write_b128 v158, v[198:201] offset:768
	s_cbranch_vccnz .LBB0_110
	s_cmpk_gt_i32 s36, 0x17ff
	s_mov_b64 s[30:31], -1
	s_cbranch_scc0 .LBB0_116
	s_add_i32 s8, s36, 0xfffff220
	s_cmpk_gt_u32 s8, 0xfff
	s_cbranch_scc0 .LBB0_121
	v_readlane_b32 s28, v254, 2
	v_readlane_b32 s29, v254, 3
	s_and_b32 s45, s36, 15
	s_and_b32 s0, s41, 0x700
	v_readlane_b32 s30, v254, 4
	v_readlane_b32 s31, v254, 5
	s_mov_b64 s[26:27], s[28:29]
	s_cbranch_execz .LBB0_122
	v_readlane_b32 s22, v255, 3
	s_mov_b32 s1, 10
	s_mov_b64 s[28:29], 21
	s_movk_i32 s4, 0x400
	s_movk_i32 s47, 0x800
	s_mov_b32 s46, 2
	s_mov_b32 s5, 0x42800000
	v_readlane_b32 s23, v255, 4
	s_mov_b64 s[30:31], 0

; __device__ __forceinline__ unsigned pk4_fp8(float a, float b, float c, float d) { unsigned w = 0u; w = __builtin_amdgcn_cvt_pk_fp8_f32(a, b, w, false); w = __builtin_amdgcn_cvt_pk_fp8_f32(c, d, w, true); return w; }
; #define LAS __attribute__((address_space(3)))
; #define LDS_WAIT() asm volatile("s_waitcnt lgkmcnt(0)" ::: "memory")
; __device__ __forceinline__ void cvt_pack8(const f32x4 (&v)[16], const CvtItem& c, LAS unsigned char* blk, int s4, int lane) {
;     const float w = c.wscale; const int cb = lane & 15, j = 4 * s4 + (lane >> 4);
; #pragma unroll
;     for (int jn = 0; jn < 4; ++jn) {
;         v4u o; o.x = pg8::pk4_fp8(v[0][jn] * w, v[1][jn] * w, v[2][jn] * w, v[3][jn] * w); o.y = pg8::pk4_fp8(v[4][jn] * w, v[5][jn] * w, v[6][jn] * w, v[7][jn] * w);
;         o.z = pg8::pk4_fp8(v[8][jn] * w, v[9][jn] * w, v[10][jn] * w, v[11][jn] * w); o.w = pg8::pk4_fp8(v[12][jn] * w, v[13][jn] * w, v[14][jn] * w, v[15][jn] * w);
;         *(LAS v4u*)(blk + (4 * cb + jn) * 256 + ((j ^ cb) * 16)) = o; }
; }
; __device__ __forceinline__ void cvt_flush8(const CvtItem& c, const LAS unsigned char* blk, int lane) {
;     LDS_WAIT();
; #pragma unroll
;     for (int t = 0; t < 16; ++t) { const int idx = 64 * t + lane, n = idx >> 4, pc = idx & 15, nn = c.nb * 64 + n;
;         const size_t row = (c.which < 2) ? (size_t)((nn >> 7) * 256 + (nn & 127) + c.which * 128) : (size_t)nn;
;         *(v4u*)(c.dst + row * c.K + 16 * pc) = *(const LAS v4u*)(blk + n * 256 + ((pc ^ ((n >> 2) & 15)) * 16)); }
;     LDS_WAIT();
; }
.LBB0_717:
	s_waitcnt vmcnt(7)
	v_mul_f32_e32 v66, v179, v66
	s_waitcnt vmcnt(6)
	v_mul_f32_e32 v70, v179, v70
	v_cvt_pk_fp8_f32 v180, v66, v70
	v_mul_f32_e32 v66, v179, v78
	v_mul_f32_e32 v70, v179, v90
	v_cvt_pk_fp8_f32 v181, v66, v70
	s_waitcnt vmcnt(5)
	v_mul_f32_e32 v66, v179, v86
	s_waitcnt vmcnt(4)
	v_mul_f32_e32 v70, v179, v98
	v_cvt_pk_fp8_f32 v182, v66, v70
	s_waitcnt vmcnt(3)
	v_mul_f32_e32 v66, v179, v110
	s_waitcnt vmcnt(2)
	v_mul_f32_e32 v70, v179, v118
	v_mul_f32_e32 v74, v179, v74
	v_mul_f32_e32 v82, v179, v82
	v_cvt_pk_fp8_f32 v183, v66, v70
	v_cvt_pk_fp8_f32 v180, v74, v82 op_sel:[0,0,1]
	v_mul_f32_e32 v74, v179, v94
	v_mul_f32_e32 v78, v179, v106
	v_cvt_pk_fp8_f32 v181, v74, v78 op_sel:[0,0,1]
	v_mul_f32_e32 v74, v179, v102
	v_mul_f32_e32 v78, v179, v114
	v_cvt_pk_fp8_f32 v182, v74, v78 op_sel:[0,0,1]
	s_waitcnt vmcnt(1)
	v_mul_f32_e32 v74, v179, v122
	s_waitcnt vmcnt(0)
	v_mul_f32_e32 v78, v179, v126
	v_cvt_pk_fp8_f32 v183, v74, v78 op_sel:[0,0,1]
	v_mul_f32_e32 v66, v179, v67
	v_mul_f32_e32 v67, v179, v71
	v_mul_f32_e32 v70, v179, v75
	ds_write_b128 v161, v[180:183]
	v_cvt_pk_fp8_f32 v180, v66, v67
	v_mul_f32_e32 v66, v179, v79
	v_mul_f32_e32 v67, v179, v91
	v_cvt_pk_fp8_f32 v181, v66, v67
	v_mul_f32_e32 v66, v179, v87
	v_mul_f32_e32 v67, v179, v99
	v_cvt_pk_fp8_f32 v182, v66, v67
	v_mul_f32_e32 v66, v179, v111
	v_mul_f32_e32 v67, v179, v119
	v_mul_f32_e32 v71, v179, v83
	v_cvt_pk_fp8_f32 v183, v66, v67
	v_cvt_pk_fp8_f32 v180, v70, v71 op_sel:[0,0,1]
	v_mul_f32_e32 v70, v179, v95
	v_mul_f32_e32 v71, v179, v107
	v_cvt_pk_fp8_f32 v181, v70, v71 op_sel:[0,0,1]
	v_mul_f32_e32 v70, v179, v103
	v_mul_f32_e32 v71, v179, v115
	v_cvt_pk_fp8_f32 v182, v70, v71 op_sel:[0,0,1]
	v_mul_f32_e32 v70, v179, v123
	v_mul_f32_e32 v71, v179, v127
	v_cvt_pk_fp8_f32 v183, v70, v71 op_sel:[0,0,1]
	v_mul_f32_e32 v66, v179, v68
	v_mul_f32_e32 v67, v179, v72
	v_mul_f32_e32 v68, v179, v76
	ds_write_b128 v161, v[180:183] offset:256
	v_cvt_pk_fp8_f32 v180, v66, v67
	v_mul_f32_e32 v66, v179, v80
	v_mul_f32_e32 v67, v179, v92
	v_cvt_pk_fp8_f32 v181, v66, v67
	v_mul_f32_e32 v66, v179, v88
	v_mul_f32_e32 v67, v179, v100
	v_cvt_pk_fp8_f32 v182, v66, v67
	v_mul_f32_e32 v66, v179, v112
	v_mul_f32_e32 v67, v179, v120
	v_mul_f32_e32 v70, v179, v84
	v_cvt_pk_fp8_f32 v183, v66, v67
	v_cvt_pk_fp8_f32 v180, v68, v70 op_sel:[0,0,1]
	v_mul_f32_e32 v68, v179, v96
	v_mul_f32_e32 v70, v179, v108
	v_cvt_pk_fp8_f32 v181, v68, v70 op_sel:[0,0,1]
	v_mul_f32_e32 v68, v179, v104
	v_mul_f32_e32 v70, v179, v116
	v_cvt_pk_fp8_f32 v182, v68, v70 op_sel:[0,0,1]
	v_mul_f32_e32 v68, v179, v124
	v_mul_f32_e32 v70, v179, v128
	v_cvt_pk_fp8_f32 v183, v68, v70 op_sel:[0,0,1]
	v_mul_f32_e32 v67, v179, v69
	v_mul_f32_e32 v68, v179, v73
	v_cvt_pk_fp8_f32 v66, v67, v68
	v_mul_f32_e32 v69, v179, v77
	v_mul_f32_e32 v70, v179, v85
	v_mul_f32_e32 v68, v179, v81
	v_cvt_pk_fp8_f32 v66, v69, v70 op_sel:[0,0,1]
	v_mul_f32_e32 v69, v179, v93
	v_cvt_pk_fp8_f32 v67, v68, v69
	v_mul_f32_e32 v70, v179, v97
	v_mul_f32_e32 v71, v179, v109
	v_mul_f32_e32 v69, v179, v89
	v_cvt_pk_fp8_f32 v67, v70, v71 op_sel:[0,0,1]
	v_mul_f32_e32 v70, v179, v101
	v_cvt_pk_fp8_f32 v68, v69, v70
	v_mul_f32_e32 v71, v179, v105
	v_mul_f32_e32 v72, v179, v117
	v_mul_f32_e32 v70, v179, v113
	v_cvt_pk_fp8_f32 v68, v71, v72 op_sel:[0,0,1]
	v_mul_f32_e32 v71, v179, v121
	v_cvt_pk_fp8_f32 v69, v70, v71
	v_mul_f32_e32 v72, v179, v125
	v_mul_f32_e32 v73, v179, v129
	s_lshl_b32 s4, s31, 6
	v_cvt_pk_fp8_f32 v69, v72, v73 op_sel:[0,0,1]
	s_and_b32 s31, s31, 0x1fffffe
	ds_write_b128 v161, v[180:183] offset:512
	s_and_b32 s4, s4, 64
	ds_write_b128 v161, v[66:69] offset:768
	s_add_i32 s31, s31, s30
	s_waitcnt lgkmcnt(0)
	v_or_b32_e32 v66, s4, v142
	s_lshl_b32 s30, s31, 7
	v_or_b32_e32 v70, s30, v66
	ds_read_b128 v[66:69], v162
	v_ashrrev_i32_e32 v71, 31, v70
	v_lshlrev_b64 v[70:71], 10, v[70:71]
	v_lshl_add_u64 v[70:71], s[6:7], 0, v[70:71]
	v_lshl_add_u64 v[70:71], v[70:71], 0, v[134:135]
	s_waitcnt lgkmcnt(0)
	global_store_dwordx4 v[70:71], v[66:69], off nt
	s_add_i32 s25, s25, s26
	s_andn2_b64 vcc, exec, s[2:3]
	v_or_b32_e32 v66, s4, v143
	v_or_b32_e32 v70, s30, v66
	ds_read_b128 v[66:69], v163
	v_ashrrev_i32_e32 v71, 31, v70
	v_lshlrev_b64 v[70:71], 10, v[70:71]
	v_lshl_add_u64 v[70:71], s[6:7], 0, v[70:71]
	v_lshl_add_u64 v[70:71], v[70:71], 0, v[134:135]
	s_waitcnt lgkmcnt(0)
	global_store_dwordx4 v[70:71], v[66:69], off nt
	s_mov_b32 s31, s28
	v_mov_b32_e32 v179, v178
	v_or_b32_e32 v66, s4, v144
	v_or_b32_e32 v70, s30, v66
	ds_read_b128 v[66:69], v164
	v_ashrrev_i32_e32 v71, 31, v70
	v_lshlrev_b64 v[70:71], 10, v[70:71]
	v_lshl_add_u64 v[70:71], s[6:7], 0, v[70:71]
	v_lshl_add_u64 v[70:71], v[70:71], 0, v[134:135]
	s_waitcnt lgkmcnt(0)
	global_store_dwordx4 v[70:71], v[66:69], off nt
	s_nop 1
	v_or_b32_e32 v66, s4, v145
	v_or_b32_e32 v70, s30, v66
	ds_read_b128 v[66:69], v165
	v_ashrrev_i32_e32 v71, 31, v70
	v_lshlrev_b64 v[70:71], 10, v[70:71]
	v_lshl_add_u64 v[70:71], s[6:7], 0, v[70:71]
	v_lshl_add_u64 v[70:71], v[70:71], 0, v[134:135]
	s_waitcnt lgkmcnt(0)
	global_store_dwordx4 v[70:71], v[66:69], off nt
	s_nop 1
	v_or_b32_e32 v66, s4, v146
	v_or_b32_e32 v70, s30, v66
	ds_read_b128 v[66:69], v166
	v_ashrrev_i32_e32 v71, 31, v70
	v_lshlrev_b64 v[70:71], 10, v[70:71]
	v_lshl_add_u64 v[70:71], s[6:7], 0, v[70:71]
	v_lshl_add_u64 v[70:71], v[70:71], 0, v[134:135]
	s_waitcnt lgkmcnt(0)
	global_store_dwordx4 v[70:71], v[66:69], off nt
	s_nop 1
	v_or_b32_e32 v66, s4, v147
	v_or_b32_e32 v70, s30, v66
	ds_read_b128 v[66:69], v167
	v_ashrrev_i32_e32 v71, 31, v70
	v_lshlrev_b64 v[70:71], 10, v[70:71]
	v_lshl_add_u64 v[70:71], s[6:7], 0, v[70:71]
	v_lshl_add_u64 v[70:71], v[70:71], 0, v[134:135]
	s_waitcnt lgkmcnt(0)
; #define LAS __attribute__((address_space(3)))
; #define LDS_WAIT() asm volatile("s_waitcnt lgkmcnt(0)" ::: "memory")
; __device__ __forceinline__ void cvt_flush8(const CvtItem& c, const LAS unsigned char* blk, int lane) {
;     LDS_WAIT();
; #pragma unroll
;     for (int t = 0; t < 16; ++t) { const int idx = 64 * t + lane, n = idx >> 4, pc = idx & 15, nn = c.nb * 64 + n;
;         const size_t row = (c.which < 2) ? (size_t)((nn >> 7) * 256 + (nn & 127) + c.which * 128) : (size_t)nn;
;         *(v4u*)(c.dst + row * c.K + 16 * pc) = *(const LAS v4u*)(blk + n * 256 + ((pc ^ ((n >> 2) & 15)) * 16)); }
;     LDS_WAIT();
; }
	global_store_dwordx4 v[70:71], v[66:69], off nt
	s_nop 1
	v_or_b32_e32 v66, s4, v148
	v_or_b32_e32 v70, s30, v66
	ds_read_b128 v[66:69], v168
	v_ashrrev_i32_e32 v71, 31, v70
	v_lshlrev_b64 v[70:71], 10, v[70:71]
	v_lshl_add_u64 v[70:71], s[6:7], 0, v[70:71]
	v_lshl_add_u64 v[70:71], v[70:71], 0, v[134:135]
	s_waitcnt lgkmcnt(0)
	global_store_dwordx4 v[70:71], v[66:69], off nt
	s_nop 1
	v_or_b32_e32 v66, s4, v149
	v_or_b32_e32 v70, s30, v66
	ds_read_b128 v[66:69], v169
	v_ashrrev_i32_e32 v71, 31, v70
	v_lshlrev_b64 v[70:71], 10, v[70:71]
	v_lshl_add_u64 v[70:71], s[6:7], 0, v[70:71]
	v_lshl_add_u64 v[70:71], v[70:71], 0, v[134:135]
	s_waitcnt lgkmcnt(0)
	global_store_dwordx4 v[70:71], v[66:69], off nt
	s_nop 1
	v_or_b32_e32 v66, s4, v150
	v_or_b32_e32 v70, s30, v66
	ds_read_b128 v[66:69], v170
	v_ashrrev_i32_e32 v71, 31, v70
	v_lshlrev_b64 v[70:71], 10, v[70:71]
	v_lshl_add_u64 v[70:71], s[6:7], 0, v[70:71]
	v_lshl_add_u64 v[70:71], v[70:71], 0, v[134:135]
	s_waitcnt lgkmcnt(0)
	global_store_dwordx4 v[70:71], v[66:69], off nt
	s_nop 1
	v_or_b32_e32 v66, s4, v151
	v_or_b32_e32 v70, s30, v66
	ds_read_b128 v[66:69], v171
	v_ashrrev_i32_e32 v71, 31, v70
	v_lshlrev_b64 v[70:71], 10, v[70:71]
	v_lshl_add_u64 v[70:71], s[6:7], 0, v[70:71]
	v_lshl_add_u64 v[70:71], v[70:71], 0, v[134:135]
	s_waitcnt lgkmcnt(0)
	global_store_dwordx4 v[70:71], v[66:69], off nt
	s_nop 1
	v_or_b32_e32 v66, s4, v152
	v_or_b32_e32 v70, s30, v66
	ds_read_b128 v[66:69], v172
	v_ashrrev_i32_e32 v71, 31, v70
	v_lshlrev_b64 v[70:71], 10, v[70:71]
	v_lshl_add_u64 v[70:71], s[6:7], 0, v[70:71]
	v_lshl_add_u64 v[70:71], v[70:71], 0, v[134:135]
	s_waitcnt lgkmcnt(0)
	global_store_dwordx4 v[70:71], v[66:69], off nt
	s_nop 1
	v_or_b32_e32 v66, s4, v153
	v_or_b32_e32 v70, s30, v66
	ds_read_b128 v[66:69], v173
	v_ashrrev_i32_e32 v71, 31, v70
	v_lshlrev_b64 v[70:71], 10, v[70:71]
	v_lshl_add_u64 v[70:71], s[6:7], 0, v[70:71]
	v_lshl_add_u64 v[70:71], v[70:71], 0, v[134:135]
	s_waitcnt lgkmcnt(0)
	global_store_dwordx4 v[70:71], v[66:69], off nt
	s_nop 1
	v_or_b32_e32 v66, s4, v154
	v_or_b32_e32 v70, s30, v66
	ds_read_b128 v[66:69], v174
	v_ashrrev_i32_e32 v71, 31, v70
	v_lshlrev_b64 v[70:71], 10, v[70:71]
	v_lshl_add_u64 v[70:71], s[6:7], 0, v[70:71]
	v_lshl_add_u64 v[70:71], v[70:71], 0, v[134:135]
	s_waitcnt lgkmcnt(0)
	global_store_dwordx4 v[70:71], v[66:69], off nt
	s_nop 1
	v_or_b32_e32 v66, s4, v155
	v_or_b32_e32 v70, s30, v66
	ds_read_b128 v[66:69], v175
	v_ashrrev_i32_e32 v71, 31, v70
	v_lshlrev_b64 v[70:71], 10, v[70:71]
	v_lshl_add_u64 v[70:71], s[6:7], 0, v[70:71]
	v_lshl_add_u64 v[70:71], v[70:71], 0, v[134:135]
	s_waitcnt lgkmcnt(0)
	global_store_dwordx4 v[70:71], v[66:69], off nt
	s_nop 1
	v_or_b32_e32 v66, s4, v156
	v_or_b32_e32 v70, s30, v66
	ds_read_b128 v[66:69], v176
	v_ashrrev_i32_e32 v71, 31, v70
	v_lshlrev_b64 v[70:71], 10, v[70:71]
	v_lshl_add_u64 v[70:71], s[6:7], 0, v[70:71]
	v_lshl_add_u64 v[70:71], v[70:71], 0, v[134:135]
	s_waitcnt lgkmcnt(0)
	global_store_dwordx4 v[70:71], v[66:69], off nt
	s_nop 1
	v_or_b32_e32 v66, s4, v157
	v_or_b32_e32 v70, s30, v66
	ds_read_b128 v[66:69], v177
	v_ashrrev_i32_e32 v71, 31, v70
	v_lshlrev_b64 v[70:71], 10, v[70:71]
	v_lshl_add_u64 v[70:71], s[6:7], 0, v[70:71]
	v_lshl_add_u64 v[70:71], v[70:71], 0, v[134:135]
	s_waitcnt lgkmcnt(0)
	global_store_dwordx4 v[70:71], v[66:69], off nt
	s_waitcnt lgkmcnt(0)
	s_mov_b64 s[6:7], s[8:9]
	s_mov_b32 s30, s27
	s_cbranch_vccz .LBB0_720
.LBB0_718:
	v_readlane_b32 s2, v254, 52
	s_add_i32 s29, s29, s2
	s_mov_b32 s2, 0x80000
	v_add_co_u32_e32 v66, vcc, s2, v132
	s_mov_b32 s2, 0x82000
	s_nop 0
	v_addc_co_u32_e32 v67, vcc, 0, v133, vcc
	v_add_co_u32_e32 v70, vcc, s2, v132
	s_mov_b32 s2, 0x84000
	s_nop 0
	v_addc_co_u32_e32 v71, vcc, 0, v133, vcc
	v_add_co_u32_e32 v74, vcc, s2, v132
	s_mov_b32 s2, 0x86000
	s_nop 0
	v_addc_co_u32_e32 v75, vcc, 0, v133, vcc
	v_add_co_u32_e32 v78, vcc, s2, v132
	s_mov_b32 s2, 0x88000
	s_nop 0
	v_addc_co_u32_e32 v79, vcc, 0, v133, vcc
	global_load_dwordx4 v[82:85], v[78:79], off nt
	v_add_co_u32_e32 v78, vcc, s2, v132
	s_mov_b32 s2, 0x8a000
	s_nop 0
	v_addc_co_u32_e32 v79, vcc, 0, v133, vcc
	v_add_co_u32_e32 v86, vcc, s2, v132
	s_mov_b32 s2, 0x8c000
	s_nop 0
	v_addc_co_u32_e32 v87, vcc, 0, v133, vcc
	global_load_dwordx4 v[90:93], v[86:87], off nt
	v_add_co_u32_e32 v86, vcc, s2, v132
	s_mov_b32 s2, 0x8e000
	s_nop 0
	v_addc_co_u32_e32 v87, vcc, 0, v133, vcc
	global_load_dwordx4 v[94:97], v[86:87], off nt
	v_add_co_u32_e32 v86, vcc, s2, v132
	s_mov_b32 s2, 0x90000
	s_nop 0
	v_addc_co_u32_e32 v87, vcc, 0, v133, vcc
	global_load_dwordx4 v[106:109], v[86:87], off nt
	v_add_co_u32_e32 v86, vcc, s2, v132
	s_mov_b32 s2, 0x92000
	s_nop 0
	v_addc_co_u32_e32 v87, vcc, 0, v133, vcc
	v_add_co_u32_e32 v98, vcc, s2, v132
	s_mov_b32 s2, 0x94000
	s_nop 0
	v_addc_co_u32_e32 v99, vcc, 0, v133, vcc
	v_add_co_u32_e32 v102, vcc, s2, v132
	s_waitcnt vmcnt(4)
; __device__ __forceinline__ unsigned pk4_fp8(float a, float b, float c, float d) { unsigned w = 0u; w = __builtin_amdgcn_cvt_pk_fp8_f32(a, b, w, false); w = __builtin_amdgcn_cvt_pk_fp8_f32(c, d, w, true); return w; }
; #define LAS __attribute__((address_space(3)))
; #define CVT_LOAD(v, c, s_) do { _Pragma("unroll") for (int i_ = 0; i_ < 16; ++i_) v[i_] = *(const f32x4*)((c).src + (size_t)(64 * (s_) + i_) * (c).N); } while (0)
; __device__ __forceinline__ void cvt_pack8(const f32x4 (&v)[16], const CvtItem& c, LAS unsigned char* blk, int s4, int lane) {
;     const float w = c.wscale; const int cb = lane & 15, j = 4 * s4 + (lane >> 4);
; #pragma unroll
;     for (int jn = 0; jn < 4; ++jn) {
;         v4u o; o.x = pg8::pk4_fp8(v[0][jn] * w, v[1][jn] * w, v[2][jn] * w, v[3][jn] * w); o.y = pg8::pk4_fp8(v[4][jn] * w, v[5][jn] * w, v[6][jn] * w, v[7][jn] * w);
;         o.z = pg8::pk4_fp8(v[8][jn] * w, v[9][jn] * w, v[10][jn] * w, v[11][jn] * w); o.w = pg8::pk4_fp8(v[12][jn] * w, v[13][jn] * w, v[14][jn] * w, v[15][jn] * w);
;         *(LAS v4u*)(blk + (4 * cb + jn) * 256 + ((j ^ cb) * 16)) = o; }
; }
; __device__ __forceinline__ void cvt_moe_pipe2(const CvtSrc& A, const CvtSrc& B, LAS float* scr, int gw, int NGW, int lane) {
;     LAS unsigned char* blk = (LAS unsigned char*)scr;
;     f32x4 va[16], vb[16]; CvtItem c, cn;
;     const int it1 = A.n + B.n; int it = gw;
;     if (it < it1) { c = cvt_moe_item2(it, A, B, lane); CVT_LOAD(va, c, 0); }
;     while (it < it1) {
;         const int i1 = it + NGW; const bool more = i1 < it1;
;         CVT_LOAD(vb, c, 1); cvt_pack8(va, c, blk, 0, lane);
;         CVT_LOAD(va, c, 2); cvt_pack8(vb, c, blk, 1, lane);
;         CVT_LOAD(vb, c, 3); cvt_pack8(va, c, blk, 2, lane);
;         if (more) { cn = cvt_moe_item2(i1, A, B, lane); CVT_LOAD(va, cn, 0); }
;         cvt_pack8(vb, c, blk, 3, lane);
	v_mul_f32_e32 v62, v62, v179
	v_mul_f32_e32 v6, v6, v179
	v_addc_co_u32_e32 v103, vcc, 0, v133, vcc
	s_mov_b32 s2, 0x96000
	v_cvt_pk_fp8_f32 v180, v62, v6
	v_add_co_u32_e32 v110, vcc, s2, v132
	s_mov_b32 s2, 0x98000
	s_nop 0
	v_addc_co_u32_e32 v111, vcc, 0, v133, vcc
	global_load_dwordx4 v[102:105], v[102:103], off nt
	v_mul_f32_e32 v2, v2, v179
	global_load_dwordx4 v[114:117], v[110:111], off nt
	v_add_co_u32_e32 v110, vcc, s2, v132
	v_mul_f32_e32 v18, v18, v179
	global_load_dwordx4 v[66:69], v[66:67], off nt
	v_addc_co_u32_e32 v111, vcc, 0, v133, vcc
	global_load_dwordx4 v[70:73], v[70:71], off nt
	s_mov_b32 s2, 0x9a000
	v_cvt_pk_fp8_f32 v180, v2, v18 op_sel:[0,0,1]
	v_mul_f32_e32 v2, v10, v179
	v_mul_f32_e32 v6, v26, v179
	global_load_dwordx4 v[78:81], v[78:79], off nt
	v_add_co_u32_e32 v118, vcc, s2, v132
	v_cvt_pk_fp8_f32 v181, v2, v6
	v_mul_f32_e32 v2, v14, v179
	v_mul_f32_e32 v6, v34, v179
	global_load_dwordx4 v[86:89], v[86:87], off nt
	v_addc_co_u32_e32 v119, vcc, 0, v133, vcc
	global_load_dwordx4 v[98:101], v[98:99], off nt
	s_mov_b32 s2, 0x9c000
	v_cvt_pk_fp8_f32 v182, v2, v6
	v_mul_f32_e32 v2, v38, v179
	v_mul_f32_e32 v6, v54, v179
	global_load_dwordx4 v[110:113], v[110:111], off nt
	v_add_co_u32_e32 v122, vcc, s2, v132
	global_load_dwordx4 v[118:121], v[118:119], off nt
	v_cvt_pk_fp8_f32 v183, v2, v6
	global_load_dwordx4 v[74:77], v[74:75], off nt
	v_addc_co_u32_e32 v123, vcc, 0, v133, vcc
	s_mov_b32 s2, 0x9e000
	v_mul_f32_e32 v10, v22, v179
	v_mul_f32_e32 v18, v42, v179
	v_add_co_u32_e32 v126, vcc, s2, v132
	v_cvt_pk_fp8_f32 v181, v10, v18 op_sel:[0,0,1]
	v_mul_f32_e32 v10, v30, v179
	v_mul_f32_e32 v14, v46, v179
	v_addc_co_u32_e32 v127, vcc, 0, v133, vcc
	v_cvt_pk_fp8_f32 v182, v10, v14 op_sel:[0,0,1]
	v_mul_f32_e32 v10, v50, v179
	v_mul_f32_e32 v14, v58, v179
	global_load_dwordx4 v[122:125], v[122:123], off nt
	v_cvt_pk_fp8_f32 v183, v10, v14 op_sel:[0,0,1]
	global_load_dwordx4 v[126:129], v[126:127], off nt
	v_mul_f32_e32 v2, v63, v179
	v_mul_f32_e32 v6, v7, v179
	ds_write_b128 v158, v[180:183]
	v_cvt_pk_fp8_f32 v180, v2, v6
	v_mul_f32_e32 v3, v3, v179
	v_mul_f32_e32 v7, v19, v179
	v_mul_f32_e32 v2, v11, v179
	v_cvt_pk_fp8_f32 v180, v3, v7 op_sel:[0,0,1]
	v_mul_f32_e32 v3, v27, v179
	v_cvt_pk_fp8_f32 v181, v2, v3
	v_mul_f32_e32 v2, v15, v179
	v_mul_f32_e32 v3, v35, v179
	v_cvt_pk_fp8_f32 v182, v2, v3
	v_mul_f32_e32 v2, v39, v179
	v_mul_f32_e32 v3, v55, v179
	v_cvt_pk_fp8_f32 v183, v2, v3
	v_mul_f32_e32 v6, v23, v179
	v_mul_f32_e32 v7, v43, v179
	v_cvt_pk_fp8_f32 v181, v6, v7 op_sel:[0,0,1]
	v_mul_f32_e32 v6, v31, v179
	v_mul_f32_e32 v7, v47, v179
	v_cvt_pk_fp8_f32 v182, v6, v7 op_sel:[0,0,1]
	v_mul_f32_e32 v6, v51, v179
	v_mul_f32_e32 v7, v59, v179
	v_cvt_pk_fp8_f32 v183, v6, v7 op_sel:[0,0,1]
	v_mul_f32_e32 v2, v64, v179
	v_mul_f32_e32 v3, v8, v179
	v_mul_f32_e32 v4, v4, v179
	ds_write_b128 v158, v[180:183] offset:256
	v_cvt_pk_fp8_f32 v180, v2, v3
	v_mul_f32_e32 v2, v12, v179
	v_mul_f32_e32 v3, v28, v179
	v_cvt_pk_fp8_f32 v181, v2, v3
	v_mul_f32_e32 v2, v16, v179
	v_mul_f32_e32 v3, v36, v179
	v_cvt_pk_fp8_f32 v182, v2, v3
	v_mul_f32_e32 v2, v40, v179
	v_mul_f32_e32 v3, v56, v179
	v_mul_f32_e32 v6, v20, v179
	v_cvt_pk_fp8_f32 v183, v2, v3
	v_cvt_pk_fp8_f32 v180, v4, v6 op_sel:[0,0,1]
	v_mul_f32_e32 v4, v24, v179
	v_mul_f32_e32 v6, v44, v179
	v_cvt_pk_fp8_f32 v181, v4, v6 op_sel:[0,0,1]
	v_mul_f32_e32 v4, v32, v179
	v_mul_f32_e32 v6, v48, v179
	v_cvt_pk_fp8_f32 v182, v4, v6 op_sel:[0,0,1]
	v_mul_f32_e32 v4, v52, v179
	v_mul_f32_e32 v6, v60, v179
	v_cvt_pk_fp8_f32 v183, v4, v6 op_sel:[0,0,1]
	v_mul_f32_e32 v3, v65, v179
	v_mul_f32_e32 v4, v9, v179
	v_cvt_pk_fp8_f32 v2, v3, v4
	v_mul_f32_e32 v5, v5, v179
	v_mul_f32_e32 v6, v21, v179
	v_mul_f32_e32 v4, v13, v179
	v_cvt_pk_fp8_f32 v2, v5, v6 op_sel:[0,0,1]
	v_mul_f32_e32 v5, v29, v179
	v_cvt_pk_fp8_f32 v3, v4, v5
	v_mul_f32_e32 v6, v25, v179
	v_mul_f32_e32 v7, v45, v179
	v_mul_f32_e32 v5, v17, v179
	v_cvt_pk_fp8_f32 v3, v6, v7 op_sel:[0,0,1]
	v_mul_f32_e32 v6, v37, v179
	v_cvt_pk_fp8_f32 v4, v5, v6
	v_mul_f32_e32 v7, v33, v179
	v_mul_f32_e32 v8, v49, v179
	v_mul_f32_e32 v6, v41, v179
	v_cvt_pk_fp8_f32 v4, v7, v8 op_sel:[0,0,1]
	v_mul_f32_e32 v7, v57, v179
	v_cvt_pk_fp8_f32 v5, v6, v7
	v_mul_f32_e32 v8, v53, v179
	v_mul_f32_e32 v9, v61, v179
	s_mov_b32 s2, 0x100000
	v_cvt_pk_fp8_f32 v5, v8, v9 op_sel:[0,0,1]
	ds_write_b128 v158, v[180:183] offset:512
	ds_write_b128 v158, v[2:5] offset:768
	v_add_co_u32_e32 v2, vcc, s2, v132
	s_mov_b32 s2, 0x102000
	s_nop 0
	v_addc_co_u32_e32 v3, vcc, 0, v133, vcc
	global_load_dwordx4 v[62:65], v[2:3], off nt
	v_add_co_u32_e32 v2, vcc, s2, v132
	s_mov_b32 s2, 0x104000
	s_nop 0
	v_addc_co_u32_e32 v3, vcc, 0, v133, vcc
	global_load_dwordx4 v[6:9], v[2:3], off nt
	v_add_co_u32_e32 v2, vcc, s2, v132
	s_mov_b32 s2, 0x106000
	s_nop 0
	v_addc_co_u32_e32 v3, vcc, 0, v133, vcc
	v_add_co_u32_e32 v10, vcc, s2, v132
	s_mov_b32 s2, 0x108000
	s_nop 0
	v_addc_co_u32_e32 v11, vcc, 0, v133, vcc
	global_load_dwordx4 v[2:5], v[2:3], off nt
	s_waitcnt vmcnt(12)
	v_mul_f32_e32 v66, v179, v66
	global_load_dwordx4 v[18:21], v[10:11], off nt
	v_add_co_u32_e32 v10, vcc, s2, v132
	s_mov_b32 s2, 0x10a000
	s_nop 0
	v_addc_co_u32_e32 v11, vcc, 0, v133, vcc
	v_add_co_u32_e32 v14, vcc, s2, v132
	s_mov_b32 s2, 0x10c000
	s_nop 0
	v_addc_co_u32_e32 v15, vcc, 0, v133, vcc
	global_load_dwordx4 v[10:13], v[10:11], off nt
	s_waitcnt vmcnt(13)
; __device__ __forceinline__ unsigned pk4_fp8(float a, float b, float c, float d) { unsigned w = 0u; w = __builtin_amdgcn_cvt_pk_fp8_f32(a, b, w, false); w = __builtin_amdgcn_cvt_pk_fp8_f32(c, d, w, true); return w; }
; #define LAS __attribute__((address_space(3)))
; #define CVT_LOAD(v, c, s_) do { _Pragma("unroll") for (int i_ = 0; i_ < 16; ++i_) v[i_] = *(const f32x4*)((c).src + (size_t)(64 * (s_) + i_) * (c).N); } while (0)
; __device__ __forceinline__ void cvt_pack8(const f32x4 (&v)[16], const CvtItem& c, LAS unsigned char* blk, int s4, int lane) {
;     const float w = c.wscale; const int cb = lane & 15, j = 4 * s4 + (lane >> 4);
; #pragma unroll
;     for (int jn = 0; jn < 4; ++jn) {
;         v4u o; o.x = pg8::pk4_fp8(v[0][jn] * w, v[1][jn] * w, v[2][jn] * w, v[3][jn] * w); o.y = pg8::pk4_fp8(v[4][jn] * w, v[5][jn] * w, v[6][jn] * w, v[7][jn] * w);
;         o.z = pg8::pk4_fp8(v[8][jn] * w, v[9][jn] * w, v[10][jn] * w, v[11][jn] * w); o.w = pg8::pk4_fp8(v[12][jn] * w, v[13][jn] * w, v[14][jn] * w, v[15][jn] * w);
;         *(LAS v4u*)(blk + (4 * cb + jn) * 256 + ((j ^ cb) * 16)) = o; }
; }
; __device__ __forceinline__ void cvt_moe_pipe2(const CvtSrc& A, const CvtSrc& B, LAS float* scr, int gw, int NGW, int lane) {
;     LAS unsigned char* blk = (LAS unsigned char*)scr;
;     f32x4 va[16], vb[16]; CvtItem c, cn;
;     const int it1 = A.n + B.n; int it = gw;
;     if (it < it1) { c = cvt_moe_item2(it, A, B, lane); CVT_LOAD(va, c, 0); }
;     while (it < it1) {
;         const int i1 = it + NGW; const bool more = i1 < it1;
;         CVT_LOAD(vb, c, 1); cvt_pack8(va, c, blk, 0, lane);
;         CVT_LOAD(va, c, 2); cvt_pack8(vb, c, blk, 1, lane);
;         CVT_LOAD(vb, c, 3); cvt_pack8(va, c, blk, 2, lane);
;         if (more) { cn = cvt_moe_item2(i1, A, B, lane); CVT_LOAD(va, cn, 0); }
;         cvt_pack8(vb, c, blk, 3, lane);
	v_mul_f32_e32 v70, v179, v70
	global_load_dwordx4 v[26:29], v[14:15], off nt
	v_add_co_u32_e32 v14, vcc, s2, v132
	s_mov_b32 s2, 0x10e000
	s_nop 0
	v_addc_co_u32_e32 v15, vcc, 0, v133, vcc
	global_load_dwordx4 v[22:25], v[14:15], off nt
	v_add_co_u32_e32 v14, vcc, s2, v132
	s_mov_b32 s2, 0x110000
	s_nop 0
	v_addc_co_u32_e32 v15, vcc, 0, v133, vcc
	global_load_dwordx4 v[42:45], v[14:15], off nt
	v_add_co_u32_e32 v14, vcc, s2, v132
	s_mov_b32 s2, 0x112000
	s_nop 0
	v_addc_co_u32_e32 v15, vcc, 0, v133, vcc
	v_add_co_u32_e32 v30, vcc, s2, v132
	s_mov_b32 s2, 0x114000
	s_nop 0
	v_addc_co_u32_e32 v31, vcc, 0, v133, vcc
	global_load_dwordx4 v[14:17], v[14:15], off nt
	v_cvt_pk_fp8_f32 v180, v66, v70
	global_load_dwordx4 v[34:37], v[30:31], off nt
	v_add_co_u32_e32 v30, vcc, s2, v132
	s_mov_b32 s2, 0x116000
	s_nop 0
	v_addc_co_u32_e32 v31, vcc, 0, v133, vcc
	v_add_co_u32_e32 v38, vcc, s2, v132
	s_waitcnt vmcnt(17)
	v_mul_f32_e32 v66, v179, v78
	v_mul_f32_e32 v70, v179, v90
	v_addc_co_u32_e32 v39, vcc, 0, v133, vcc
	s_mov_b32 s2, 0x118000
	v_cvt_pk_fp8_f32 v181, v66, v70
	s_waitcnt vmcnt(16)
	v_mul_f32_e32 v66, v179, v86
	s_waitcnt vmcnt(15)
	v_mul_f32_e32 v70, v179, v98
	global_load_dwordx4 v[30:33], v[30:31], off nt
	v_cvt_pk_fp8_f32 v182, v66, v70
	global_load_dwordx4 v[46:49], v[38:39], off nt
	v_add_co_u32_e32 v38, vcc, s2, v132
	s_waitcnt vmcnt(16)
	v_mul_f32_e32 v66, v179, v110
	s_waitcnt vmcnt(15)
	v_mul_f32_e32 v70, v179, v118
	v_addc_co_u32_e32 v39, vcc, 0, v133, vcc
	s_mov_b32 s2, 0x11a000
	s_waitcnt vmcnt(14)
	v_mul_f32_e32 v74, v179, v74
	v_mul_f32_e32 v82, v179, v82
	v_cvt_pk_fp8_f32 v183, v66, v70
	v_add_co_u32_e32 v50, vcc, s2, v132
	v_cvt_pk_fp8_f32 v180, v74, v82 op_sel:[0,0,1]
	v_mul_f32_e32 v74, v179, v94
	v_mul_f32_e32 v78, v179, v106
	v_addc_co_u32_e32 v51, vcc, 0, v133, vcc
	s_mov_b32 s2, 0x11c000
	v_cvt_pk_fp8_f32 v181, v74, v78 op_sel:[0,0,1]
	v_mul_f32_e32 v74, v179, v102
	v_mul_f32_e32 v78, v179, v114
	global_load_dwordx4 v[38:41], v[38:39], off nt
	v_cvt_pk_fp8_f32 v182, v74, v78 op_sel:[0,0,1]
	global_load_dwordx4 v[54:57], v[50:51], off nt
	v_add_co_u32_e32 v50, vcc, s2, v132
	s_waitcnt vmcnt(15)
	v_mul_f32_e32 v74, v179, v122
	s_waitcnt vmcnt(14)
	v_mul_f32_e32 v78, v179, v126
	v_addc_co_u32_e32 v51, vcc, 0, v133, vcc
	s_mov_b32 s2, 0x11e000
	v_cvt_pk_fp8_f32 v183, v74, v78 op_sel:[0,0,1]
	v_add_co_u32_e32 v58, vcc, s2, v132
	global_load_dwordx4 v[50:53], v[50:51], off nt
	s_nop 0
	v_addc_co_u32_e32 v59, vcc, 0, v133, vcc
	global_load_dwordx4 v[58:61], v[58:59], off nt
	ds_write_b128 v159, v[180:183]
	v_mul_f32_e32 v66, v179, v67
	v_mul_f32_e32 v67, v179, v71
	v_cvt_pk_fp8_f32 v180, v66, v67
	v_mul_f32_e32 v66, v179, v79
	v_mul_f32_e32 v67, v179, v91
	v_cvt_pk_fp8_f32 v181, v66, v67
	v_mul_f32_e32 v66, v179, v87
	v_mul_f32_e32 v67, v179, v99
	v_cvt_pk_fp8_f32 v182, v66, v67
	v_mul_f32_e32 v66, v179, v111
	v_mul_f32_e32 v67, v179, v119
	v_mul_f32_e32 v70, v179, v75
	v_mul_f32_e32 v71, v179, v83
	v_cvt_pk_fp8_f32 v183, v66, v67
	v_cvt_pk_fp8_f32 v180, v70, v71 op_sel:[0,0,1]
	v_mul_f32_e32 v70, v179, v95
	v_mul_f32_e32 v71, v179, v107
	v_cvt_pk_fp8_f32 v181, v70, v71 op_sel:[0,0,1]
	v_mul_f32_e32 v70, v179, v103
	v_mul_f32_e32 v71, v179, v115
	v_cvt_pk_fp8_f32 v182, v70, v71 op_sel:[0,0,1]
	v_mul_f32_e32 v70, v179, v123
	v_mul_f32_e32 v71, v179, v127
	v_cvt_pk_fp8_f32 v183, v70, v71 op_sel:[0,0,1]
	v_mul_f32_e32 v66, v179, v68
	v_mul_f32_e32 v67, v179, v72
	v_mul_f32_e32 v68, v179, v76
	ds_write_b128 v159, v[180:183] offset:256
	v_cvt_pk_fp8_f32 v180, v66, v67
	v_mul_f32_e32 v66, v179, v80
	v_mul_f32_e32 v67, v179, v92
	v_cvt_pk_fp8_f32 v181, v66, v67
	v_mul_f32_e32 v66, v179, v88
	v_mul_f32_e32 v67, v179, v100
	v_cvt_pk_fp8_f32 v182, v66, v67
	v_mul_f32_e32 v66, v179, v112
	v_mul_f32_e32 v67, v179, v120
	v_mul_f32_e32 v70, v179, v84
	v_cvt_pk_fp8_f32 v183, v66, v67
	v_cvt_pk_fp8_f32 v180, v68, v70 op_sel:[0,0,1]
	v_mul_f32_e32 v68, v179, v96
	v_mul_f32_e32 v70, v179, v108
	v_cvt_pk_fp8_f32 v181, v68, v70 op_sel:[0,0,1]
	v_mul_f32_e32 v68, v179, v104
	v_mul_f32_e32 v70, v179, v116
	v_cvt_pk_fp8_f32 v182, v68, v70 op_sel:[0,0,1]
	v_mul_f32_e32 v68, v179, v124
	v_mul_f32_e32 v70, v179, v128
	v_cvt_pk_fp8_f32 v183, v68, v70 op_sel:[0,0,1]
	v_mul_f32_e32 v67, v179, v69
	v_mul_f32_e32 v68, v179, v73
	v_cvt_pk_fp8_f32 v66, v67, v68
	v_mul_f32_e32 v69, v179, v77
	v_mul_f32_e32 v70, v179, v85
	v_mul_f32_e32 v68, v179, v81
	v_cvt_pk_fp8_f32 v66, v69, v70 op_sel:[0,0,1]
	v_mul_f32_e32 v69, v179, v93
	v_cvt_pk_fp8_f32 v67, v68, v69
	v_mul_f32_e32 v70, v179, v97
	v_mul_f32_e32 v71, v179, v109
	v_mul_f32_e32 v69, v179, v89
	v_cvt_pk_fp8_f32 v67, v70, v71 op_sel:[0,0,1]
	v_mul_f32_e32 v70, v179, v101
	v_cvt_pk_fp8_f32 v68, v69, v70
	v_mul_f32_e32 v71, v179, v105
	v_mul_f32_e32 v72, v179, v117
	v_mul_f32_e32 v70, v179, v113
	v_cvt_pk_fp8_f32 v68, v71, v72 op_sel:[0,0,1]
	v_mul_f32_e32 v71, v179, v121
	v_cvt_pk_fp8_f32 v69, v70, v71
	v_mul_f32_e32 v72, v179, v125
	v_mul_f32_e32 v73, v179, v129
	s_mov_b32 s2, 0x180000
	v_cvt_pk_fp8_f32 v69, v72, v73 op_sel:[0,0,1]
	ds_write_b128 v159, v[180:183] offset:512
	s_waitcnt vmcnt(15)
	v_mul_f32_e32 v130, v179, v62
	s_waitcnt vmcnt(14)
; __device__ __forceinline__ unsigned pk4_fp8(float a, float b, float c, float d) { unsigned w = 0u; w = __builtin_amdgcn_cvt_pk_fp8_f32(a, b, w, false); w = __builtin_amdgcn_cvt_pk_fp8_f32(c, d, w, true); return w; }
; #define LAS __attribute__((address_space(3)))
; #define CVT_LOAD(v, c, s_) do { _Pragma("unroll") for (int i_ = 0; i_ < 16; ++i_) v[i_] = *(const f32x4*)((c).src + (size_t)(64 * (s_) + i_) * (c).N); } while (0)
; __device__ __forceinline__ void cvt_pack8(const f32x4 (&v)[16], const CvtItem& c, LAS unsigned char* blk, int s4, int lane) {
;     const float w = c.wscale; const int cb = lane & 15, j = 4 * s4 + (lane >> 4);
; #pragma unroll
;     for (int jn = 0; jn < 4; ++jn) {
;         v4u o; o.x = pg8::pk4_fp8(v[0][jn] * w, v[1][jn] * w, v[2][jn] * w, v[3][jn] * w); o.y = pg8::pk4_fp8(v[4][jn] * w, v[5][jn] * w, v[6][jn] * w, v[7][jn] * w);
;         o.z = pg8::pk4_fp8(v[8][jn] * w, v[9][jn] * w, v[10][jn] * w, v[11][jn] * w); o.w = pg8::pk4_fp8(v[12][jn] * w, v[13][jn] * w, v[14][jn] * w, v[15][jn] * w);
;         *(LAS v4u*)(blk + (4 * cb + jn) * 256 + ((j ^ cb) * 16)) = o; }
; }
; __device__ __forceinline__ void cvt_moe_pipe2(const CvtSrc& A, const CvtSrc& B, LAS float* scr, int gw, int NGW, int lane) {
;     LAS unsigned char* blk = (LAS unsigned char*)scr;
;     f32x4 va[16], vb[16]; CvtItem c, cn;
;     const int it1 = A.n + B.n; int it = gw;
;     if (it < it1) { c = cvt_moe_item2(it, A, B, lane); CVT_LOAD(va, c, 0); }
;     while (it < it1) {
;         const int i1 = it + NGW; const bool more = i1 < it1;
;         CVT_LOAD(vb, c, 1); cvt_pack8(va, c, blk, 0, lane);
;         CVT_LOAD(va, c, 2); cvt_pack8(vb, c, blk, 1, lane);
;         CVT_LOAD(vb, c, 3); cvt_pack8(va, c, blk, 2, lane);
;         if (more) { cn = cvt_moe_item2(i1, A, B, lane); CVT_LOAD(va, cn, 0); }
;         cvt_pack8(vb, c, blk, 3, lane);
;         cvt_flush8(c, blk, lane);
;         if (more) c = cn;
	v_mul_f32_e32 v137, v179, v6
	ds_write_b128 v159, v[66:69] offset:768
	v_add_co_u32_e32 v66, vcc, s2, v132
	s_mov_b32 s2, 0x182000
	s_nop 0
	v_addc_co_u32_e32 v67, vcc, 0, v133, vcc
	v_add_co_u32_e32 v70, vcc, s2, v132
	s_mov_b32 s2, 0x184000
	s_nop 0
	v_addc_co_u32_e32 v71, vcc, 0, v133, vcc
	v_add_co_u32_e32 v74, vcc, s2, v132
	s_mov_b32 s2, 0x186000
	s_nop 0
	v_addc_co_u32_e32 v75, vcc, 0, v133, vcc
	v_add_co_u32_e32 v78, vcc, s2, v132
	s_mov_b32 s2, 0x188000
	s_nop 0
	v_addc_co_u32_e32 v79, vcc, 0, v133, vcc
	global_load_dwordx4 v[74:77], v[74:75], off nt
	global_load_dwordx4 v[82:85], v[78:79], off nt
	v_add_co_u32_e32 v78, vcc, s2, v132
	s_mov_b32 s2, 0x18a000
	s_nop 0
	v_addc_co_u32_e32 v79, vcc, 0, v133, vcc
	v_add_co_u32_e32 v86, vcc, s2, v132
	s_mov_b32 s2, 0x18c000
	s_nop 0
	v_addc_co_u32_e32 v87, vcc, 0, v133, vcc
	global_load_dwordx4 v[78:81], v[78:79], off nt
	v_cvt_pk_fp8_f32 v180, v130, v137
	global_load_dwordx4 v[90:93], v[86:87], off nt
	v_add_co_u32_e32 v86, vcc, s2, v132
	s_mov_b32 s2, 0x18e000
	s_nop 0
	v_addc_co_u32_e32 v87, vcc, 0, v133, vcc
	global_load_dwordx4 v[94:97], v[86:87], off nt
	v_add_co_u32_e32 v86, vcc, s2, v132
	s_mov_b32 s2, 0x190000
	s_nop 0
	v_addc_co_u32_e32 v87, vcc, 0, v133, vcc
	global_load_dwordx4 v[106:109], v[86:87], off nt
	v_add_co_u32_e32 v86, vcc, s2, v132
	s_mov_b32 s2, 0x192000
	s_nop 0
	v_addc_co_u32_e32 v87, vcc, 0, v133, vcc
	v_add_co_u32_e32 v98, vcc, s2, v132
	s_mov_b32 s2, 0x194000
	s_nop 0
	v_addc_co_u32_e32 v99, vcc, 0, v133, vcc
	v_add_co_u32_e32 v102, vcc, s2, v132
	s_waitcnt vmcnt(19)
	v_mul_f32_e32 v181, v179, v2
	s_waitcnt vmcnt(18)
	v_mul_f32_e32 v182, v179, v18
	v_addc_co_u32_e32 v103, vcc, 0, v133, vcc
	s_mov_b32 s2, 0x196000
	v_cvt_pk_fp8_f32 v180, v181, v182 op_sel:[0,0,1]
	s_waitcnt vmcnt(17)
	v_mul_f32_e32 v130, v179, v10
	s_waitcnt vmcnt(16)
	v_mul_f32_e32 v137, v179, v26
	v_add_co_u32_e32 v110, vcc, s2, v132
	v_cvt_pk_fp8_f32 v181, v130, v137
	s_nop 0
	v_addc_co_u32_e32 v111, vcc, 0, v133, vcc
	s_mov_b32 s2, 0x198000
	global_load_dwordx4 v[102:105], v[102:103], off nt
	s_waitcnt vmcnt(16)
	v_mul_f32_e32 v182, v179, v22
	global_load_dwordx4 v[114:117], v[110:111], off nt
	v_add_co_u32_e32 v110, vcc, s2, v132
	s_mov_b32 s2, 0x19a000
	s_nop 0
	v_addc_co_u32_e32 v111, vcc, 0, v133, vcc
	s_waitcnt vmcnt(16)
	v_mul_f32_e32 v183, v179, v42
	v_add_co_u32_e32 v118, vcc, s2, v132
	v_cvt_pk_fp8_f32 v181, v182, v183 op_sel:[0,0,1]
	s_waitcnt vmcnt(15)
	v_mul_f32_e32 v130, v179, v14
	s_waitcnt vmcnt(14)
	v_mul_f32_e32 v137, v179, v34
	v_addc_co_u32_e32 v119, vcc, 0, v133, vcc
	s_mov_b32 s2, 0x19c000
	v_cvt_pk_fp8_f32 v182, v130, v137
	v_add_co_u32_e32 v122, vcc, s2, v132
	s_mov_b32 s2, 0x19e000
	s_nop 0
	v_addc_co_u32_e32 v123, vcc, 0, v133, vcc
	v_add_co_u32_e32 v126, vcc, s2, v132
	s_waitcnt vmcnt(13)
	v_mul_f32_e32 v183, v179, v30
	s_waitcnt vmcnt(12)
	v_mul_f32_e32 v184, v179, v46
	v_addc_co_u32_e32 v127, vcc, 0, v133, vcc
	v_cvt_pk_fp8_f32 v182, v183, v184 op_sel:[0,0,1]
	s_waitcnt vmcnt(11)
	v_mul_f32_e32 v130, v179, v38
	s_waitcnt vmcnt(10)
	v_mul_f32_e32 v137, v179, v54
	global_load_dwordx4 v[66:69], v[66:67], off nt
	v_cvt_pk_fp8_f32 v183, v130, v137
	global_load_dwordx4 v[70:73], v[70:71], off nt
	s_waitcnt vmcnt(11)
	v_mul_f32_e32 v184, v179, v50
	global_load_dwordx4 v[86:89], v[86:87], off nt
	s_waitcnt vmcnt(11)
	v_mul_f32_e32 v185, v179, v58
	global_load_dwordx4 v[98:101], v[98:99], off nt
	v_cvt_pk_fp8_f32 v183, v184, v185 op_sel:[0,0,1]
	global_load_dwordx4 v[110:113], v[110:111], off nt
	v_mul_f32_e32 v130, v179, v63
	global_load_dwordx4 v[118:121], v[118:119], off nt
	ds_write_b128 v160, v[180:183]
	global_load_dwordx4 v[122:125], v[122:123], off nt
	v_mul_f32_e32 v137, v179, v7
	global_load_dwordx4 v[126:129], v[126:127], off nt
	v_cvt_pk_fp8_f32 v180, v130, v137
	v_mul_f32_e32 v181, v179, v3
	v_mul_f32_e32 v182, v179, v19
	v_mul_f32_e32 v130, v179, v11
	v_cvt_pk_fp8_f32 v180, v181, v182 op_sel:[0,0,1]
	v_mul_f32_e32 v137, v179, v27
	v_cvt_pk_fp8_f32 v181, v130, v137
	v_mul_f32_e32 v182, v179, v23
	v_mul_f32_e32 v183, v179, v43
	v_mul_f32_e32 v130, v179, v15
	v_cvt_pk_fp8_f32 v181, v182, v183 op_sel:[0,0,1]
	v_mul_f32_e32 v137, v179, v35
	v_cvt_pk_fp8_f32 v182, v130, v137
	v_mul_f32_e32 v183, v179, v31
	v_mul_f32_e32 v184, v179, v47
	v_mul_f32_e32 v130, v179, v39
	v_cvt_pk_fp8_f32 v182, v183, v184 op_sel:[0,0,1]
	v_mul_f32_e32 v137, v179, v55
	v_cvt_pk_fp8_f32 v183, v130, v137
	v_mul_f32_e32 v184, v179, v51
	v_mul_f32_e32 v185, v179, v59
	v_mul_f32_e32 v130, v179, v64
	v_cvt_pk_fp8_f32 v183, v184, v185 op_sel:[0,0,1]
	v_mul_f32_e32 v137, v179, v8
	v_mul_f32_e32 v184, v179, v48
	v_mul_f32_e32 v185, v179, v60
	ds_write_b128 v160, v[180:183] offset:256
	v_cvt_pk_fp8_f32 v180, v130, v137
	v_mul_f32_e32 v181, v179, v4
	v_mul_f32_e32 v182, v179, v20
	v_mul_f32_e32 v130, v179, v12
	v_cvt_pk_fp8_f32 v180, v181, v182 op_sel:[0,0,1]
	v_mul_f32_e32 v137, v179, v28
	v_cvt_pk_fp8_f32 v181, v130, v137
	v_mul_f32_e32 v182, v179, v24
	v_mul_f32_e32 v183, v179, v44
	v_mul_f32_e32 v130, v179, v16
	v_cvt_pk_fp8_f32 v181, v182, v183 op_sel:[0,0,1]
	v_mul_f32_e32 v137, v179, v36
	v_cvt_pk_fp8_f32 v182, v130, v137
	v_mul_f32_e32 v183, v179, v32
	v_mul_f32_e32 v130, v179, v40
	v_mul_f32_e32 v137, v179, v56
	v_cvt_pk_fp8_f32 v182, v183, v184 op_sel:[0,0,1]
	v_cvt_pk_fp8_f32 v183, v130, v137
	v_mul_f32_e32 v184, v179, v52
	v_mul_f32_e32 v130, v179, v65
	v_mul_f32_e32 v137, v179, v9
	v_cvt_pk_fp8_f32 v183, v184, v185 op_sel:[0,0,1]
	v_mul_f32_e32 v184, v179, v49
	v_mul_f32_e32 v185, v179, v61
	s_cmpk_gt_i32 s29, 0x50f
	ds_write_b128 v160, v[180:183] offset:512
	v_cvt_pk_fp8_f32 v180, v130, v137
	v_mul_f32_e32 v181, v179, v5
	v_mul_f32_e32 v182, v179, v21
	v_mul_f32_e32 v130, v179, v13
	v_cvt_pk_fp8_f32 v180, v181, v182 op_sel:[0,0,1]
	v_mul_f32_e32 v137, v179, v29
	v_cvt_pk_fp8_f32 v181, v130, v137
	v_mul_f32_e32 v182, v179, v25
	v_mul_f32_e32 v183, v179, v45
	v_mul_f32_e32 v130, v179, v17
	v_cvt_pk_fp8_f32 v181, v182, v183 op_sel:[0,0,1]
	v_mul_f32_e32 v137, v179, v37
	v_cvt_pk_fp8_f32 v182, v130, v137
	v_mul_f32_e32 v183, v179, v33
	v_mul_f32_e32 v130, v179, v41
	v_mul_f32_e32 v137, v179, v57
	v_cvt_pk_fp8_f32 v182, v183, v184 op_sel:[0,0,1]
	v_cvt_pk_fp8_f32 v183, v130, v137
	v_mul_f32_e32 v184, v179, v53
	s_cselect_b64 s[2:3], -1, 0
	s_and_b64 vcc, exec, s[2:3]
	v_cvt_pk_fp8_f32 v183, v184, v185 op_sel:[0,0,1]
	ds_write_b128 v160, v[180:183] offset:768
	s_cbranch_vccnz .LBB0_717
; __device__ __forceinline__ CvtItem cvt_moe_item(int it, const float* wg, const float* wu, const float* wd, unsigned char* WGU, unsigned char* WDN, int lane) {
;     const int which = it >> 11, r = it & 2047, e = r >> 7, q = r & 127; CvtItem c; c.which = which;
;     if (which < 2) { const int nb = q & 31, k0 = (q >> 5) * 256; c.nb = nb;
;         c.N = DFF; c.K = DM; c.wscale = which ? 64.f / LOG2E : 64.f * LOG2E; c.src = (which ? wu : wg) + (size_t)e * DM * DFF + (size_t)(k0 + 16 * (lane >> 4)) * DFF + nb * 64 + 4 * (lane & 15);
;         c.dst = WGU + (size_t)e * 4096 * DM + k0; }
;     else { const int nb = q & 15, k0 = (q >> 4) * 256; c.nb = nb;
;         c.N = DM; c.K = DFF; c.wscale = 64.f; c.src = wd + (size_t)e * DFF * DM + (size_t)(k0 + 16 * (lane >> 4)) * DM + nb * 64 + 4 * (lane & 15);
;         c.dst = WDN + (size_t)e * DM * DFF + k0; }
;     return c;
; }
	s_ashr_i32 s27, s29, 11
	s_and_b32 s28, s29, 31
	s_and_b32 s33, s25, 0x300
	s_cmpk_lt_u32 s29, 0x800
	s_cselect_b64 vcc, -1, 0
	v_readlane_b32 s36, v254, 30
	s_and_b64 s[8:9], vcc, exec
	v_readlane_b32 s48, v254, 42
	v_readlane_b32 s49, v254, 43
	v_readlane_b32 s50, v254, 44
	v_readlane_b32 s51, v254, 45
	s_cselect_b32 s4, s49, s51
	s_cselect_b32 s8, s48, s50
	s_bfe_u32 s34, s29, 0x40007
	s_lshl_b32 s9, s34, 23
	s_add_u32 s8, s8, s9
	v_or_b32_e32 v2, s33, v141
	s_addc_u32 s9, s4, 0
	v_lshlrev_b32_e32 v130, 13, v2
	v_lshl_add_u64 v[2:3], s[8:9], 0, v[130:131]
	s_lshl_b32 s4, s28, 8
	v_lshl_add_u64 v[2:3], v[2:3], 0, s[4:5]
	v_mov_b32_e32 v137, v131
	v_lshl_add_u64 v[132:133], v[2:3], 0, v[136:137]
	v_cndmask_b32_e32 v178, v139, v140, vcc
	v_add_co_u32_e32 v2, vcc, s24, v132
	s_lshl_b32 s4, s34, 22
	s_nop 0
	v_addc_co_u32_e32 v3, vcc, 0, v133, vcc
	v_add_co_u32_e32 v4, vcc, s23, v132
	v_readlane_b32 s8, v255, 1
	s_nop 0
	v_addc_co_u32_e32 v5, vcc, 0, v133, vcc
	v_add_co_u32_e32 v10, vcc, s22, v132
	global_load_dwordx4 v[6:9], v[2:3], off nt
	s_nop 0
	global_load_dwordx4 v[2:5], v[4:5], off nt
	v_addc_co_u32_e32 v11, vcc, 0, v133, vcc
	v_add_co_u32_e32 v12, vcc, s21, v132
	v_readlane_b32 s9, v255, 2
	s_nop 0
	v_addc_co_u32_e32 v13, vcc, 0, v133, vcc
	v_add_co_u32_e32 v14, vcc, s20, v132
	global_load_dwordx4 v[18:21], v[10:11], off nt
	s_nop 0
	global_load_dwordx4 v[10:13], v[12:13], off nt
	v_addc_co_u32_e32 v15, vcc, 0, v133, vcc
	v_add_co_u32_e32 v16, vcc, s19, v132
	s_add_u32 s4, s8, s4
	s_nop 0
	v_addc_co_u32_e32 v17, vcc, 0, v133, vcc
	global_load_dwordx4 v[26:29], v[14:15], off nt
	global_load_dwordx4 v[22:25], v[16:17], off nt
	v_add_co_u32_e32 v14, vcc, s18, v132
	s_addc_u32 s9, s9, 0
	s_nop 0
	v_addc_co_u32_e32 v15, vcc, 0, v133, vcc
	v_add_co_u32_e32 v16, vcc, s17, v132
	s_add_u32 s8, s4, s33
	s_nop 0
	v_addc_co_u32_e32 v17, vcc, 0, v133, vcc
	v_add_co_u32_e32 v30, vcc, s16, v132
	global_load_dwordx4 v[42:45], v[14:15], off nt
	s_nop 0
	global_load_dwordx4 v[14:17], v[16:17], off nt
	v_addc_co_u32_e32 v31, vcc, 0, v133, vcc
	v_add_co_u32_e32 v32, vcc, s15, v132
	s_addc_u32 s9, s9, 0
	s_nop 0
	v_addc_co_u32_e32 v33, vcc, 0, v133, vcc
	v_add_co_u32_e32 v38, vcc, s14, v132
	global_load_dwordx4 v[34:37], v[30:31], off nt
	s_nop 0
	global_load_dwordx4 v[30:33], v[32:33], off nt
	v_addc_co_u32_e32 v39, vcc, 0, v133, vcc
	v_add_co_u32_e32 v40, vcc, s13, v132
	v_readlane_b32 s37, v254, 31
	s_nop 0
	v_addc_co_u32_e32 v41, vcc, 0, v133, vcc
	v_add_co_u32_e32 v50, vcc, s12, v132
	global_load_dwordx4 v[46:49], v[38:39], off nt
	s_nop 0
	global_load_dwordx4 v[38:41], v[40:41], off nt
	v_addc_co_u32_e32 v51, vcc, 0, v133, vcc
	v_add_co_u32_e32 v52, vcc, s11, v132
	v_readlane_b32 s38, v254, 32
	s_nop 0
	v_addc_co_u32_e32 v53, vcc, 0, v133, vcc
	v_add_co_u32_e32 v58, vcc, s10, v132
	global_load_dwordx4 v[54:57], v[50:51], off nt
	s_nop 0
	global_load_dwordx4 v[50:53], v[52:53], off nt
	v_addc_co_u32_e32 v59, vcc, 0, v133, vcc
	global_load_dwordx4 v[62:65], v[132:133], off nt
	s_nop 0
	global_load_dwordx4 v[58:61], v[58:59], off nt
	v_readlane_b32 s39, v254, 33
	v_readlane_b32 s40, v254, 34
	v_readlane_b32 s41, v254, 35
	v_readlane_b32 s42, v254, 36
	v_readlane_b32 s43, v254, 37
	v_readlane_b32 s44, v254, 38
	v_readlane_b32 s45, v254, 39
	v_readlane_b32 s46, v254, 40
	v_readlane_b32 s47, v254, 41
	s_branch .LBB0_717

; __device__ __forceinline__ unsigned pk4_fp8(float a, float b, float c, float d) { unsigned w = 0u; w = __builtin_amdgcn_cvt_pk_fp8_f32(a, b, w, false); w = __builtin_amdgcn_cvt_pk_fp8_f32(c, d, w, true); return w; }
; #define LAS __attribute__((address_space(3)))
; #define LDS_WAIT() asm volatile("s_waitcnt lgkmcnt(0)" ::: "memory")
; __device__ __forceinline__ void cvt_pack8(const f32x4 (&v)[16], const CvtItem& c, LAS unsigned char* blk, int s4, int lane) {
;     const float w = c.wscale; const int cb = lane & 15, j = 4 * s4 + (lane >> 4);
; #pragma unroll
;     for (int jn = 0; jn < 4; ++jn) {
;         v4u o; o.x = pg8::pk4_fp8(v[0][jn] * w, v[1][jn] * w, v[2][jn] * w, v[3][jn] * w); o.y = pg8::pk4_fp8(v[4][jn] * w, v[5][jn] * w, v[6][jn] * w, v[7][jn] * w);
;         o.z = pg8::pk4_fp8(v[8][jn] * w, v[9][jn] * w, v[10][jn] * w, v[11][jn] * w); o.w = pg8::pk4_fp8(v[12][jn] * w, v[13][jn] * w, v[14][jn] * w, v[15][jn] * w);
;         *(LAS v4u*)(blk + (4 * cb + jn) * 256 + ((j ^ cb) * 16)) = o; }
; }
; __device__ __forceinline__ void cvt_flush8(const CvtItem& c, const LAS unsigned char* blk, int lane) {
;     LDS_WAIT();
; #pragma unroll
;     for (int t = 0; t < 16; ++t) { const int idx = 64 * t + lane, n = idx >> 4, pc = idx & 15, nn = c.nb * 64 + n;
;         const size_t row = (c.which < 2) ? (size_t)((nn >> 7) * 256 + (nn & 127) + c.which * 128) : (size_t)nn;
;         *(v4u*)(c.dst + row * c.K + 16 * pc) = *(const LAS v4u*)(blk + n * 256 + ((pc ^ ((n >> 2) & 15)) * 16)); }
;     LDS_WAIT();
; }
.LBB0_724:
	s_waitcnt vmcnt(7)
	v_mul_f32_e32 v66, v177, v66
	s_waitcnt vmcnt(6)
	v_mul_f32_e32 v70, v177, v70
	v_cvt_pk_fp8_f32 v178, v66, v70
	v_mul_f32_e32 v66, v177, v78
	v_mul_f32_e32 v70, v177, v90
	v_cvt_pk_fp8_f32 v179, v66, v70
	s_waitcnt vmcnt(5)
	v_mul_f32_e32 v66, v177, v86
	s_waitcnt vmcnt(4)
	v_mul_f32_e32 v70, v177, v98
	v_cvt_pk_fp8_f32 v180, v66, v70
	s_waitcnt vmcnt(3)
	v_mul_f32_e32 v66, v177, v110
	s_waitcnt vmcnt(2)
	v_mul_f32_e32 v70, v177, v118
	v_mul_f32_e32 v74, v177, v74
	v_mul_f32_e32 v82, v177, v82
	v_cvt_pk_fp8_f32 v181, v66, v70
	v_cvt_pk_fp8_f32 v178, v74, v82 op_sel:[0,0,1]
	v_mul_f32_e32 v74, v177, v94
	v_mul_f32_e32 v78, v177, v106
	v_cvt_pk_fp8_f32 v179, v74, v78 op_sel:[0,0,1]
	v_mul_f32_e32 v74, v177, v102
	v_mul_f32_e32 v78, v177, v114
	v_cvt_pk_fp8_f32 v180, v74, v78 op_sel:[0,0,1]
	s_waitcnt vmcnt(1)
	v_mul_f32_e32 v74, v177, v122
	s_waitcnt vmcnt(0)
	v_mul_f32_e32 v78, v177, v126
	v_cvt_pk_fp8_f32 v181, v74, v78 op_sel:[0,0,1]
	v_mul_f32_e32 v66, v177, v67
	v_mul_f32_e32 v67, v177, v71
	v_mul_f32_e32 v70, v177, v75
	ds_write_b128 v159, v[178:181]
	v_cvt_pk_fp8_f32 v178, v66, v67
	v_mul_f32_e32 v66, v177, v79
	v_mul_f32_e32 v67, v177, v91
	v_cvt_pk_fp8_f32 v179, v66, v67
	v_mul_f32_e32 v66, v177, v87
	v_mul_f32_e32 v67, v177, v99
	v_cvt_pk_fp8_f32 v180, v66, v67
	v_mul_f32_e32 v66, v177, v111
	v_mul_f32_e32 v67, v177, v119
	v_mul_f32_e32 v71, v177, v83
	v_cvt_pk_fp8_f32 v181, v66, v67
	v_cvt_pk_fp8_f32 v178, v70, v71 op_sel:[0,0,1]
	v_mul_f32_e32 v70, v177, v95
	v_mul_f32_e32 v71, v177, v107
	v_cvt_pk_fp8_f32 v179, v70, v71 op_sel:[0,0,1]
	v_mul_f32_e32 v70, v177, v103
	v_mul_f32_e32 v71, v177, v115
	v_cvt_pk_fp8_f32 v180, v70, v71 op_sel:[0,0,1]
	v_mul_f32_e32 v70, v177, v123
	v_mul_f32_e32 v71, v177, v127
	v_cvt_pk_fp8_f32 v181, v70, v71 op_sel:[0,0,1]
	v_mul_f32_e32 v66, v177, v68
	v_mul_f32_e32 v67, v177, v72
	v_mul_f32_e32 v68, v177, v76
	ds_write_b128 v159, v[178:181] offset:256
	v_cvt_pk_fp8_f32 v178, v66, v67
	v_mul_f32_e32 v66, v177, v80
	v_mul_f32_e32 v67, v177, v92
	v_cvt_pk_fp8_f32 v179, v66, v67
	v_mul_f32_e32 v66, v177, v88
	v_mul_f32_e32 v67, v177, v100
	v_cvt_pk_fp8_f32 v180, v66, v67
	v_mul_f32_e32 v66, v177, v112
	v_mul_f32_e32 v67, v177, v120
	v_mul_f32_e32 v70, v177, v84
	v_cvt_pk_fp8_f32 v181, v66, v67
	v_cvt_pk_fp8_f32 v178, v68, v70 op_sel:[0,0,1]
	v_mul_f32_e32 v68, v177, v96
	v_mul_f32_e32 v70, v177, v108
	v_cvt_pk_fp8_f32 v179, v68, v70 op_sel:[0,0,1]
	v_mul_f32_e32 v68, v177, v104
	v_mul_f32_e32 v70, v177, v116
	v_cvt_pk_fp8_f32 v180, v68, v70 op_sel:[0,0,1]
	v_mul_f32_e32 v68, v177, v124
	v_mul_f32_e32 v70, v177, v128
	v_cvt_pk_fp8_f32 v181, v68, v70 op_sel:[0,0,1]
	v_mul_f32_e32 v67, v177, v69
	v_mul_f32_e32 v68, v177, v73
	v_cvt_pk_fp8_f32 v66, v67, v68
	v_mul_f32_e32 v69, v177, v77
	v_mul_f32_e32 v70, v177, v85
	v_mul_f32_e32 v68, v177, v81
	v_cvt_pk_fp8_f32 v66, v69, v70 op_sel:[0,0,1]
	v_mul_f32_e32 v69, v177, v93
	v_cvt_pk_fp8_f32 v67, v68, v69
	v_mul_f32_e32 v70, v177, v97
	v_mul_f32_e32 v71, v177, v109
	v_mul_f32_e32 v69, v177, v89
	v_cvt_pk_fp8_f32 v67, v70, v71 op_sel:[0,0,1]
	v_mul_f32_e32 v70, v177, v101
	v_cvt_pk_fp8_f32 v68, v69, v70
	v_mul_f32_e32 v71, v177, v105
	v_mul_f32_e32 v72, v177, v117
	v_mul_f32_e32 v70, v177, v113
	v_cvt_pk_fp8_f32 v68, v71, v72 op_sel:[0,0,1]
	v_mul_f32_e32 v71, v177, v121
	v_cvt_pk_fp8_f32 v69, v70, v71
	v_mul_f32_e32 v72, v177, v125
	v_mul_f32_e32 v73, v177, v129
	s_lshl_b32 s4, s30, 6
	v_cvt_pk_fp8_f32 v69, v72, v73 op_sel:[0,0,1]
	s_and_b32 s30, s30, 0x1fffffe
	ds_write_b128 v159, v[178:181] offset:512
	s_and_b32 s4, s4, 64
	ds_write_b128 v159, v[66:69] offset:768
	s_add_i32 s30, s30, s29
	s_waitcnt lgkmcnt(0)
	v_or_b32_e32 v66, s4, v138
	s_lshl_b32 s29, s30, 7
	v_or_b32_e32 v70, s29, v66
	ds_read_b128 v[66:69], v160
	v_ashrrev_i32_e32 v71, 31, v70
	v_lshlrev_b64 v[70:71], 10, v[70:71]
	v_lshl_add_u64 v[70:71], s[6:7], 0, v[70:71]
	v_lshl_add_u64 v[70:71], v[70:71], 0, v[134:135]
	s_waitcnt lgkmcnt(0)
	global_store_dwordx4 v[70:71], v[66:69], off nt
	s_add_i32 s2, s2, s3
	s_add_i32 s25, s25, s26
	v_or_b32_e32 v66, s4, v1
	v_or_b32_e32 v70, s29, v66
	ds_read_b128 v[66:69], v161
	v_ashrrev_i32_e32 v71, 31, v70
	v_lshlrev_b64 v[70:71], 10, v[70:71]
	v_lshl_add_u64 v[70:71], s[6:7], 0, v[70:71]
	v_lshl_add_u64 v[70:71], v[70:71], 0, v[134:135]
	s_waitcnt lgkmcnt(0)
	global_store_dwordx4 v[70:71], v[66:69], off nt
	s_cmpk_lt_i32 s2, 0x510
	s_mov_b32 s30, s28
	v_or_b32_e32 v66, s4, v142
	v_or_b32_e32 v70, s29, v66
	ds_read_b128 v[66:69], v162
	v_ashrrev_i32_e32 v71, 31, v70
	v_lshlrev_b64 v[70:71], 10, v[70:71]
	v_lshl_add_u64 v[70:71], s[6:7], 0, v[70:71]
	v_lshl_add_u64 v[70:71], v[70:71], 0, v[134:135]
	s_waitcnt lgkmcnt(0)
	global_store_dwordx4 v[70:71], v[66:69], off nt
	v_mov_b32_e32 v177, v176
	s_nop 0
	v_or_b32_e32 v66, s4, v143
	v_or_b32_e32 v70, s29, v66
	ds_read_b128 v[66:69], v163
	v_ashrrev_i32_e32 v71, 31, v70
	v_lshlrev_b64 v[70:71], 10, v[70:71]
	v_lshl_add_u64 v[70:71], s[6:7], 0, v[70:71]
	v_lshl_add_u64 v[70:71], v[70:71], 0, v[134:135]
	s_waitcnt lgkmcnt(0)
	global_store_dwordx4 v[70:71], v[66:69], off nt
	s_nop 1
	v_or_b32_e32 v66, s4, v144
	v_or_b32_e32 v70, s29, v66
	ds_read_b128 v[66:69], v164
	v_ashrrev_i32_e32 v71, 31, v70
	v_lshlrev_b64 v[70:71], 10, v[70:71]
	v_lshl_add_u64 v[70:71], s[6:7], 0, v[70:71]
	v_lshl_add_u64 v[70:71], v[70:71], 0, v[134:135]
	s_waitcnt lgkmcnt(0)
	global_store_dwordx4 v[70:71], v[66:69], off nt
	s_nop 1
	v_or_b32_e32 v66, s4, v145
	v_or_b32_e32 v70, s29, v66
	ds_read_b128 v[66:69], v165
	v_ashrrev_i32_e32 v71, 31, v70
	v_lshlrev_b64 v[70:71], 10, v[70:71]
	v_lshl_add_u64 v[70:71], s[6:7], 0, v[70:71]
	v_lshl_add_u64 v[70:71], v[70:71], 0, v[134:135]
	s_waitcnt lgkmcnt(0)
; #define LAS __attribute__((address_space(3)))
; #define LDS_WAIT() asm volatile("s_waitcnt lgkmcnt(0)" ::: "memory")
; __device__ __forceinline__ void cvt_flush8(const CvtItem& c, const LAS unsigned char* blk, int lane) {
;     LDS_WAIT();
; #pragma unroll
;     for (int t = 0; t < 16; ++t) { const int idx = 64 * t + lane, n = idx >> 4, pc = idx & 15, nn = c.nb * 64 + n;
;         const size_t row = (c.which < 2) ? (size_t)((nn >> 7) * 256 + (nn & 127) + c.which * 128) : (size_t)nn;
;         *(v4u*)(c.dst + row * c.K + 16 * pc) = *(const LAS v4u*)(blk + n * 256 + ((pc ^ ((n >> 2) & 15)) * 16)); }
;     LDS_WAIT();
; }
	global_store_dwordx4 v[70:71], v[66:69], off nt
	s_nop 1
	v_or_b32_e32 v66, s4, v146
	v_or_b32_e32 v70, s29, v66
	ds_read_b128 v[66:69], v166
	v_ashrrev_i32_e32 v71, 31, v70
	v_lshlrev_b64 v[70:71], 10, v[70:71]
	v_lshl_add_u64 v[70:71], s[6:7], 0, v[70:71]
	v_lshl_add_u64 v[70:71], v[70:71], 0, v[134:135]
	s_waitcnt lgkmcnt(0)
	global_store_dwordx4 v[70:71], v[66:69], off nt
	s_nop 1
	v_or_b32_e32 v66, s4, v147
	v_or_b32_e32 v70, s29, v66
	ds_read_b128 v[66:69], v167
	v_ashrrev_i32_e32 v71, 31, v70
	v_lshlrev_b64 v[70:71], 10, v[70:71]
	v_lshl_add_u64 v[70:71], s[6:7], 0, v[70:71]
	v_lshl_add_u64 v[70:71], v[70:71], 0, v[134:135]
	s_waitcnt lgkmcnt(0)
	global_store_dwordx4 v[70:71], v[66:69], off nt
	s_nop 1
	v_or_b32_e32 v66, s4, v148
	v_or_b32_e32 v70, s29, v66
	ds_read_b128 v[66:69], v168
	v_ashrrev_i32_e32 v71, 31, v70
	v_lshlrev_b64 v[70:71], 10, v[70:71]
	v_lshl_add_u64 v[70:71], s[6:7], 0, v[70:71]
	v_lshl_add_u64 v[70:71], v[70:71], 0, v[134:135]
	s_waitcnt lgkmcnt(0)
	global_store_dwordx4 v[70:71], v[66:69], off nt
	s_nop 1
	v_or_b32_e32 v66, s4, v149
	v_or_b32_e32 v70, s29, v66
	ds_read_b128 v[66:69], v169
	v_ashrrev_i32_e32 v71, 31, v70
	v_lshlrev_b64 v[70:71], 10, v[70:71]
	v_lshl_add_u64 v[70:71], s[6:7], 0, v[70:71]
	v_lshl_add_u64 v[70:71], v[70:71], 0, v[134:135]
	s_waitcnt lgkmcnt(0)
	global_store_dwordx4 v[70:71], v[66:69], off nt
	s_nop 1
	v_or_b32_e32 v66, s4, v150
	v_or_b32_e32 v70, s29, v66
	ds_read_b128 v[66:69], v170
	v_ashrrev_i32_e32 v71, 31, v70
	v_lshlrev_b64 v[70:71], 10, v[70:71]
	v_lshl_add_u64 v[70:71], s[6:7], 0, v[70:71]
	v_lshl_add_u64 v[70:71], v[70:71], 0, v[134:135]
	s_waitcnt lgkmcnt(0)
	global_store_dwordx4 v[70:71], v[66:69], off nt
	s_nop 1
	v_or_b32_e32 v66, s4, v151
	v_or_b32_e32 v70, s29, v66
	ds_read_b128 v[66:69], v171
	v_ashrrev_i32_e32 v71, 31, v70
	v_lshlrev_b64 v[70:71], 10, v[70:71]
	v_lshl_add_u64 v[70:71], s[6:7], 0, v[70:71]
	v_lshl_add_u64 v[70:71], v[70:71], 0, v[134:135]
	s_waitcnt lgkmcnt(0)
	global_store_dwordx4 v[70:71], v[66:69], off nt
	s_nop 1
	v_or_b32_e32 v66, s4, v152
	v_or_b32_e32 v70, s29, v66
	ds_read_b128 v[66:69], v172
	v_ashrrev_i32_e32 v71, 31, v70
	v_lshlrev_b64 v[70:71], 10, v[70:71]
	v_lshl_add_u64 v[70:71], s[6:7], 0, v[70:71]
	v_lshl_add_u64 v[70:71], v[70:71], 0, v[134:135]
	s_waitcnt lgkmcnt(0)
	global_store_dwordx4 v[70:71], v[66:69], off nt
	s_nop 1
	v_or_b32_e32 v66, s4, v153
	v_or_b32_e32 v70, s29, v66
	ds_read_b128 v[66:69], v173
	v_ashrrev_i32_e32 v71, 31, v70
	v_lshlrev_b64 v[70:71], 10, v[70:71]
	v_lshl_add_u64 v[70:71], s[6:7], 0, v[70:71]
	v_lshl_add_u64 v[70:71], v[70:71], 0, v[134:135]
	s_waitcnt lgkmcnt(0)
	global_store_dwordx4 v[70:71], v[66:69], off nt
	s_nop 1
	v_or_b32_e32 v66, s4, v154
	v_or_b32_e32 v70, s29, v66
	ds_read_b128 v[66:69], v174
	v_ashrrev_i32_e32 v71, 31, v70
	v_lshlrev_b64 v[70:71], 10, v[70:71]
	v_lshl_add_u64 v[70:71], s[6:7], 0, v[70:71]
	v_lshl_add_u64 v[70:71], v[70:71], 0, v[134:135]
	s_waitcnt lgkmcnt(0)
	global_store_dwordx4 v[70:71], v[66:69], off nt
	s_nop 1
	v_or_b32_e32 v66, s4, v155
	v_or_b32_e32 v70, s29, v66
	ds_read_b128 v[66:69], v175
	v_ashrrev_i32_e32 v71, 31, v70
	v_lshlrev_b64 v[70:71], 10, v[70:71]
	v_lshl_add_u64 v[70:71], s[6:7], 0, v[70:71]
	v_lshl_add_u64 v[70:71], v[70:71], 0, v[134:135]
	s_waitcnt lgkmcnt(0)
	global_store_dwordx4 v[70:71], v[66:69], off nt
	s_waitcnt lgkmcnt(0)
	s_mov_b64 s[6:7], s[8:9]
	s_mov_b32 s29, s27
	s_cbranch_scc0 .LBB0_727
.LBB0_725:
	s_mov_b32 s31, 0x80000
	v_add_co_u32_e32 v66, vcc, s31, v132
	s_mov_b32 s31, 0x82000
	s_nop 0
	v_addc_co_u32_e32 v67, vcc, 0, v133, vcc
	v_add_co_u32_e32 v70, vcc, s31, v132
	s_mov_b32 s31, 0x84000
	s_nop 0
	v_addc_co_u32_e32 v71, vcc, 0, v133, vcc
	v_add_co_u32_e32 v74, vcc, s31, v132
	s_mov_b32 s31, 0x86000
	s_nop 0
	v_addc_co_u32_e32 v75, vcc, 0, v133, vcc
	v_add_co_u32_e32 v78, vcc, s31, v132
	s_mov_b32 s31, 0x88000
	s_nop 0
	v_addc_co_u32_e32 v79, vcc, 0, v133, vcc
	global_load_dwordx4 v[82:85], v[78:79], off nt
	v_add_co_u32_e32 v78, vcc, s31, v132
	s_mov_b32 s31, 0x8a000
	s_nop 0
	v_addc_co_u32_e32 v79, vcc, 0, v133, vcc
	v_add_co_u32_e32 v86, vcc, s31, v132
	s_mov_b32 s31, 0x8c000
	s_nop 0
	v_addc_co_u32_e32 v87, vcc, 0, v133, vcc
	global_load_dwordx4 v[90:93], v[86:87], off nt
	v_add_co_u32_e32 v86, vcc, s31, v132
	s_mov_b32 s31, 0x8e000
	s_nop 0
	v_addc_co_u32_e32 v87, vcc, 0, v133, vcc
	global_load_dwordx4 v[94:97], v[86:87], off nt
	v_add_co_u32_e32 v86, vcc, s31, v132
	s_mov_b32 s31, 0x90000
	s_nop 0
	v_addc_co_u32_e32 v87, vcc, 0, v133, vcc
	global_load_dwordx4 v[106:109], v[86:87], off nt
	v_add_co_u32_e32 v86, vcc, s31, v132
	s_mov_b32 s31, 0x92000
	s_nop 0
	v_addc_co_u32_e32 v87, vcc, 0, v133, vcc
	v_add_co_u32_e32 v98, vcc, s31, v132
	s_mov_b32 s31, 0x94000
	s_nop 0
	v_addc_co_u32_e32 v99, vcc, 0, v133, vcc
	v_add_co_u32_e32 v102, vcc, s31, v132
	s_waitcnt vmcnt(4)
; __device__ __forceinline__ unsigned pk4_fp8(float a, float b, float c, float d) { unsigned w = 0u; w = __builtin_amdgcn_cvt_pk_fp8_f32(a, b, w, false); w = __builtin_amdgcn_cvt_pk_fp8_f32(c, d, w, true); return w; }
; #define LAS __attribute__((address_space(3)))
; #define CVT_LOAD(v, c, s_) do { _Pragma("unroll") for (int i_ = 0; i_ < 16; ++i_) v[i_] = *(const f32x4*)((c).src + (size_t)(64 * (s_) + i_) * (c).N); } while (0)
; __device__ __forceinline__ void cvt_pack8(const f32x4 (&v)[16], const CvtItem& c, LAS unsigned char* blk, int s4, int lane) {
;     const float w = c.wscale; const int cb = lane & 15, j = 4 * s4 + (lane >> 4);
; #pragma unroll
;     for (int jn = 0; jn < 4; ++jn) {
;         v4u o; o.x = pg8::pk4_fp8(v[0][jn] * w, v[1][jn] * w, v[2][jn] * w, v[3][jn] * w); o.y = pg8::pk4_fp8(v[4][jn] * w, v[5][jn] * w, v[6][jn] * w, v[7][jn] * w);
;         o.z = pg8::pk4_fp8(v[8][jn] * w, v[9][jn] * w, v[10][jn] * w, v[11][jn] * w); o.w = pg8::pk4_fp8(v[12][jn] * w, v[13][jn] * w, v[14][jn] * w, v[15][jn] * w);
;         *(LAS v4u*)(blk + (4 * cb + jn) * 256 + ((j ^ cb) * 16)) = o; }
; }
; __device__ __forceinline__ void cvt_moe_pipe2(const CvtSrc& A, const CvtSrc& B, LAS float* scr, int gw, int NGW, int lane) {
;     LAS unsigned char* blk = (LAS unsigned char*)scr;
;     f32x4 va[16], vb[16]; CvtItem c, cn;
;     const int it1 = A.n + B.n; int it = gw;
;     if (it < it1) { c = cvt_moe_item2(it, A, B, lane); CVT_LOAD(va, c, 0); }
;     while (it < it1) {
;         const int i1 = it + NGW; const bool more = i1 < it1;
;         CVT_LOAD(vb, c, 1); cvt_pack8(va, c, blk, 0, lane);
;         CVT_LOAD(va, c, 2); cvt_pack8(vb, c, blk, 1, lane);
;         CVT_LOAD(vb, c, 3); cvt_pack8(va, c, blk, 2, lane);
;         if (more) { cn = cvt_moe_item2(i1, A, B, lane); CVT_LOAD(va, cn, 0); }
;         cvt_pack8(vb, c, blk, 3, lane);
	v_mul_f32_e32 v62, v62, v177
	v_mul_f32_e32 v6, v6, v177
	v_addc_co_u32_e32 v103, vcc, 0, v133, vcc
	s_mov_b32 s31, 0x96000
	v_cvt_pk_fp8_f32 v178, v62, v6
	v_add_co_u32_e32 v110, vcc, s31, v132
	s_mov_b32 s31, 0x98000
	s_nop 0
	v_addc_co_u32_e32 v111, vcc, 0, v133, vcc
	global_load_dwordx4 v[102:105], v[102:103], off nt
	v_mul_f32_e32 v2, v2, v177
	global_load_dwordx4 v[114:117], v[110:111], off nt
	v_add_co_u32_e32 v110, vcc, s31, v132
	v_mul_f32_e32 v18, v18, v177
	global_load_dwordx4 v[66:69], v[66:67], off nt
	v_addc_co_u32_e32 v111, vcc, 0, v133, vcc
	global_load_dwordx4 v[70:73], v[70:71], off nt
	s_mov_b32 s31, 0x9a000
	v_cvt_pk_fp8_f32 v178, v2, v18 op_sel:[0,0,1]
	v_mul_f32_e32 v2, v10, v177
	v_mul_f32_e32 v6, v26, v177
	global_load_dwordx4 v[78:81], v[78:79], off nt
	v_add_co_u32_e32 v118, vcc, s31, v132
	v_cvt_pk_fp8_f32 v179, v2, v6
	v_mul_f32_e32 v2, v14, v177
	v_mul_f32_e32 v6, v34, v177
	global_load_dwordx4 v[86:89], v[86:87], off nt
	v_addc_co_u32_e32 v119, vcc, 0, v133, vcc
	global_load_dwordx4 v[98:101], v[98:99], off nt
	s_mov_b32 s31, 0x9c000
	v_cvt_pk_fp8_f32 v180, v2, v6
	v_mul_f32_e32 v2, v38, v177
	v_mul_f32_e32 v6, v54, v177
	global_load_dwordx4 v[110:113], v[110:111], off nt
	v_add_co_u32_e32 v122, vcc, s31, v132
	global_load_dwordx4 v[118:121], v[118:119], off nt
	v_cvt_pk_fp8_f32 v181, v2, v6
	global_load_dwordx4 v[74:77], v[74:75], off nt
	v_addc_co_u32_e32 v123, vcc, 0, v133, vcc
	s_mov_b32 s31, 0x9e000
	v_mul_f32_e32 v10, v22, v177
	v_mul_f32_e32 v18, v42, v177
	v_add_co_u32_e32 v126, vcc, s31, v132
	v_cvt_pk_fp8_f32 v179, v10, v18 op_sel:[0,0,1]
	v_mul_f32_e32 v10, v30, v177
	v_mul_f32_e32 v14, v46, v177
	v_addc_co_u32_e32 v127, vcc, 0, v133, vcc
	v_cvt_pk_fp8_f32 v180, v10, v14 op_sel:[0,0,1]
	v_mul_f32_e32 v10, v50, v177
	v_mul_f32_e32 v14, v58, v177
	global_load_dwordx4 v[122:125], v[122:123], off nt
	v_cvt_pk_fp8_f32 v181, v10, v14 op_sel:[0,0,1]
	global_load_dwordx4 v[126:129], v[126:127], off nt
	v_mul_f32_e32 v2, v63, v177
	v_mul_f32_e32 v6, v7, v177
	ds_write_b128 v156, v[178:181]
	v_cvt_pk_fp8_f32 v178, v2, v6
	v_mul_f32_e32 v3, v3, v177
	v_mul_f32_e32 v7, v19, v177
	v_mul_f32_e32 v2, v11, v177
	v_cvt_pk_fp8_f32 v178, v3, v7 op_sel:[0,0,1]
	v_mul_f32_e32 v3, v27, v177
	v_cvt_pk_fp8_f32 v179, v2, v3
	v_mul_f32_e32 v2, v15, v177
	v_mul_f32_e32 v3, v35, v177
	v_cvt_pk_fp8_f32 v180, v2, v3
	v_mul_f32_e32 v2, v39, v177
	v_mul_f32_e32 v3, v55, v177
	v_cvt_pk_fp8_f32 v181, v2, v3
	v_mul_f32_e32 v6, v23, v177
	v_mul_f32_e32 v7, v43, v177
	v_cvt_pk_fp8_f32 v179, v6, v7 op_sel:[0,0,1]
	v_mul_f32_e32 v6, v31, v177
	v_mul_f32_e32 v7, v47, v177
	v_cvt_pk_fp8_f32 v180, v6, v7 op_sel:[0,0,1]
	v_mul_f32_e32 v6, v51, v177
	v_mul_f32_e32 v7, v59, v177
	v_cvt_pk_fp8_f32 v181, v6, v7 op_sel:[0,0,1]
	v_mul_f32_e32 v2, v64, v177
	v_mul_f32_e32 v3, v8, v177
	v_mul_f32_e32 v4, v4, v177
	ds_write_b128 v156, v[178:181] offset:256
	v_cvt_pk_fp8_f32 v178, v2, v3
	v_mul_f32_e32 v2, v12, v177
	v_mul_f32_e32 v3, v28, v177
	v_cvt_pk_fp8_f32 v179, v2, v3
	v_mul_f32_e32 v2, v16, v177
	v_mul_f32_e32 v3, v36, v177
	v_cvt_pk_fp8_f32 v180, v2, v3
	v_mul_f32_e32 v2, v40, v177
	v_mul_f32_e32 v3, v56, v177
	v_mul_f32_e32 v6, v20, v177
	v_cvt_pk_fp8_f32 v181, v2, v3
	v_cvt_pk_fp8_f32 v178, v4, v6 op_sel:[0,0,1]
	v_mul_f32_e32 v4, v24, v177
	v_mul_f32_e32 v6, v44, v177
	v_cvt_pk_fp8_f32 v179, v4, v6 op_sel:[0,0,1]
	v_mul_f32_e32 v4, v32, v177
	v_mul_f32_e32 v6, v48, v177
	v_cvt_pk_fp8_f32 v180, v4, v6 op_sel:[0,0,1]
	v_mul_f32_e32 v4, v52, v177
	v_mul_f32_e32 v6, v60, v177
	v_cvt_pk_fp8_f32 v181, v4, v6 op_sel:[0,0,1]
	v_mul_f32_e32 v3, v65, v177
	v_mul_f32_e32 v4, v9, v177
	v_cvt_pk_fp8_f32 v2, v3, v4
	v_mul_f32_e32 v5, v5, v177
	v_mul_f32_e32 v6, v21, v177
	v_mul_f32_e32 v4, v13, v177
	v_cvt_pk_fp8_f32 v2, v5, v6 op_sel:[0,0,1]
	v_mul_f32_e32 v5, v29, v177
	v_cvt_pk_fp8_f32 v3, v4, v5
	v_mul_f32_e32 v6, v25, v177
	v_mul_f32_e32 v7, v45, v177
	v_mul_f32_e32 v5, v17, v177
	v_cvt_pk_fp8_f32 v3, v6, v7 op_sel:[0,0,1]
	v_mul_f32_e32 v6, v37, v177
	v_cvt_pk_fp8_f32 v4, v5, v6
	v_mul_f32_e32 v7, v33, v177
	v_mul_f32_e32 v8, v49, v177
	v_mul_f32_e32 v6, v41, v177
	v_cvt_pk_fp8_f32 v4, v7, v8 op_sel:[0,0,1]
	v_mul_f32_e32 v7, v57, v177
	v_cvt_pk_fp8_f32 v5, v6, v7
	v_mul_f32_e32 v8, v53, v177
	v_mul_f32_e32 v9, v61, v177
	s_mov_b32 s31, 0x100000
	v_cvt_pk_fp8_f32 v5, v8, v9 op_sel:[0,0,1]
	ds_write_b128 v156, v[178:181] offset:512
	ds_write_b128 v156, v[2:5] offset:768
	v_add_co_u32_e32 v2, vcc, s31, v132
	s_mov_b32 s31, 0x102000
	s_nop 0
	v_addc_co_u32_e32 v3, vcc, 0, v133, vcc
	global_load_dwordx4 v[62:65], v[2:3], off nt
	v_add_co_u32_e32 v2, vcc, s31, v132
	s_mov_b32 s31, 0x104000
	s_nop 0
	v_addc_co_u32_e32 v3, vcc, 0, v133, vcc
	global_load_dwordx4 v[6:9], v[2:3], off nt
	v_add_co_u32_e32 v2, vcc, s31, v132
	s_mov_b32 s31, 0x106000
	s_nop 0
	v_addc_co_u32_e32 v3, vcc, 0, v133, vcc
	v_add_co_u32_e32 v10, vcc, s31, v132
	s_mov_b32 s31, 0x108000
	s_nop 0
	v_addc_co_u32_e32 v11, vcc, 0, v133, vcc
	global_load_dwordx4 v[2:5], v[2:3], off nt
	s_waitcnt vmcnt(12)
	v_mul_f32_e32 v66, v177, v66
	global_load_dwordx4 v[18:21], v[10:11], off nt
	v_add_co_u32_e32 v10, vcc, s31, v132
	s_mov_b32 s31, 0x10a000
	s_nop 0
	v_addc_co_u32_e32 v11, vcc, 0, v133, vcc
	v_add_co_u32_e32 v14, vcc, s31, v132
	s_mov_b32 s31, 0x10c000
	s_nop 0
	v_addc_co_u32_e32 v15, vcc, 0, v133, vcc
	global_load_dwordx4 v[10:13], v[10:11], off nt
	s_waitcnt vmcnt(13)
; __device__ __forceinline__ unsigned pk4_fp8(float a, float b, float c, float d) { unsigned w = 0u; w = __builtin_amdgcn_cvt_pk_fp8_f32(a, b, w, false); w = __builtin_amdgcn_cvt_pk_fp8_f32(c, d, w, true); return w; }
; #define LAS __attribute__((address_space(3)))
; #define CVT_LOAD(v, c, s_) do { _Pragma("unroll") for (int i_ = 0; i_ < 16; ++i_) v[i_] = *(const f32x4*)((c).src + (size_t)(64 * (s_) + i_) * (c).N); } while (0)
; __device__ __forceinline__ void cvt_pack8(const f32x4 (&v)[16], const CvtItem& c, LAS unsigned char* blk, int s4, int lane) {
;     const float w = c.wscale; const int cb = lane & 15, j = 4 * s4 + (lane >> 4);
; #pragma unroll
;     for (int jn = 0; jn < 4; ++jn) {
;         v4u o; o.x = pg8::pk4_fp8(v[0][jn] * w, v[1][jn] * w, v[2][jn] * w, v[3][jn] * w); o.y = pg8::pk4_fp8(v[4][jn] * w, v[5][jn] * w, v[6][jn] * w, v[7][jn] * w);
;         o.z = pg8::pk4_fp8(v[8][jn] * w, v[9][jn] * w, v[10][jn] * w, v[11][jn] * w); o.w = pg8::pk4_fp8(v[12][jn] * w, v[13][jn] * w, v[14][jn] * w, v[15][jn] * w);
;         *(LAS v4u*)(blk + (4 * cb + jn) * 256 + ((j ^ cb) * 16)) = o; }
; }
; __device__ __forceinline__ void cvt_moe_pipe2(const CvtSrc& A, const CvtSrc& B, LAS float* scr, int gw, int NGW, int lane) {
;     LAS unsigned char* blk = (LAS unsigned char*)scr;
;     f32x4 va[16], vb[16]; CvtItem c, cn;
;     const int it1 = A.n + B.n; int it = gw;
;     if (it < it1) { c = cvt_moe_item2(it, A, B, lane); CVT_LOAD(va, c, 0); }
;     while (it < it1) {
;         const int i1 = it + NGW; const bool more = i1 < it1;
;         CVT_LOAD(vb, c, 1); cvt_pack8(va, c, blk, 0, lane);
;         CVT_LOAD(va, c, 2); cvt_pack8(vb, c, blk, 1, lane);
;         CVT_LOAD(vb, c, 3); cvt_pack8(va, c, blk, 2, lane);
;         if (more) { cn = cvt_moe_item2(i1, A, B, lane); CVT_LOAD(va, cn, 0); }
;         cvt_pack8(vb, c, blk, 3, lane);
	v_mul_f32_e32 v70, v177, v70
	global_load_dwordx4 v[26:29], v[14:15], off nt
	v_add_co_u32_e32 v14, vcc, s31, v132
	s_mov_b32 s31, 0x10e000
	s_nop 0
	v_addc_co_u32_e32 v15, vcc, 0, v133, vcc
	global_load_dwordx4 v[22:25], v[14:15], off nt
	v_add_co_u32_e32 v14, vcc, s31, v132
	s_mov_b32 s31, 0x110000
	s_nop 0
	v_addc_co_u32_e32 v15, vcc, 0, v133, vcc
	global_load_dwordx4 v[42:45], v[14:15], off nt
	v_add_co_u32_e32 v14, vcc, s31, v132
	s_mov_b32 s31, 0x112000
	s_nop 0
	v_addc_co_u32_e32 v15, vcc, 0, v133, vcc
	v_add_co_u32_e32 v30, vcc, s31, v132
	s_mov_b32 s31, 0x114000
	s_nop 0
	v_addc_co_u32_e32 v31, vcc, 0, v133, vcc
	global_load_dwordx4 v[14:17], v[14:15], off nt
	v_cvt_pk_fp8_f32 v178, v66, v70
	global_load_dwordx4 v[34:37], v[30:31], off nt
	v_add_co_u32_e32 v30, vcc, s31, v132
	s_mov_b32 s31, 0x116000
	s_nop 0
	v_addc_co_u32_e32 v31, vcc, 0, v133, vcc
	v_add_co_u32_e32 v38, vcc, s31, v132
	s_waitcnt vmcnt(17)
	v_mul_f32_e32 v66, v177, v78
	v_mul_f32_e32 v70, v177, v90
	v_addc_co_u32_e32 v39, vcc, 0, v133, vcc
	s_mov_b32 s31, 0x118000
	v_cvt_pk_fp8_f32 v179, v66, v70
	s_waitcnt vmcnt(16)
	v_mul_f32_e32 v66, v177, v86
	s_waitcnt vmcnt(15)
	v_mul_f32_e32 v70, v177, v98
	global_load_dwordx4 v[30:33], v[30:31], off nt
	v_cvt_pk_fp8_f32 v180, v66, v70
	global_load_dwordx4 v[46:49], v[38:39], off nt
	v_add_co_u32_e32 v38, vcc, s31, v132
	s_waitcnt vmcnt(16)
	v_mul_f32_e32 v66, v177, v110
	s_waitcnt vmcnt(15)
	v_mul_f32_e32 v70, v177, v118
	v_addc_co_u32_e32 v39, vcc, 0, v133, vcc
	s_mov_b32 s31, 0x11a000
	s_waitcnt vmcnt(14)
	v_mul_f32_e32 v74, v177, v74
	v_mul_f32_e32 v82, v177, v82
	v_cvt_pk_fp8_f32 v181, v66, v70
	v_add_co_u32_e32 v50, vcc, s31, v132
	v_cvt_pk_fp8_f32 v178, v74, v82 op_sel:[0,0,1]
	v_mul_f32_e32 v74, v177, v94
	v_mul_f32_e32 v78, v177, v106
	v_addc_co_u32_e32 v51, vcc, 0, v133, vcc
	s_mov_b32 s31, 0x11c000
	v_cvt_pk_fp8_f32 v179, v74, v78 op_sel:[0,0,1]
	v_mul_f32_e32 v74, v177, v102
	v_mul_f32_e32 v78, v177, v114
	global_load_dwordx4 v[38:41], v[38:39], off nt
	v_cvt_pk_fp8_f32 v180, v74, v78 op_sel:[0,0,1]
	global_load_dwordx4 v[54:57], v[50:51], off nt
	v_add_co_u32_e32 v50, vcc, s31, v132
	s_waitcnt vmcnt(15)
	v_mul_f32_e32 v74, v177, v122
	s_waitcnt vmcnt(14)
	v_mul_f32_e32 v78, v177, v126
	v_addc_co_u32_e32 v51, vcc, 0, v133, vcc
	s_mov_b32 s31, 0x11e000
	v_cvt_pk_fp8_f32 v181, v74, v78 op_sel:[0,0,1]
	v_add_co_u32_e32 v58, vcc, s31, v132
	global_load_dwordx4 v[50:53], v[50:51], off nt
	s_nop 0
	v_addc_co_u32_e32 v59, vcc, 0, v133, vcc
	global_load_dwordx4 v[58:61], v[58:59], off nt
	ds_write_b128 v157, v[178:181]
	v_mul_f32_e32 v66, v177, v67
	v_mul_f32_e32 v67, v177, v71
	v_cvt_pk_fp8_f32 v178, v66, v67
	v_mul_f32_e32 v66, v177, v79
	v_mul_f32_e32 v67, v177, v91
	v_cvt_pk_fp8_f32 v179, v66, v67
	v_mul_f32_e32 v66, v177, v87
	v_mul_f32_e32 v67, v177, v99
	v_cvt_pk_fp8_f32 v180, v66, v67
	v_mul_f32_e32 v66, v177, v111
	v_mul_f32_e32 v67, v177, v119
	v_mul_f32_e32 v70, v177, v75
	v_mul_f32_e32 v71, v177, v83
	v_cvt_pk_fp8_f32 v181, v66, v67
	v_cvt_pk_fp8_f32 v178, v70, v71 op_sel:[0,0,1]
	v_mul_f32_e32 v70, v177, v95
	v_mul_f32_e32 v71, v177, v107
	v_cvt_pk_fp8_f32 v179, v70, v71 op_sel:[0,0,1]
	v_mul_f32_e32 v70, v177, v103
	v_mul_f32_e32 v71, v177, v115
	v_cvt_pk_fp8_f32 v180, v70, v71 op_sel:[0,0,1]
	v_mul_f32_e32 v70, v177, v123
	v_mul_f32_e32 v71, v177, v127
	v_cvt_pk_fp8_f32 v181, v70, v71 op_sel:[0,0,1]
	v_mul_f32_e32 v66, v177, v68
	v_mul_f32_e32 v67, v177, v72
	v_mul_f32_e32 v68, v177, v76
	ds_write_b128 v157, v[178:181] offset:256
	v_cvt_pk_fp8_f32 v178, v66, v67
	v_mul_f32_e32 v66, v177, v80
	v_mul_f32_e32 v67, v177, v92
	v_cvt_pk_fp8_f32 v179, v66, v67
	v_mul_f32_e32 v66, v177, v88
	v_mul_f32_e32 v67, v177, v100
	v_cvt_pk_fp8_f32 v180, v66, v67
	v_mul_f32_e32 v66, v177, v112
	v_mul_f32_e32 v67, v177, v120
	v_mul_f32_e32 v70, v177, v84
	v_cvt_pk_fp8_f32 v181, v66, v67
	v_cvt_pk_fp8_f32 v178, v68, v70 op_sel:[0,0,1]
	v_mul_f32_e32 v68, v177, v96
	v_mul_f32_e32 v70, v177, v108
	v_cvt_pk_fp8_f32 v179, v68, v70 op_sel:[0,0,1]
	v_mul_f32_e32 v68, v177, v104
	v_mul_f32_e32 v70, v177, v116
	v_cvt_pk_fp8_f32 v180, v68, v70 op_sel:[0,0,1]
	v_mul_f32_e32 v68, v177, v124
	v_mul_f32_e32 v70, v177, v128
	v_cvt_pk_fp8_f32 v181, v68, v70 op_sel:[0,0,1]
	v_mul_f32_e32 v67, v177, v69
	v_mul_f32_e32 v68, v177, v73
	v_cvt_pk_fp8_f32 v66, v67, v68
	v_mul_f32_e32 v69, v177, v77
	v_mul_f32_e32 v70, v177, v85
	v_mul_f32_e32 v68, v177, v81
	v_cvt_pk_fp8_f32 v66, v69, v70 op_sel:[0,0,1]
	v_mul_f32_e32 v69, v177, v93
	v_cvt_pk_fp8_f32 v67, v68, v69
	v_mul_f32_e32 v70, v177, v97
	v_mul_f32_e32 v71, v177, v109
	v_mul_f32_e32 v69, v177, v89
	v_cvt_pk_fp8_f32 v67, v70, v71 op_sel:[0,0,1]
	v_mul_f32_e32 v70, v177, v101
	v_cvt_pk_fp8_f32 v68, v69, v70
	v_mul_f32_e32 v71, v177, v105
	v_mul_f32_e32 v72, v177, v117
	v_mul_f32_e32 v70, v177, v113
	v_cvt_pk_fp8_f32 v68, v71, v72 op_sel:[0,0,1]
	v_mul_f32_e32 v71, v177, v121
	v_cvt_pk_fp8_f32 v69, v70, v71
	v_mul_f32_e32 v72, v177, v125
	v_mul_f32_e32 v73, v177, v129
	s_mov_b32 s31, 0x180000
	v_cvt_pk_fp8_f32 v69, v72, v73 op_sel:[0,0,1]
	ds_write_b128 v157, v[178:181] offset:512
	s_waitcnt vmcnt(15)
	v_mul_f32_e32 v130, v177, v62
	s_waitcnt vmcnt(14)
; __device__ __forceinline__ unsigned pk4_fp8(float a, float b, float c, float d) { unsigned w = 0u; w = __builtin_amdgcn_cvt_pk_fp8_f32(a, b, w, false); w = __builtin_amdgcn_cvt_pk_fp8_f32(c, d, w, true); return w; }
; #define LAS __attribute__((address_space(3)))
; #define CVT_LOAD(v, c, s_) do { _Pragma("unroll") for (int i_ = 0; i_ < 16; ++i_) v[i_] = *(const f32x4*)((c).src + (size_t)(64 * (s_) + i_) * (c).N); } while (0)
; __device__ __forceinline__ void cvt_pack8(const f32x4 (&v)[16], const CvtItem& c, LAS unsigned char* blk, int s4, int lane) {
;     const float w = c.wscale; const int cb = lane & 15, j = 4 * s4 + (lane >> 4);
; #pragma unroll
;     for (int jn = 0; jn < 4; ++jn) {
;         v4u o; o.x = pg8::pk4_fp8(v[0][jn] * w, v[1][jn] * w, v[2][jn] * w, v[3][jn] * w); o.y = pg8::pk4_fp8(v[4][jn] * w, v[5][jn] * w, v[6][jn] * w, v[7][jn] * w);
;         o.z = pg8::pk4_fp8(v[8][jn] * w, v[9][jn] * w, v[10][jn] * w, v[11][jn] * w); o.w = pg8::pk4_fp8(v[12][jn] * w, v[13][jn] * w, v[14][jn] * w, v[15][jn] * w);
;         *(LAS v4u*)(blk + (4 * cb + jn) * 256 + ((j ^ cb) * 16)) = o; }
; }
; __device__ __forceinline__ void cvt_moe_pipe2(const CvtSrc& A, const CvtSrc& B, LAS float* scr, int gw, int NGW, int lane) {
;     LAS unsigned char* blk = (LAS unsigned char*)scr;
;     f32x4 va[16], vb[16]; CvtItem c, cn;
;     const int it1 = A.n + B.n; int it = gw;
;     if (it < it1) { c = cvt_moe_item2(it, A, B, lane); CVT_LOAD(va, c, 0); }
;     while (it < it1) {
;         const int i1 = it + NGW; const bool more = i1 < it1;
;         CVT_LOAD(vb, c, 1); cvt_pack8(va, c, blk, 0, lane);
;         CVT_LOAD(va, c, 2); cvt_pack8(vb, c, blk, 1, lane);
;         CVT_LOAD(vb, c, 3); cvt_pack8(va, c, blk, 2, lane);
;         if (more) { cn = cvt_moe_item2(i1, A, B, lane); CVT_LOAD(va, cn, 0); }
;         cvt_pack8(vb, c, blk, 3, lane);
;         cvt_flush8(c, blk, lane);
;         if (more) c = cn;
	v_mul_f32_e32 v137, v177, v6
	ds_write_b128 v157, v[66:69] offset:768
	v_add_co_u32_e32 v66, vcc, s31, v132
	s_mov_b32 s31, 0x182000
	s_nop 0
	v_addc_co_u32_e32 v67, vcc, 0, v133, vcc
	v_add_co_u32_e32 v70, vcc, s31, v132
	s_mov_b32 s31, 0x184000
	s_nop 0
	v_addc_co_u32_e32 v71, vcc, 0, v133, vcc
	v_add_co_u32_e32 v74, vcc, s31, v132
	s_mov_b32 s31, 0x186000
	s_nop 0
	v_addc_co_u32_e32 v75, vcc, 0, v133, vcc
	v_add_co_u32_e32 v78, vcc, s31, v132
	s_mov_b32 s31, 0x188000
	s_nop 0
	v_addc_co_u32_e32 v79, vcc, 0, v133, vcc
	global_load_dwordx4 v[74:77], v[74:75], off nt
	global_load_dwordx4 v[82:85], v[78:79], off nt
	v_add_co_u32_e32 v78, vcc, s31, v132
	s_mov_b32 s31, 0x18a000
	s_nop 0
	v_addc_co_u32_e32 v79, vcc, 0, v133, vcc
	v_add_co_u32_e32 v86, vcc, s31, v132
	s_mov_b32 s31, 0x18c000
	s_nop 0
	v_addc_co_u32_e32 v87, vcc, 0, v133, vcc
	global_load_dwordx4 v[78:81], v[78:79], off nt
	v_cvt_pk_fp8_f32 v178, v130, v137
	global_load_dwordx4 v[90:93], v[86:87], off nt
	v_add_co_u32_e32 v86, vcc, s31, v132
	s_mov_b32 s31, 0x18e000
	s_nop 0
	v_addc_co_u32_e32 v87, vcc, 0, v133, vcc
	global_load_dwordx4 v[94:97], v[86:87], off nt
	v_add_co_u32_e32 v86, vcc, s31, v132
	s_mov_b32 s31, 0x190000
	s_nop 0
	v_addc_co_u32_e32 v87, vcc, 0, v133, vcc
	global_load_dwordx4 v[106:109], v[86:87], off nt
	v_add_co_u32_e32 v86, vcc, s31, v132
	s_mov_b32 s31, 0x192000
	s_nop 0
	v_addc_co_u32_e32 v87, vcc, 0, v133, vcc
	v_add_co_u32_e32 v98, vcc, s31, v132
	s_mov_b32 s31, 0x194000
	s_nop 0
	v_addc_co_u32_e32 v99, vcc, 0, v133, vcc
	v_add_co_u32_e32 v102, vcc, s31, v132
	s_waitcnt vmcnt(19)
	v_mul_f32_e32 v179, v177, v2
	s_waitcnt vmcnt(18)
	v_mul_f32_e32 v180, v177, v18
	v_addc_co_u32_e32 v103, vcc, 0, v133, vcc
	s_mov_b32 s31, 0x196000
	v_cvt_pk_fp8_f32 v178, v179, v180 op_sel:[0,0,1]
	s_waitcnt vmcnt(17)
	v_mul_f32_e32 v130, v177, v10
	s_waitcnt vmcnt(16)
	v_mul_f32_e32 v137, v177, v26
	v_add_co_u32_e32 v110, vcc, s31, v132
	v_cvt_pk_fp8_f32 v179, v130, v137
	s_nop 0
	v_addc_co_u32_e32 v111, vcc, 0, v133, vcc
	s_mov_b32 s31, 0x198000
	global_load_dwordx4 v[102:105], v[102:103], off nt
	s_waitcnt vmcnt(16)
	v_mul_f32_e32 v180, v177, v22
	global_load_dwordx4 v[114:117], v[110:111], off nt
	v_add_co_u32_e32 v110, vcc, s31, v132
	s_mov_b32 s31, 0x19a000
	s_nop 0
	v_addc_co_u32_e32 v111, vcc, 0, v133, vcc
	s_waitcnt vmcnt(16)
	v_mul_f32_e32 v181, v177, v42
	v_add_co_u32_e32 v118, vcc, s31, v132
	v_cvt_pk_fp8_f32 v179, v180, v181 op_sel:[0,0,1]
	s_waitcnt vmcnt(15)
	v_mul_f32_e32 v130, v177, v14
	s_waitcnt vmcnt(14)
	v_mul_f32_e32 v137, v177, v34
	v_addc_co_u32_e32 v119, vcc, 0, v133, vcc
	s_mov_b32 s31, 0x19c000
	v_cvt_pk_fp8_f32 v180, v130, v137
	v_add_co_u32_e32 v122, vcc, s31, v132
	s_mov_b32 s31, 0x19e000
	s_nop 0
	v_addc_co_u32_e32 v123, vcc, 0, v133, vcc
	v_add_co_u32_e32 v126, vcc, s31, v132
	s_waitcnt vmcnt(13)
	v_mul_f32_e32 v181, v177, v30
	s_waitcnt vmcnt(12)
	v_mul_f32_e32 v182, v177, v46
	v_addc_co_u32_e32 v127, vcc, 0, v133, vcc
	v_cvt_pk_fp8_f32 v180, v181, v182 op_sel:[0,0,1]
	s_waitcnt vmcnt(11)
	v_mul_f32_e32 v130, v177, v38
	s_waitcnt vmcnt(10)
	v_mul_f32_e32 v137, v177, v54
	global_load_dwordx4 v[66:69], v[66:67], off nt
	v_cvt_pk_fp8_f32 v181, v130, v137
	global_load_dwordx4 v[70:73], v[70:71], off nt
	s_waitcnt vmcnt(11)
	v_mul_f32_e32 v182, v177, v50
	global_load_dwordx4 v[86:89], v[86:87], off nt
	s_waitcnt vmcnt(11)
	v_mul_f32_e32 v183, v177, v58
	global_load_dwordx4 v[98:101], v[98:99], off nt
	v_cvt_pk_fp8_f32 v181, v182, v183 op_sel:[0,0,1]
	global_load_dwordx4 v[110:113], v[110:111], off nt
	v_mul_f32_e32 v130, v177, v63
	global_load_dwordx4 v[118:121], v[118:119], off nt
	ds_write_b128 v158, v[178:181]
	global_load_dwordx4 v[122:125], v[122:123], off nt
	v_mul_f32_e32 v137, v177, v7
	global_load_dwordx4 v[126:129], v[126:127], off nt
	v_cvt_pk_fp8_f32 v178, v130, v137
	v_mul_f32_e32 v179, v177, v3
	v_mul_f32_e32 v180, v177, v19
	v_mul_f32_e32 v130, v177, v11
	v_cvt_pk_fp8_f32 v178, v179, v180 op_sel:[0,0,1]
	v_mul_f32_e32 v137, v177, v27
	v_cvt_pk_fp8_f32 v179, v130, v137
	v_mul_f32_e32 v180, v177, v23
	v_mul_f32_e32 v181, v177, v43
	v_mul_f32_e32 v130, v177, v15
	v_cvt_pk_fp8_f32 v179, v180, v181 op_sel:[0,0,1]
	v_mul_f32_e32 v137, v177, v35
	v_cvt_pk_fp8_f32 v180, v130, v137
	v_mul_f32_e32 v181, v177, v31
	v_mul_f32_e32 v182, v177, v47
	v_mul_f32_e32 v130, v177, v39
	v_cvt_pk_fp8_f32 v180, v181, v182 op_sel:[0,0,1]
	v_mul_f32_e32 v137, v177, v55
	v_cvt_pk_fp8_f32 v181, v130, v137
	v_mul_f32_e32 v182, v177, v51
	v_mul_f32_e32 v183, v177, v59
	v_mul_f32_e32 v130, v177, v64
	v_cvt_pk_fp8_f32 v181, v182, v183 op_sel:[0,0,1]
	v_mul_f32_e32 v137, v177, v8
	v_mul_f32_e32 v182, v177, v48
	v_mul_f32_e32 v183, v177, v60
	ds_write_b128 v158, v[178:181] offset:256
	v_cvt_pk_fp8_f32 v178, v130, v137
	v_mul_f32_e32 v179, v177, v4
	v_mul_f32_e32 v180, v177, v20
	v_mul_f32_e32 v130, v177, v12
	v_cvt_pk_fp8_f32 v178, v179, v180 op_sel:[0,0,1]
	v_mul_f32_e32 v137, v177, v28
	v_cvt_pk_fp8_f32 v179, v130, v137
	v_mul_f32_e32 v180, v177, v24
	v_mul_f32_e32 v181, v177, v44
	v_mul_f32_e32 v130, v177, v16
	v_cvt_pk_fp8_f32 v179, v180, v181 op_sel:[0,0,1]
	v_mul_f32_e32 v137, v177, v36
	v_cvt_pk_fp8_f32 v180, v130, v137
	v_mul_f32_e32 v181, v177, v32
	v_mul_f32_e32 v130, v177, v40
	v_mul_f32_e32 v137, v177, v56
	v_cvt_pk_fp8_f32 v180, v181, v182 op_sel:[0,0,1]
	v_cvt_pk_fp8_f32 v181, v130, v137
	v_mul_f32_e32 v182, v177, v52
	v_mul_f32_e32 v130, v177, v65
	v_mul_f32_e32 v137, v177, v9
	v_cvt_pk_fp8_f32 v181, v182, v183 op_sel:[0,0,1]
	v_mul_f32_e32 v182, v177, v49
	v_mul_f32_e32 v183, v177, v61
	v_readlane_b32 s4, v254, 52
	ds_write_b128 v158, v[178:181] offset:512
	v_cvt_pk_fp8_f32 v178, v130, v137
	v_mul_f32_e32 v179, v177, v5
	v_mul_f32_e32 v180, v177, v21
	v_mul_f32_e32 v130, v177, v13
	v_cvt_pk_fp8_f32 v178, v179, v180 op_sel:[0,0,1]
	v_mul_f32_e32 v137, v177, v29
	v_cvt_pk_fp8_f32 v179, v130, v137
	v_mul_f32_e32 v180, v177, v25
	v_mul_f32_e32 v181, v177, v45
	v_mul_f32_e32 v130, v177, v17
	v_cvt_pk_fp8_f32 v179, v180, v181 op_sel:[0,0,1]
	v_mul_f32_e32 v137, v177, v37
	v_cvt_pk_fp8_f32 v180, v130, v137
	v_mul_f32_e32 v181, v177, v33
	v_mul_f32_e32 v130, v177, v41
	v_mul_f32_e32 v137, v177, v57
	v_cvt_pk_fp8_f32 v180, v181, v182 op_sel:[0,0,1]
	v_cvt_pk_fp8_f32 v181, v130, v137
	v_mul_f32_e32 v182, v177, v53
	s_add_i32 s4, s4, s2
	s_addk_i32 s4, 0xfe00
	v_cvt_pk_fp8_f32 v181, v182, v183 op_sel:[0,0,1]
	s_cmpk_gt_i32 s4, 0x50f
	ds_write_b128 v158, v[178:181] offset:768
	s_cbranch_scc1 .LBB0_724
; __device__ __forceinline__ CvtItem cvt_moe_item(int it, const float* wg, const float* wu, const float* wd, unsigned char* WGU, unsigned char* WDN, int lane) {
;     const int which = it >> 11, r = it & 2047, e = r >> 7, q = r & 127; CvtItem c; c.which = which;
;     if (which < 2) { const int nb = q & 31, k0 = (q >> 5) * 256; c.nb = nb;
;         c.N = DFF; c.K = DM; c.wscale = which ? 64.f / LOG2E : 64.f * LOG2E; c.src = (which ? wu : wg) + (size_t)e * DM * DFF + (size_t)(k0 + 16 * (lane >> 4)) * DFF + nb * 64 + 4 * (lane & 15);
;         c.dst = WGU + (size_t)e * 4096 * DM + k0; }
;     else { const int nb = q & 15, k0 = (q >> 4) * 256; c.nb = nb;
;         c.N = DM; c.K = DFF; c.wscale = 64.f; c.src = wd + (size_t)e * DFF * DM + (size_t)(k0 + 16 * (lane >> 4)) * DM + nb * 64 + 4 * (lane & 15);
;         c.dst = WDN + (size_t)e * DM * DFF + k0; }
;     return c;
; }
	s_ashr_i32 s27, s4, 11
	s_and_b32 s28, s4, 31
	s_and_b32 s31, s25, 0x300
	s_cmpk_lt_u32 s4, 0x800
	s_cselect_b64 vcc, -1, 0
	v_readlane_b32 s36, v254, 30
	s_and_b64 s[8:9], vcc, exec
	v_readlane_b32 s48, v254, 42
	v_readlane_b32 s49, v254, 43
	v_readlane_b32 s50, v254, 44
	v_readlane_b32 s51, v254, 45
	s_cselect_b32 s9, s49, s51
	s_cselect_b32 s8, s48, s50
	s_bfe_u32 s33, s4, 0x40007
	s_lshl_b32 s4, s33, 23
	s_add_u32 s8, s8, s4
	v_or_b32_e32 v2, s31, v141
	s_addc_u32 s9, s9, 0
	v_lshlrev_b32_e32 v130, 13, v2
	v_lshl_add_u64 v[2:3], s[8:9], 0, v[130:131]
	s_lshl_b32 s4, s28, 8
	v_lshl_add_u64 v[2:3], v[2:3], 0, s[4:5]
	v_mov_b32_e32 v137, v131
	v_lshl_add_u64 v[132:133], v[2:3], 0, v[136:137]
	v_cndmask_b32_e32 v176, v139, v140, vcc
	v_add_co_u32_e32 v2, vcc, s24, v132
	s_lshl_b32 s4, s33, 22
	s_nop 0
	v_addc_co_u32_e32 v3, vcc, 0, v133, vcc
	v_add_co_u32_e32 v4, vcc, s23, v132
	v_readlane_b32 s8, v255, 1
	s_nop 0
	v_addc_co_u32_e32 v5, vcc, 0, v133, vcc
	v_add_co_u32_e32 v10, vcc, s22, v132
	global_load_dwordx4 v[6:9], v[2:3], off nt
	s_nop 0
	global_load_dwordx4 v[2:5], v[4:5], off nt
	v_addc_co_u32_e32 v11, vcc, 0, v133, vcc
	v_add_co_u32_e32 v12, vcc, s21, v132
	v_readlane_b32 s9, v255, 2
	s_nop 0
	v_addc_co_u32_e32 v13, vcc, 0, v133, vcc
	v_add_co_u32_e32 v14, vcc, s20, v132
	global_load_dwordx4 v[18:21], v[10:11], off nt
	s_nop 0
	global_load_dwordx4 v[10:13], v[12:13], off nt
	v_addc_co_u32_e32 v15, vcc, 0, v133, vcc
	v_add_co_u32_e32 v16, vcc, s19, v132
	s_add_u32 s4, s8, s4
	s_nop 0
	v_addc_co_u32_e32 v17, vcc, 0, v133, vcc
	global_load_dwordx4 v[26:29], v[14:15], off nt
	global_load_dwordx4 v[22:25], v[16:17], off nt
	v_add_co_u32_e32 v14, vcc, s18, v132
	s_addc_u32 s9, s9, 0
	s_nop 0
	v_addc_co_u32_e32 v15, vcc, 0, v133, vcc
	v_add_co_u32_e32 v16, vcc, s17, v132
	s_add_u32 s8, s4, s31
	s_nop 0
	v_addc_co_u32_e32 v17, vcc, 0, v133, vcc
	v_add_co_u32_e32 v30, vcc, s16, v132
	global_load_dwordx4 v[42:45], v[14:15], off nt
	s_nop 0
	global_load_dwordx4 v[14:17], v[16:17], off nt
	v_addc_co_u32_e32 v31, vcc, 0, v133, vcc
	v_add_co_u32_e32 v32, vcc, s15, v132
	s_addc_u32 s9, s9, 0
	s_nop 0
	v_addc_co_u32_e32 v33, vcc, 0, v133, vcc
	v_add_co_u32_e32 v38, vcc, s14, v132
	global_load_dwordx4 v[34:37], v[30:31], off nt
	s_nop 0
	global_load_dwordx4 v[30:33], v[32:33], off nt
	v_addc_co_u32_e32 v39, vcc, 0, v133, vcc
	v_add_co_u32_e32 v40, vcc, s13, v132
	v_readlane_b32 s37, v254, 31
	s_nop 0
	v_addc_co_u32_e32 v41, vcc, 0, v133, vcc
	v_add_co_u32_e32 v50, vcc, s12, v132
	global_load_dwordx4 v[46:49], v[38:39], off nt
	s_nop 0
	global_load_dwordx4 v[38:41], v[40:41], off nt
	v_addc_co_u32_e32 v51, vcc, 0, v133, vcc
	v_add_co_u32_e32 v52, vcc, s11, v132
	v_readlane_b32 s38, v254, 32
	s_nop 0
	v_addc_co_u32_e32 v53, vcc, 0, v133, vcc
	v_add_co_u32_e32 v58, vcc, s10, v132
	global_load_dwordx4 v[54:57], v[50:51], off nt
	s_nop 0
	global_load_dwordx4 v[50:53], v[52:53], off nt
	v_addc_co_u32_e32 v59, vcc, 0, v133, vcc
	global_load_dwordx4 v[62:65], v[132:133], off nt
	s_nop 0
	global_load_dwordx4 v[58:61], v[58:59], off nt
	v_readlane_b32 s39, v254, 33
	v_readlane_b32 s40, v254, 34
	v_readlane_b32 s41, v254, 35
	v_readlane_b32 s42, v254, 36
	v_readlane_b32 s43, v254, 37
	v_readlane_b32 s44, v254, 38
	v_readlane_b32 s45, v254, 39
	v_readlane_b32 s46, v254, 40
	v_readlane_b32 s47, v254, 41
	s_branch .LBB0_724

; __device__ __forceinline__ unsigned pk4_fp8(float a, float b, float c, float d) { unsigned w = 0u; w = __builtin_amdgcn_cvt_pk_fp8_f32(a, b, w, false); w = __builtin_amdgcn_cvt_pk_fp8_f32(c, d, w, true); return w; }
; #define LAS __attribute__((address_space(3)))
; #define LDS_WAIT() asm volatile("s_waitcnt lgkmcnt(0)" ::: "memory")
; __device__ __forceinline__ void cvt_pack8(const f32x4 (&v)[16], const CvtItem& c, LAS unsigned char* blk, int s4, int lane) {
;     const float w = c.wscale; const int cb = lane & 15, j = 4 * s4 + (lane >> 4);
; #pragma unroll
;     for (int jn = 0; jn < 4; ++jn) {
;         v4u o; o.x = pg8::pk4_fp8(v[0][jn] * w, v[1][jn] * w, v[2][jn] * w, v[3][jn] * w); o.y = pg8::pk4_fp8(v[4][jn] * w, v[5][jn] * w, v[6][jn] * w, v[7][jn] * w);
;         o.z = pg8::pk4_fp8(v[8][jn] * w, v[9][jn] * w, v[10][jn] * w, v[11][jn] * w); o.w = pg8::pk4_fp8(v[12][jn] * w, v[13][jn] * w, v[14][jn] * w, v[15][jn] * w);
;         *(LAS v4u*)(blk + (4 * cb + jn) * 256 + ((j ^ cb) * 16)) = o; }
; }
; __device__ __forceinline__ void cvt_flush8(const CvtItem& c, const LAS unsigned char* blk, int lane) {
;     LDS_WAIT();
; #pragma unroll
;     for (int t = 0; t < 16; ++t) { const int idx = 64 * t + lane, n = idx >> 4, pc = idx & 15, nn = c.nb * 64 + n;
;         const size_t row = (c.which < 2) ? (size_t)((nn >> 7) * 256 + (nn & 127) + c.which * 128) : (size_t)nn;
;         *(v4u*)(c.dst + row * c.K + 16 * pc) = *(const LAS v4u*)(blk + n * 256 + ((pc ^ ((n >> 2) & 15)) * 16)); }
;     LDS_WAIT();
; }
.LBB0_1448:
	s_waitcnt vmcnt(7)
	v_mul_f32_e32 v66, v179, v66
	s_waitcnt vmcnt(6)
	v_mul_f32_e32 v70, v179, v70
	v_cvt_pk_fp8_f32 v180, v66, v70
	v_mul_f32_e32 v66, v179, v78
	v_mul_f32_e32 v70, v179, v90
	v_cvt_pk_fp8_f32 v181, v66, v70
	s_waitcnt vmcnt(5)
	v_mul_f32_e32 v66, v179, v82
	s_waitcnt vmcnt(4)
	v_mul_f32_e32 v70, v179, v98
	v_cvt_pk_fp8_f32 v182, v66, v70
	s_waitcnt vmcnt(3)
	v_mul_f32_e32 v66, v179, v106
	s_waitcnt vmcnt(2)
	v_mul_f32_e32 v70, v179, v118
	v_mul_f32_e32 v74, v179, v74
	v_mul_f32_e32 v86, v179, v86
	v_cvt_pk_fp8_f32 v183, v66, v70
	v_cvt_pk_fp8_f32 v180, v74, v86 op_sel:[0,0,1]
	v_mul_f32_e32 v74, v179, v94
	v_mul_f32_e32 v78, v179, v110
	v_cvt_pk_fp8_f32 v181, v74, v78 op_sel:[0,0,1]
	v_mul_f32_e32 v74, v179, v102
	v_mul_f32_e32 v78, v179, v114
	v_cvt_pk_fp8_f32 v182, v74, v78 op_sel:[0,0,1]
	s_waitcnt vmcnt(1)
	v_mul_f32_e32 v74, v179, v122
	s_waitcnt vmcnt(0)
	v_mul_f32_e32 v78, v179, v126
	v_cvt_pk_fp8_f32 v183, v74, v78 op_sel:[0,0,1]
	v_mul_f32_e32 v66, v179, v67
	v_mul_f32_e32 v67, v179, v71
	v_mul_f32_e32 v70, v179, v75
	ds_write_b128 v161, v[180:183]
	v_cvt_pk_fp8_f32 v180, v66, v67
	v_mul_f32_e32 v66, v179, v79
	v_mul_f32_e32 v67, v179, v91
	v_cvt_pk_fp8_f32 v181, v66, v67
	v_mul_f32_e32 v66, v179, v83
	v_mul_f32_e32 v67, v179, v99
	v_cvt_pk_fp8_f32 v182, v66, v67
	v_mul_f32_e32 v66, v179, v107
	v_mul_f32_e32 v67, v179, v119
	v_mul_f32_e32 v71, v179, v87
	v_cvt_pk_fp8_f32 v183, v66, v67
	v_cvt_pk_fp8_f32 v180, v70, v71 op_sel:[0,0,1]
	v_mul_f32_e32 v70, v179, v95
	v_mul_f32_e32 v71, v179, v111
	v_cvt_pk_fp8_f32 v181, v70, v71 op_sel:[0,0,1]
	v_mul_f32_e32 v70, v179, v103
	v_mul_f32_e32 v71, v179, v115
	v_cvt_pk_fp8_f32 v182, v70, v71 op_sel:[0,0,1]
	v_mul_f32_e32 v70, v179, v123
	v_mul_f32_e32 v71, v179, v127
	v_cvt_pk_fp8_f32 v183, v70, v71 op_sel:[0,0,1]
	v_mul_f32_e32 v66, v179, v68
	v_mul_f32_e32 v67, v179, v72
	v_mul_f32_e32 v68, v179, v76
	ds_write_b128 v161, v[180:183] offset:256
	v_cvt_pk_fp8_f32 v180, v66, v67
	v_mul_f32_e32 v66, v179, v80
	v_mul_f32_e32 v67, v179, v92
	v_cvt_pk_fp8_f32 v181, v66, v67
	v_mul_f32_e32 v66, v179, v84
	v_mul_f32_e32 v67, v179, v100
	v_cvt_pk_fp8_f32 v182, v66, v67
	v_mul_f32_e32 v66, v179, v108
	v_mul_f32_e32 v67, v179, v120
	v_mul_f32_e32 v70, v179, v88
	v_cvt_pk_fp8_f32 v183, v66, v67
	v_cvt_pk_fp8_f32 v180, v68, v70 op_sel:[0,0,1]
	v_mul_f32_e32 v68, v179, v96
	v_mul_f32_e32 v70, v179, v112
	v_cvt_pk_fp8_f32 v181, v68, v70 op_sel:[0,0,1]
	v_mul_f32_e32 v68, v179, v104
	v_mul_f32_e32 v70, v179, v116
	v_cvt_pk_fp8_f32 v182, v68, v70 op_sel:[0,0,1]
	v_mul_f32_e32 v68, v179, v124
	v_mul_f32_e32 v70, v179, v128
	v_cvt_pk_fp8_f32 v183, v68, v70 op_sel:[0,0,1]
	v_mul_f32_e32 v67, v179, v69
	v_mul_f32_e32 v68, v179, v73
	v_cvt_pk_fp8_f32 v66, v67, v68
	v_mul_f32_e32 v69, v179, v77
	v_mul_f32_e32 v70, v179, v89
	v_mul_f32_e32 v68, v179, v81
	v_cvt_pk_fp8_f32 v66, v69, v70 op_sel:[0,0,1]
	v_mul_f32_e32 v69, v179, v93
	v_cvt_pk_fp8_f32 v67, v68, v69
	v_mul_f32_e32 v70, v179, v97
	v_mul_f32_e32 v71, v179, v113
	v_mul_f32_e32 v69, v179, v85
	v_cvt_pk_fp8_f32 v67, v70, v71 op_sel:[0,0,1]
	v_mul_f32_e32 v70, v179, v101
	v_cvt_pk_fp8_f32 v68, v69, v70
	v_mul_f32_e32 v71, v179, v105
	v_mul_f32_e32 v72, v179, v117
	v_mul_f32_e32 v70, v179, v109
	v_cvt_pk_fp8_f32 v68, v71, v72 op_sel:[0,0,1]
	v_mul_f32_e32 v71, v179, v121
	v_cvt_pk_fp8_f32 v69, v70, v71
	v_mul_f32_e32 v72, v179, v125
	v_mul_f32_e32 v73, v179, v129
	s_lshl_b32 s4, s57, 6
	v_cvt_pk_fp8_f32 v69, v72, v73 op_sel:[0,0,1]
	s_and_b32 s33, s57, 0x1fffffe
	ds_write_b128 v161, v[180:183] offset:512
	s_and_b32 s4, s4, 64
	ds_write_b128 v161, v[66:69] offset:768
	s_add_i32 s33, s33, s56
	s_waitcnt lgkmcnt(0)
	v_or_b32_e32 v66, s4, v142
	s_lshl_b32 s33, s33, 7
	v_or_b32_e32 v70, s33, v66
	ds_read_b128 v[66:69], v162
	v_ashrrev_i32_e32 v71, 31, v70
	v_lshlrev_b64 v[70:71], 10, v[70:71]
	v_lshl_add_u64 v[70:71], s[6:7], 0, v[70:71]
	v_lshl_add_u64 v[70:71], v[70:71], 0, v[134:135]
	s_waitcnt lgkmcnt(0)
	global_store_dwordx4 v[70:71], v[66:69], off nt
	s_add_i32 s25, s25, s26
	s_andn2_b64 vcc, exec, s[2:3]
	v_or_b32_e32 v66, s4, v143
	v_or_b32_e32 v70, s33, v66
	ds_read_b128 v[66:69], v163
	v_ashrrev_i32_e32 v71, 31, v70
	v_lshlrev_b64 v[70:71], 10, v[70:71]
	v_lshl_add_u64 v[70:71], s[6:7], 0, v[70:71]
	v_lshl_add_u64 v[70:71], v[70:71], 0, v[134:135]
	s_waitcnt lgkmcnt(0)
	global_store_dwordx4 v[70:71], v[66:69], off nt
	s_mov_b32 s56, s53
	s_mov_b32 s57, s54
	v_or_b32_e32 v66, s4, v144
	v_or_b32_e32 v70, s33, v66
	ds_read_b128 v[66:69], v164
	v_ashrrev_i32_e32 v71, 31, v70
	v_lshlrev_b64 v[70:71], 10, v[70:71]
	v_lshl_add_u64 v[70:71], s[6:7], 0, v[70:71]
	v_lshl_add_u64 v[70:71], v[70:71], 0, v[134:135]
	s_waitcnt lgkmcnt(0)
	global_store_dwordx4 v[70:71], v[66:69], off nt
	v_mov_b32_e32 v179, v178
	s_nop 0
	v_or_b32_e32 v66, s4, v145
	v_or_b32_e32 v70, s33, v66
	ds_read_b128 v[66:69], v165
	v_ashrrev_i32_e32 v71, 31, v70
	v_lshlrev_b64 v[70:71], 10, v[70:71]
	v_lshl_add_u64 v[70:71], s[6:7], 0, v[70:71]
	v_lshl_add_u64 v[70:71], v[70:71], 0, v[134:135]
	s_waitcnt lgkmcnt(0)
	global_store_dwordx4 v[70:71], v[66:69], off nt
	s_nop 1
	v_or_b32_e32 v66, s4, v146
	v_or_b32_e32 v70, s33, v66
	ds_read_b128 v[66:69], v166
	v_ashrrev_i32_e32 v71, 31, v70
	v_lshlrev_b64 v[70:71], 10, v[70:71]
	v_lshl_add_u64 v[70:71], s[6:7], 0, v[70:71]
	v_lshl_add_u64 v[70:71], v[70:71], 0, v[134:135]
	s_waitcnt lgkmcnt(0)
	global_store_dwordx4 v[70:71], v[66:69], off nt
	s_nop 1
	v_or_b32_e32 v66, s4, v147
	v_or_b32_e32 v70, s33, v66
	ds_read_b128 v[66:69], v167
	v_ashrrev_i32_e32 v71, 31, v70
	v_lshlrev_b64 v[70:71], 10, v[70:71]
	v_lshl_add_u64 v[70:71], s[6:7], 0, v[70:71]
	v_lshl_add_u64 v[70:71], v[70:71], 0, v[134:135]
	s_waitcnt lgkmcnt(0)
; #define LAS __attribute__((address_space(3)))
; #define LDS_WAIT() asm volatile("s_waitcnt lgkmcnt(0)" ::: "memory")
; __device__ __forceinline__ void cvt_flush8(const CvtItem& c, const LAS unsigned char* blk, int lane) {
;     LDS_WAIT();
; #pragma unroll
;     for (int t = 0; t < 16; ++t) { const int idx = 64 * t + lane, n = idx >> 4, pc = idx & 15, nn = c.nb * 64 + n;
;         const size_t row = (c.which < 2) ? (size_t)((nn >> 7) * 256 + (nn & 127) + c.which * 128) : (size_t)nn;
;         *(v4u*)(c.dst + row * c.K + 16 * pc) = *(const LAS v4u*)(blk + n * 256 + ((pc ^ ((n >> 2) & 15)) * 16)); }
;     LDS_WAIT();
; }
	global_store_dwordx4 v[70:71], v[66:69], off nt
	s_nop 1
	v_or_b32_e32 v66, s4, v148
	v_or_b32_e32 v70, s33, v66
	ds_read_b128 v[66:69], v168
	v_ashrrev_i32_e32 v71, 31, v70
	v_lshlrev_b64 v[70:71], 10, v[70:71]
	v_lshl_add_u64 v[70:71], s[6:7], 0, v[70:71]
	v_lshl_add_u64 v[70:71], v[70:71], 0, v[134:135]
	s_waitcnt lgkmcnt(0)
	global_store_dwordx4 v[70:71], v[66:69], off nt
	s_nop 1
	v_or_b32_e32 v66, s4, v149
	v_or_b32_e32 v70, s33, v66
	ds_read_b128 v[66:69], v169
	v_ashrrev_i32_e32 v71, 31, v70
	v_lshlrev_b64 v[70:71], 10, v[70:71]
	v_lshl_add_u64 v[70:71], s[6:7], 0, v[70:71]
	v_lshl_add_u64 v[70:71], v[70:71], 0, v[134:135]
	s_waitcnt lgkmcnt(0)
	global_store_dwordx4 v[70:71], v[66:69], off nt
	s_nop 1
	v_or_b32_e32 v66, s4, v150
	v_or_b32_e32 v70, s33, v66
	ds_read_b128 v[66:69], v170
	v_ashrrev_i32_e32 v71, 31, v70
	v_lshlrev_b64 v[70:71], 10, v[70:71]
	v_lshl_add_u64 v[70:71], s[6:7], 0, v[70:71]
	v_lshl_add_u64 v[70:71], v[70:71], 0, v[134:135]
	s_waitcnt lgkmcnt(0)
	global_store_dwordx4 v[70:71], v[66:69], off nt
	s_nop 1
	v_or_b32_e32 v66, s4, v151
	v_or_b32_e32 v70, s33, v66
	ds_read_b128 v[66:69], v171
	v_ashrrev_i32_e32 v71, 31, v70
	v_lshlrev_b64 v[70:71], 10, v[70:71]
	v_lshl_add_u64 v[70:71], s[6:7], 0, v[70:71]
	v_lshl_add_u64 v[70:71], v[70:71], 0, v[134:135]
	s_waitcnt lgkmcnt(0)
	global_store_dwordx4 v[70:71], v[66:69], off nt
	s_nop 1
	v_or_b32_e32 v66, s4, v152
	v_or_b32_e32 v70, s33, v66
	ds_read_b128 v[66:69], v172
	v_ashrrev_i32_e32 v71, 31, v70
	v_lshlrev_b64 v[70:71], 10, v[70:71]
	v_lshl_add_u64 v[70:71], s[6:7], 0, v[70:71]
	v_lshl_add_u64 v[70:71], v[70:71], 0, v[134:135]
	s_waitcnt lgkmcnt(0)
	global_store_dwordx4 v[70:71], v[66:69], off nt
	s_nop 1
	v_or_b32_e32 v66, s4, v153
	v_or_b32_e32 v70, s33, v66
	ds_read_b128 v[66:69], v173
	v_ashrrev_i32_e32 v71, 31, v70
	v_lshlrev_b64 v[70:71], 10, v[70:71]
	v_lshl_add_u64 v[70:71], s[6:7], 0, v[70:71]
	v_lshl_add_u64 v[70:71], v[70:71], 0, v[134:135]
	s_waitcnt lgkmcnt(0)
	global_store_dwordx4 v[70:71], v[66:69], off nt
	s_nop 1
	v_or_b32_e32 v66, s4, v154
	v_or_b32_e32 v70, s33, v66
	ds_read_b128 v[66:69], v174
	v_ashrrev_i32_e32 v71, 31, v70
	v_lshlrev_b64 v[70:71], 10, v[70:71]
	v_lshl_add_u64 v[70:71], s[6:7], 0, v[70:71]
	v_lshl_add_u64 v[70:71], v[70:71], 0, v[134:135]
	s_waitcnt lgkmcnt(0)
	global_store_dwordx4 v[70:71], v[66:69], off nt
	s_nop 1
	v_or_b32_e32 v66, s4, v155
	v_or_b32_e32 v70, s33, v66
	ds_read_b128 v[66:69], v175
	v_ashrrev_i32_e32 v71, 31, v70
	v_lshlrev_b64 v[70:71], 10, v[70:71]
	v_lshl_add_u64 v[70:71], s[6:7], 0, v[70:71]
	v_lshl_add_u64 v[70:71], v[70:71], 0, v[134:135]
	s_waitcnt lgkmcnt(0)
	global_store_dwordx4 v[70:71], v[66:69], off nt
	s_nop 1
	v_or_b32_e32 v66, s4, v156
	v_or_b32_e32 v70, s33, v66
	ds_read_b128 v[66:69], v176
	v_ashrrev_i32_e32 v71, 31, v70
	v_lshlrev_b64 v[70:71], 10, v[70:71]
	v_lshl_add_u64 v[70:71], s[6:7], 0, v[70:71]
	v_lshl_add_u64 v[70:71], v[70:71], 0, v[134:135]
	s_waitcnt lgkmcnt(0)
	global_store_dwordx4 v[70:71], v[66:69], off nt
	s_nop 1
	v_or_b32_e32 v66, s4, v157
	v_or_b32_e32 v70, s33, v66
	ds_read_b128 v[66:69], v177
	v_ashrrev_i32_e32 v71, 31, v70
	v_lshlrev_b64 v[70:71], 10, v[70:71]
	v_lshl_add_u64 v[70:71], s[6:7], 0, v[70:71]
	v_lshl_add_u64 v[70:71], v[70:71], 0, v[134:135]
	s_waitcnt lgkmcnt(0)
	global_store_dwordx4 v[70:71], v[66:69], off nt
	s_waitcnt lgkmcnt(0)
	s_mov_b64 s[6:7], s[8:9]
	s_cbranch_vccz .LBB0_1451
.LBB0_1449:
	v_readlane_b32 s2, v254, 52
	s_add_i32 s55, s55, s2
	s_mov_b32 s2, 0x80000
	v_add_co_u32_e32 v66, vcc, s2, v132
	s_mov_b32 s2, 0x82000
	s_nop 0
	v_addc_co_u32_e32 v67, vcc, 0, v133, vcc
	v_add_co_u32_e32 v70, vcc, s2, v132
	s_mov_b32 s2, 0x84000
	s_nop 0
	v_addc_co_u32_e32 v71, vcc, 0, v133, vcc
	v_add_co_u32_e32 v74, vcc, s2, v132
	s_mov_b32 s2, 0x86000
	s_nop 0
	v_addc_co_u32_e32 v75, vcc, 0, v133, vcc
	v_add_co_u32_e32 v78, vcc, s2, v132
	s_mov_b32 s2, 0x88000
	s_nop 0
	v_addc_co_u32_e32 v79, vcc, 0, v133, vcc
	global_load_dwordx4 v[82:85], v[78:79], off nt
	v_add_co_u32_e32 v78, vcc, s2, v132
	s_mov_b32 s2, 0x8a000
	s_nop 0
	v_addc_co_u32_e32 v79, vcc, 0, v133, vcc
	v_add_co_u32_e32 v86, vcc, s2, v132
	s_mov_b32 s2, 0x8c000
	s_nop 0
	v_addc_co_u32_e32 v87, vcc, 0, v133, vcc
	global_load_dwordx4 v[90:93], v[86:87], off nt
	v_add_co_u32_e32 v86, vcc, s2, v132
	s_mov_b32 s2, 0x8e000
	s_nop 0
	v_addc_co_u32_e32 v87, vcc, 0, v133, vcc
	global_load_dwordx4 v[94:97], v[86:87], off nt
	v_add_co_u32_e32 v86, vcc, s2, v132
	s_mov_b32 s2, 0x90000
	s_nop 0
	v_addc_co_u32_e32 v87, vcc, 0, v133, vcc
	global_load_dwordx4 v[106:109], v[86:87], off nt
	v_add_co_u32_e32 v86, vcc, s2, v132
	s_mov_b32 s2, 0x92000
	s_nop 0
	v_addc_co_u32_e32 v87, vcc, 0, v133, vcc
	v_add_co_u32_e32 v98, vcc, s2, v132
	s_mov_b32 s2, 0x94000
	s_nop 0
	v_addc_co_u32_e32 v99, vcc, 0, v133, vcc
	v_add_co_u32_e32 v102, vcc, s2, v132
	s_waitcnt vmcnt(4)
; __device__ __forceinline__ unsigned pk4_fp8(float a, float b, float c, float d) { unsigned w = 0u; w = __builtin_amdgcn_cvt_pk_fp8_f32(a, b, w, false); w = __builtin_amdgcn_cvt_pk_fp8_f32(c, d, w, true); return w; }
; #define LAS __attribute__((address_space(3)))
; #define CVT_LOAD(v, c, s_) do { _Pragma("unroll") for (int i_ = 0; i_ < 16; ++i_) v[i_] = *(const f32x4*)((c).src + (size_t)(64 * (s_) + i_) * (c).N); } while (0)
; __device__ __forceinline__ void cvt_pack8(const f32x4 (&v)[16], const CvtItem& c, LAS unsigned char* blk, int s4, int lane) {
;     const float w = c.wscale; const int cb = lane & 15, j = 4 * s4 + (lane >> 4);
; #pragma unroll
;     for (int jn = 0; jn < 4; ++jn) {
;         v4u o; o.x = pg8::pk4_fp8(v[0][jn] * w, v[1][jn] * w, v[2][jn] * w, v[3][jn] * w); o.y = pg8::pk4_fp8(v[4][jn] * w, v[5][jn] * w, v[6][jn] * w, v[7][jn] * w);
;         o.z = pg8::pk4_fp8(v[8][jn] * w, v[9][jn] * w, v[10][jn] * w, v[11][jn] * w); o.w = pg8::pk4_fp8(v[12][jn] * w, v[13][jn] * w, v[14][jn] * w, v[15][jn] * w);
;         *(LAS v4u*)(blk + (4 * cb + jn) * 256 + ((j ^ cb) * 16)) = o; }
; }
; __device__ __forceinline__ void cvt_moe_pipe2(const CvtSrc& A, const CvtSrc& B, LAS float* scr, int gw, int NGW, int lane) {
;     LAS unsigned char* blk = (LAS unsigned char*)scr;
;     f32x4 va[16], vb[16]; CvtItem c, cn;
;     const int it1 = A.n + B.n; int it = gw;
;     if (it < it1) { c = cvt_moe_item2(it, A, B, lane); CVT_LOAD(va, c, 0); }
;     while (it < it1) {
;         const int i1 = it + NGW; const bool more = i1 < it1;
;         CVT_LOAD(vb, c, 1); cvt_pack8(va, c, blk, 0, lane);
;         CVT_LOAD(va, c, 2); cvt_pack8(vb, c, blk, 1, lane);
;         CVT_LOAD(vb, c, 3); cvt_pack8(va, c, blk, 2, lane);
;         if (more) { cn = cvt_moe_item2(i1, A, B, lane); CVT_LOAD(va, cn, 0); }
;         cvt_pack8(vb, c, blk, 3, lane);
	v_mul_f32_e32 v62, v62, v179
	v_mul_f32_e32 v6, v6, v179
	v_addc_co_u32_e32 v103, vcc, 0, v133, vcc
	s_mov_b32 s2, 0x96000
	v_cvt_pk_fp8_f32 v180, v62, v6
	v_add_co_u32_e32 v110, vcc, s2, v132
	s_mov_b32 s2, 0x98000
	s_nop 0
	v_addc_co_u32_e32 v111, vcc, 0, v133, vcc
	global_load_dwordx4 v[102:105], v[102:103], off nt
	v_mul_f32_e32 v2, v2, v179
	global_load_dwordx4 v[114:117], v[110:111], off nt
	v_add_co_u32_e32 v110, vcc, s2, v132
	v_mul_f32_e32 v18, v18, v179
	global_load_dwordx4 v[66:69], v[66:67], off nt
	v_addc_co_u32_e32 v111, vcc, 0, v133, vcc
	global_load_dwordx4 v[70:73], v[70:71], off nt
	s_mov_b32 s2, 0x9a000
	v_cvt_pk_fp8_f32 v180, v2, v18 op_sel:[0,0,1]
	v_mul_f32_e32 v2, v10, v179
	v_mul_f32_e32 v6, v26, v179
	global_load_dwordx4 v[78:81], v[78:79], off nt
	v_add_co_u32_e32 v118, vcc, s2, v132
	v_cvt_pk_fp8_f32 v181, v2, v6
	v_mul_f32_e32 v2, v14, v179
	v_mul_f32_e32 v6, v34, v179
	global_load_dwordx4 v[86:89], v[86:87], off nt
	v_addc_co_u32_e32 v119, vcc, 0, v133, vcc
	global_load_dwordx4 v[98:101], v[98:99], off nt
	s_mov_b32 s2, 0x9c000
	v_cvt_pk_fp8_f32 v182, v2, v6
	v_mul_f32_e32 v2, v38, v179
	v_mul_f32_e32 v6, v54, v179
	global_load_dwordx4 v[110:113], v[110:111], off nt
	v_add_co_u32_e32 v122, vcc, s2, v132
	global_load_dwordx4 v[118:121], v[118:119], off nt
	v_cvt_pk_fp8_f32 v183, v2, v6
	global_load_dwordx4 v[74:77], v[74:75], off nt
	v_addc_co_u32_e32 v123, vcc, 0, v133, vcc
	s_mov_b32 s2, 0x9e000
	v_mul_f32_e32 v10, v22, v179
	v_mul_f32_e32 v18, v42, v179
	v_add_co_u32_e32 v126, vcc, s2, v132
	v_cvt_pk_fp8_f32 v181, v10, v18 op_sel:[0,0,1]
	v_mul_f32_e32 v10, v30, v179
	v_mul_f32_e32 v14, v46, v179
	v_addc_co_u32_e32 v127, vcc, 0, v133, vcc
	v_cvt_pk_fp8_f32 v182, v10, v14 op_sel:[0,0,1]
	v_mul_f32_e32 v10, v50, v179
	v_mul_f32_e32 v14, v58, v179
	global_load_dwordx4 v[122:125], v[122:123], off nt
	v_cvt_pk_fp8_f32 v183, v10, v14 op_sel:[0,0,1]
	global_load_dwordx4 v[126:129], v[126:127], off nt
	v_mul_f32_e32 v2, v63, v179
	v_mul_f32_e32 v6, v7, v179
	ds_write_b128 v158, v[180:183]
	v_cvt_pk_fp8_f32 v180, v2, v6
	v_mul_f32_e32 v3, v3, v179
	v_mul_f32_e32 v7, v19, v179
	v_mul_f32_e32 v2, v11, v179
	v_cvt_pk_fp8_f32 v180, v3, v7 op_sel:[0,0,1]
	v_mul_f32_e32 v3, v27, v179
	v_cvt_pk_fp8_f32 v181, v2, v3
	v_mul_f32_e32 v2, v15, v179
	v_mul_f32_e32 v3, v35, v179
	v_cvt_pk_fp8_f32 v182, v2, v3
	v_mul_f32_e32 v2, v39, v179
	v_mul_f32_e32 v3, v55, v179
	v_cvt_pk_fp8_f32 v183, v2, v3
	v_mul_f32_e32 v6, v23, v179
	v_mul_f32_e32 v7, v43, v179
	v_cvt_pk_fp8_f32 v181, v6, v7 op_sel:[0,0,1]
	v_mul_f32_e32 v6, v31, v179
	v_mul_f32_e32 v7, v47, v179
	v_cvt_pk_fp8_f32 v182, v6, v7 op_sel:[0,0,1]
	v_mul_f32_e32 v6, v51, v179
	v_mul_f32_e32 v7, v59, v179
	v_cvt_pk_fp8_f32 v183, v6, v7 op_sel:[0,0,1]
	v_mul_f32_e32 v2, v64, v179
	v_mul_f32_e32 v3, v8, v179
	v_mul_f32_e32 v4, v4, v179
	ds_write_b128 v158, v[180:183] offset:256
	v_cvt_pk_fp8_f32 v180, v2, v3
	v_mul_f32_e32 v2, v12, v179
	v_mul_f32_e32 v3, v28, v179
	v_cvt_pk_fp8_f32 v181, v2, v3
	v_mul_f32_e32 v2, v16, v179
	v_mul_f32_e32 v3, v36, v179
	v_cvt_pk_fp8_f32 v182, v2, v3
	v_mul_f32_e32 v2, v40, v179
	v_mul_f32_e32 v3, v56, v179
	v_mul_f32_e32 v6, v20, v179
	v_cvt_pk_fp8_f32 v183, v2, v3
	v_cvt_pk_fp8_f32 v180, v4, v6 op_sel:[0,0,1]
	v_mul_f32_e32 v4, v24, v179
	v_mul_f32_e32 v6, v44, v179
	v_cvt_pk_fp8_f32 v181, v4, v6 op_sel:[0,0,1]
	v_mul_f32_e32 v4, v32, v179
	v_mul_f32_e32 v6, v48, v179
	v_cvt_pk_fp8_f32 v182, v4, v6 op_sel:[0,0,1]
	v_mul_f32_e32 v4, v52, v179
	v_mul_f32_e32 v6, v60, v179
	v_cvt_pk_fp8_f32 v183, v4, v6 op_sel:[0,0,1]
	v_mul_f32_e32 v3, v65, v179
	v_mul_f32_e32 v4, v9, v179
	v_cvt_pk_fp8_f32 v2, v3, v4
	v_mul_f32_e32 v5, v5, v179
	v_mul_f32_e32 v6, v21, v179
	v_mul_f32_e32 v4, v13, v179
	v_cvt_pk_fp8_f32 v2, v5, v6 op_sel:[0,0,1]
	v_mul_f32_e32 v5, v29, v179
	v_cvt_pk_fp8_f32 v3, v4, v5
	v_mul_f32_e32 v6, v25, v179
	v_mul_f32_e32 v7, v45, v179
	v_mul_f32_e32 v5, v17, v179
	v_cvt_pk_fp8_f32 v3, v6, v7 op_sel:[0,0,1]
	v_mul_f32_e32 v6, v37, v179
	v_cvt_pk_fp8_f32 v4, v5, v6
	v_mul_f32_e32 v7, v33, v179
	v_mul_f32_e32 v8, v49, v179
	v_mul_f32_e32 v6, v41, v179
	v_cvt_pk_fp8_f32 v4, v7, v8 op_sel:[0,0,1]
	v_mul_f32_e32 v7, v57, v179
	v_cvt_pk_fp8_f32 v5, v6, v7
	v_mul_f32_e32 v8, v53, v179
	v_mul_f32_e32 v9, v61, v179
	s_mov_b32 s2, 0x100000
	v_cvt_pk_fp8_f32 v5, v8, v9 op_sel:[0,0,1]
	ds_write_b128 v158, v[180:183] offset:512
	ds_write_b128 v158, v[2:5] offset:768
	v_add_co_u32_e32 v2, vcc, s2, v132
	s_mov_b32 s2, 0x102000
	s_nop 0
	v_addc_co_u32_e32 v3, vcc, 0, v133, vcc
	global_load_dwordx4 v[62:65], v[2:3], off nt
	v_add_co_u32_e32 v2, vcc, s2, v132
	s_mov_b32 s2, 0x104000
	s_nop 0
	v_addc_co_u32_e32 v3, vcc, 0, v133, vcc
	global_load_dwordx4 v[6:9], v[2:3], off nt
	v_add_co_u32_e32 v2, vcc, s2, v132
	s_mov_b32 s2, 0x106000
	s_nop 0
	v_addc_co_u32_e32 v3, vcc, 0, v133, vcc
	v_add_co_u32_e32 v10, vcc, s2, v132
	s_mov_b32 s2, 0x108000
	s_nop 0
	v_addc_co_u32_e32 v11, vcc, 0, v133, vcc
	global_load_dwordx4 v[2:5], v[2:3], off nt
	s_waitcnt vmcnt(12)
	v_mul_f32_e32 v66, v179, v66
	global_load_dwordx4 v[18:21], v[10:11], off nt
	v_add_co_u32_e32 v10, vcc, s2, v132
	s_mov_b32 s2, 0x10a000
	s_nop 0
	v_addc_co_u32_e32 v11, vcc, 0, v133, vcc
	v_add_co_u32_e32 v14, vcc, s2, v132
	s_mov_b32 s2, 0x10c000
	s_nop 0
	v_addc_co_u32_e32 v15, vcc, 0, v133, vcc
	global_load_dwordx4 v[10:13], v[10:11], off nt
	s_waitcnt vmcnt(13)
	v_mul_f32_e32 v70, v179, v70
	global_load_dwordx4 v[26:29], v[14:15], off nt
	v_add_co_u32_e32 v14, vcc, s2, v132
	s_mov_b32 s2, 0x10e000
	s_nop 0
	v_addc_co_u32_e32 v15, vcc, 0, v133, vcc
	global_load_dwordx4 v[22:25], v[14:15], off nt
	v_add_co_u32_e32 v14, vcc, s2, v132
	v_cvt_pk_fp8_f32 v180, v66, v70
	s_nop 0
	v_addc_co_u32_e32 v15, vcc, 0, v133, vcc
	global_load_dwordx4 v[42:45], v[14:15], off nt
	v_add_co_u32_e32 v14, vcc, s27, v132
	s_waitcnt vmcnt(15)
; __device__ __forceinline__ unsigned pk4_fp8(float a, float b, float c, float d) { unsigned w = 0u; w = __builtin_amdgcn_cvt_pk_fp8_f32(a, b, w, false); w = __builtin_amdgcn_cvt_pk_fp8_f32(c, d, w, true); return w; }
; #define LAS __attribute__((address_space(3)))
; #define CVT_LOAD(v, c, s_) do { _Pragma("unroll") for (int i_ = 0; i_ < 16; ++i_) v[i_] = *(const f32x4*)((c).src + (size_t)(64 * (s_) + i_) * (c).N); } while (0)
; __device__ __forceinline__ void cvt_pack8(const f32x4 (&v)[16], const CvtItem& c, LAS unsigned char* blk, int s4, int lane) {
;     const float w = c.wscale; const int cb = lane & 15, j = 4 * s4 + (lane >> 4);
; #pragma unroll
;     for (int jn = 0; jn < 4; ++jn) {
;         v4u o; o.x = pg8::pk4_fp8(v[0][jn] * w, v[1][jn] * w, v[2][jn] * w, v[3][jn] * w); o.y = pg8::pk4_fp8(v[4][jn] * w, v[5][jn] * w, v[6][jn] * w, v[7][jn] * w);
;         o.z = pg8::pk4_fp8(v[8][jn] * w, v[9][jn] * w, v[10][jn] * w, v[11][jn] * w); o.w = pg8::pk4_fp8(v[12][jn] * w, v[13][jn] * w, v[14][jn] * w, v[15][jn] * w);
;         *(LAS v4u*)(blk + (4 * cb + jn) * 256 + ((j ^ cb) * 16)) = o; }
; }
; __device__ __forceinline__ void cvt_moe_pipe2(const CvtSrc& A, const CvtSrc& B, LAS float* scr, int gw, int NGW, int lane) {
;     LAS unsigned char* blk = (LAS unsigned char*)scr;
;     f32x4 va[16], vb[16]; CvtItem c, cn;
;     const int it1 = A.n + B.n; int it = gw;
;     if (it < it1) { c = cvt_moe_item2(it, A, B, lane); CVT_LOAD(va, c, 0); }
;     while (it < it1) {
;         const int i1 = it + NGW; const bool more = i1 < it1;
;         CVT_LOAD(vb, c, 1); cvt_pack8(va, c, blk, 0, lane);
;         CVT_LOAD(va, c, 2); cvt_pack8(vb, c, blk, 1, lane);
;         CVT_LOAD(vb, c, 3); cvt_pack8(va, c, blk, 2, lane);
;         if (more) { cn = cvt_moe_item2(i1, A, B, lane); CVT_LOAD(va, cn, 0); }
;         cvt_pack8(vb, c, blk, 3, lane);
	v_mul_f32_e32 v66, v179, v78
	v_addc_co_u32_e32 v15, vcc, 0, v133, vcc
	v_add_co_u32_e32 v30, vcc, s28, v132
	global_load_dwordx4 v[14:17], v[14:15], off nt
	s_nop 0
	v_addc_co_u32_e32 v31, vcc, 0, v133, vcc
	global_load_dwordx4 v[34:37], v[30:31], off nt
	v_add_co_u32_e32 v30, vcc, s29, v132
	v_mul_f32_e32 v70, v179, v90
	s_nop 0
	v_addc_co_u32_e32 v31, vcc, 0, v133, vcc
	v_add_co_u32_e32 v38, vcc, s30, v132
	v_cvt_pk_fp8_f32 v181, v66, v70
	s_nop 0
	v_addc_co_u32_e32 v39, vcc, 0, v133, vcc
	s_waitcnt vmcnt(16)
	v_mul_f32_e32 v66, v179, v86
	s_waitcnt vmcnt(15)
	v_mul_f32_e32 v70, v179, v98
	global_load_dwordx4 v[30:33], v[30:31], off nt
	v_cvt_pk_fp8_f32 v182, v66, v70
	global_load_dwordx4 v[46:49], v[38:39], off nt
	v_add_co_u32_e32 v38, vcc, s31, v132
	s_waitcnt vmcnt(16)
	v_mul_f32_e32 v66, v179, v110
	s_waitcnt vmcnt(15)
	v_mul_f32_e32 v70, v179, v118
	v_addc_co_u32_e32 v39, vcc, 0, v133, vcc
	s_waitcnt vmcnt(14)
	v_mul_f32_e32 v74, v179, v74
	v_mul_f32_e32 v82, v179, v82
	v_cvt_pk_fp8_f32 v183, v66, v70
	v_add_co_u32_e32 v50, vcc, s34, v132
	v_cvt_pk_fp8_f32 v180, v74, v82 op_sel:[0,0,1]
	v_mul_f32_e32 v74, v179, v94
	v_mul_f32_e32 v78, v179, v106
	v_addc_co_u32_e32 v51, vcc, 0, v133, vcc
	v_cvt_pk_fp8_f32 v181, v74, v78 op_sel:[0,0,1]
	v_mul_f32_e32 v74, v179, v102
	v_mul_f32_e32 v78, v179, v114
	global_load_dwordx4 v[38:41], v[38:39], off nt
	v_cvt_pk_fp8_f32 v182, v74, v78 op_sel:[0,0,1]
	global_load_dwordx4 v[54:57], v[50:51], off nt
	v_add_co_u32_e32 v50, vcc, s35, v132
	s_waitcnt vmcnt(15)
	v_mul_f32_e32 v74, v179, v122
	s_waitcnt vmcnt(14)
	v_mul_f32_e32 v78, v179, v126
	v_addc_co_u32_e32 v51, vcc, 0, v133, vcc
	v_cvt_pk_fp8_f32 v183, v74, v78 op_sel:[0,0,1]
	v_add_co_u32_e32 v58, vcc, s36, v132
	global_load_dwordx4 v[50:53], v[50:51], off nt
	s_nop 0
	v_addc_co_u32_e32 v59, vcc, 0, v133, vcc
	global_load_dwordx4 v[58:61], v[58:59], off nt
	ds_write_b128 v159, v[180:183]
	v_mul_f32_e32 v66, v179, v67
	v_mul_f32_e32 v67, v179, v71
	v_cvt_pk_fp8_f32 v180, v66, v67
	v_mul_f32_e32 v66, v179, v79
	v_mul_f32_e32 v67, v179, v91
	v_cvt_pk_fp8_f32 v181, v66, v67
	v_mul_f32_e32 v66, v179, v87
	v_mul_f32_e32 v67, v179, v99
	v_cvt_pk_fp8_f32 v182, v66, v67
	v_mul_f32_e32 v66, v179, v111
	v_mul_f32_e32 v67, v179, v119
	v_mul_f32_e32 v70, v179, v75
	v_mul_f32_e32 v71, v179, v83
	v_cvt_pk_fp8_f32 v183, v66, v67
	v_cvt_pk_fp8_f32 v180, v70, v71 op_sel:[0,0,1]
	v_mul_f32_e32 v70, v179, v95
	v_mul_f32_e32 v71, v179, v107
	v_cvt_pk_fp8_f32 v181, v70, v71 op_sel:[0,0,1]
	v_mul_f32_e32 v70, v179, v103
	v_mul_f32_e32 v71, v179, v115
	v_cvt_pk_fp8_f32 v182, v70, v71 op_sel:[0,0,1]
	v_mul_f32_e32 v70, v179, v123
	v_mul_f32_e32 v71, v179, v127
	v_cvt_pk_fp8_f32 v183, v70, v71 op_sel:[0,0,1]
	v_mul_f32_e32 v66, v179, v68
	v_mul_f32_e32 v67, v179, v72
	v_mul_f32_e32 v68, v179, v76
	ds_write_b128 v159, v[180:183] offset:256
	v_cvt_pk_fp8_f32 v180, v66, v67
	v_mul_f32_e32 v66, v179, v80
	v_mul_f32_e32 v67, v179, v92
	v_cvt_pk_fp8_f32 v181, v66, v67
	v_mul_f32_e32 v66, v179, v88
	v_mul_f32_e32 v67, v179, v100
	v_cvt_pk_fp8_f32 v182, v66, v67
	v_mul_f32_e32 v66, v179, v112
	v_mul_f32_e32 v67, v179, v120
	v_mul_f32_e32 v70, v179, v84
	v_cvt_pk_fp8_f32 v183, v66, v67
	v_cvt_pk_fp8_f32 v180, v68, v70 op_sel:[0,0,1]
	v_mul_f32_e32 v68, v179, v96
	v_mul_f32_e32 v70, v179, v108
	v_cvt_pk_fp8_f32 v181, v68, v70 op_sel:[0,0,1]
	v_mul_f32_e32 v68, v179, v104
	v_mul_f32_e32 v70, v179, v116
	v_cvt_pk_fp8_f32 v182, v68, v70 op_sel:[0,0,1]
	v_mul_f32_e32 v68, v179, v124
	v_mul_f32_e32 v70, v179, v128
	v_cvt_pk_fp8_f32 v183, v68, v70 op_sel:[0,0,1]
	v_mul_f32_e32 v67, v179, v69
	v_mul_f32_e32 v68, v179, v73
	v_cvt_pk_fp8_f32 v66, v67, v68
	v_mul_f32_e32 v69, v179, v77
	v_mul_f32_e32 v70, v179, v85
	v_mul_f32_e32 v68, v179, v81
	v_cvt_pk_fp8_f32 v66, v69, v70 op_sel:[0,0,1]
	v_mul_f32_e32 v69, v179, v93
	v_cvt_pk_fp8_f32 v67, v68, v69
	v_mul_f32_e32 v70, v179, v97
	v_mul_f32_e32 v71, v179, v109
	v_mul_f32_e32 v69, v179, v89
	v_cvt_pk_fp8_f32 v67, v70, v71 op_sel:[0,0,1]
	v_mul_f32_e32 v70, v179, v101
	v_cvt_pk_fp8_f32 v68, v69, v70
	v_mul_f32_e32 v71, v179, v105
	v_mul_f32_e32 v72, v179, v117
	v_mul_f32_e32 v70, v179, v113
	v_cvt_pk_fp8_f32 v68, v71, v72 op_sel:[0,0,1]
	v_mul_f32_e32 v71, v179, v121
	v_cvt_pk_fp8_f32 v69, v70, v71
	v_mul_f32_e32 v72, v179, v125
	v_mul_f32_e32 v73, v179, v129
	ds_write_b128 v159, v[180:183] offset:512
	v_cvt_pk_fp8_f32 v69, v72, v73 op_sel:[0,0,1]
	s_waitcnt vmcnt(15)
	v_mul_f32_e32 v130, v179, v62
	s_waitcnt vmcnt(14)
	v_mul_f32_e32 v137, v179, v6
	ds_write_b128 v159, v[66:69] offset:768
	v_add_co_u32_e32 v66, vcc, s37, v132
	v_cvt_pk_fp8_f32 v180, v130, v137
	s_nop 0
	v_addc_co_u32_e32 v67, vcc, 0, v133, vcc
	v_add_co_u32_e32 v70, vcc, s38, v132
	s_waitcnt vmcnt(13)
	v_mul_f32_e32 v181, v179, v2
	v_addc_co_u32_e32 v71, vcc, 0, v133, vcc
	v_add_co_u32_e32 v74, vcc, s39, v132
	s_waitcnt vmcnt(12)
	v_mul_f32_e32 v182, v179, v18
	v_addc_co_u32_e32 v75, vcc, 0, v133, vcc
	v_add_co_u32_e32 v78, vcc, s40, v132
	global_load_dwordx4 v[74:77], v[74:75], off nt
	s_nop 0
	v_addc_co_u32_e32 v79, vcc, 0, v133, vcc
	global_load_dwordx4 v[86:89], v[78:79], off nt
	v_add_co_u32_e32 v78, vcc, s41, v132
	v_cvt_pk_fp8_f32 v180, v181, v182 op_sel:[0,0,1]
	s_nop 0
	v_addc_co_u32_e32 v79, vcc, 0, v133, vcc
	v_add_co_u32_e32 v82, vcc, s42, v132
	global_load_dwordx4 v[78:81], v[78:79], off nt
	s_nop 0
	v_addc_co_u32_e32 v83, vcc, 0, v133, vcc
	global_load_dwordx4 v[90:93], v[82:83], off nt
	v_add_co_u32_e32 v82, vcc, s43, v132
	s_waitcnt vmcnt(15)
	v_mul_f32_e32 v130, v179, v10
	v_addc_co_u32_e32 v83, vcc, 0, v133, vcc
	global_load_dwordx4 v[94:97], v[82:83], off nt
	v_add_co_u32_e32 v82, vcc, s44, v132
	s_waitcnt vmcnt(15)
; __device__ __forceinline__ unsigned pk4_fp8(float a, float b, float c, float d) { unsigned w = 0u; w = __builtin_amdgcn_cvt_pk_fp8_f32(a, b, w, false); w = __builtin_amdgcn_cvt_pk_fp8_f32(c, d, w, true); return w; }
; #define LAS __attribute__((address_space(3)))
; #define CVT_LOAD(v, c, s_) do { _Pragma("unroll") for (int i_ = 0; i_ < 16; ++i_) v[i_] = *(const f32x4*)((c).src + (size_t)(64 * (s_) + i_) * (c).N); } while (0)
; __device__ __forceinline__ void cvt_pack8(const f32x4 (&v)[16], const CvtItem& c, LAS unsigned char* blk, int s4, int lane) {
;     const float w = c.wscale; const int cb = lane & 15, j = 4 * s4 + (lane >> 4);
; #pragma unroll
;     for (int jn = 0; jn < 4; ++jn) {
;         v4u o; o.x = pg8::pk4_fp8(v[0][jn] * w, v[1][jn] * w, v[2][jn] * w, v[3][jn] * w); o.y = pg8::pk4_fp8(v[4][jn] * w, v[5][jn] * w, v[6][jn] * w, v[7][jn] * w);
;         o.z = pg8::pk4_fp8(v[8][jn] * w, v[9][jn] * w, v[10][jn] * w, v[11][jn] * w); o.w = pg8::pk4_fp8(v[12][jn] * w, v[13][jn] * w, v[14][jn] * w, v[15][jn] * w);
;         *(LAS v4u*)(blk + (4 * cb + jn) * 256 + ((j ^ cb) * 16)) = o; }
; }
; __device__ __forceinline__ void cvt_moe_pipe2(const CvtSrc& A, const CvtSrc& B, LAS float* scr, int gw, int NGW, int lane) {
;     LAS unsigned char* blk = (LAS unsigned char*)scr;
;     f32x4 va[16], vb[16]; CvtItem c, cn;
;     const int it1 = A.n + B.n; int it = gw;
;     if (it < it1) { c = cvt_moe_item2(it, A, B, lane); CVT_LOAD(va, c, 0); }
;     while (it < it1) {
;         const int i1 = it + NGW; const bool more = i1 < it1;
;         CVT_LOAD(vb, c, 1); cvt_pack8(va, c, blk, 0, lane);
;         CVT_LOAD(va, c, 2); cvt_pack8(vb, c, blk, 1, lane);
;         CVT_LOAD(vb, c, 3); cvt_pack8(va, c, blk, 2, lane);
;         if (more) { cn = cvt_moe_item2(i1, A, B, lane); CVT_LOAD(va, cn, 0); }
;         cvt_pack8(vb, c, blk, 3, lane);
;         cvt_flush8(c, blk, lane);
;         if (more) c = cn;
	v_mul_f32_e32 v137, v179, v26
	v_addc_co_u32_e32 v83, vcc, 0, v133, vcc
	global_load_dwordx4 v[110:113], v[82:83], off nt
	v_add_co_u32_e32 v82, vcc, s45, v132
	s_nop 0
	v_addc_co_u32_e32 v83, vcc, 0, v133, vcc
	v_add_co_u32_e32 v98, vcc, s46, v132
	v_cvt_pk_fp8_f32 v181, v130, v137
	s_nop 0
	v_addc_co_u32_e32 v99, vcc, 0, v133, vcc
	v_add_co_u32_e32 v102, vcc, s47, v132
	s_waitcnt vmcnt(15)
	v_mul_f32_e32 v182, v179, v22
	v_addc_co_u32_e32 v103, vcc, 0, v133, vcc
	v_add_co_u32_e32 v106, vcc, s48, v132
	global_load_dwordx4 v[102:105], v[102:103], off nt
	s_nop 0
	v_addc_co_u32_e32 v107, vcc, 0, v133, vcc
	global_load_dwordx4 v[114:117], v[106:107], off nt
	v_add_co_u32_e32 v106, vcc, s49, v132
	s_waitcnt vmcnt(16)
	v_mul_f32_e32 v183, v179, v42
	v_addc_co_u32_e32 v107, vcc, 0, v133, vcc
	v_add_co_u32_e32 v118, vcc, s50, v132
	v_cvt_pk_fp8_f32 v181, v182, v183 op_sel:[0,0,1]
	s_waitcnt vmcnt(15)
	v_mul_f32_e32 v130, v179, v14
	s_waitcnt vmcnt(14)
	v_mul_f32_e32 v137, v179, v34
	v_addc_co_u32_e32 v119, vcc, 0, v133, vcc
	v_cvt_pk_fp8_f32 v182, v130, v137
	v_add_co_u32_e32 v122, vcc, s51, v132
	s_waitcnt vmcnt(13)
	v_mul_f32_e32 v183, v179, v30
	v_addc_co_u32_e32 v123, vcc, 0, v133, vcc
	v_add_co_u32_e32 v126, vcc, s52, v132
	s_waitcnt vmcnt(12)
	v_mul_f32_e32 v184, v179, v46
	v_addc_co_u32_e32 v127, vcc, 0, v133, vcc
	v_cvt_pk_fp8_f32 v182, v183, v184 op_sel:[0,0,1]
	s_waitcnt vmcnt(11)
	v_mul_f32_e32 v130, v179, v38
	s_waitcnt vmcnt(10)
	v_mul_f32_e32 v137, v179, v54
	global_load_dwordx4 v[66:69], v[66:67], off nt
	v_cvt_pk_fp8_f32 v183, v130, v137
	global_load_dwordx4 v[70:73], v[70:71], off nt
	s_waitcnt vmcnt(11)
	v_mul_f32_e32 v184, v179, v50
	global_load_dwordx4 v[82:85], v[82:83], off nt
	s_waitcnt vmcnt(11)
	v_mul_f32_e32 v185, v179, v58
	global_load_dwordx4 v[98:101], v[98:99], off nt
	v_cvt_pk_fp8_f32 v183, v184, v185 op_sel:[0,0,1]
	global_load_dwordx4 v[106:109], v[106:107], off nt
	v_mul_f32_e32 v130, v179, v63
	global_load_dwordx4 v[118:121], v[118:119], off nt
	ds_write_b128 v160, v[180:183]
	global_load_dwordx4 v[122:125], v[122:123], off nt
	v_mul_f32_e32 v137, v179, v7
	global_load_dwordx4 v[126:129], v[126:127], off nt
	v_cvt_pk_fp8_f32 v180, v130, v137
	v_mul_f32_e32 v181, v179, v3
	v_mul_f32_e32 v182, v179, v19
	v_mul_f32_e32 v130, v179, v11
	v_cvt_pk_fp8_f32 v180, v181, v182 op_sel:[0,0,1]
	v_mul_f32_e32 v137, v179, v27
	v_cvt_pk_fp8_f32 v181, v130, v137
	v_mul_f32_e32 v182, v179, v23
	v_mul_f32_e32 v183, v179, v43
	v_mul_f32_e32 v130, v179, v15
	v_cvt_pk_fp8_f32 v181, v182, v183 op_sel:[0,0,1]
	v_mul_f32_e32 v137, v179, v35
	v_cvt_pk_fp8_f32 v182, v130, v137
	v_mul_f32_e32 v183, v179, v31
	v_mul_f32_e32 v184, v179, v47
	v_mul_f32_e32 v130, v179, v39
	v_cvt_pk_fp8_f32 v182, v183, v184 op_sel:[0,0,1]
	v_mul_f32_e32 v137, v179, v55
	v_cvt_pk_fp8_f32 v183, v130, v137
	v_mul_f32_e32 v184, v179, v51
	v_mul_f32_e32 v185, v179, v59
	v_mul_f32_e32 v130, v179, v64
	v_cvt_pk_fp8_f32 v183, v184, v185 op_sel:[0,0,1]
	v_mul_f32_e32 v137, v179, v8
	v_mul_f32_e32 v184, v179, v48
	v_mul_f32_e32 v185, v179, v60
	ds_write_b128 v160, v[180:183] offset:256
	v_cvt_pk_fp8_f32 v180, v130, v137
	v_mul_f32_e32 v181, v179, v4
	v_mul_f32_e32 v182, v179, v20
	v_mul_f32_e32 v130, v179, v12
	v_cvt_pk_fp8_f32 v180, v181, v182 op_sel:[0,0,1]
	v_mul_f32_e32 v137, v179, v28
	v_cvt_pk_fp8_f32 v181, v130, v137
	v_mul_f32_e32 v182, v179, v24
	v_mul_f32_e32 v183, v179, v44
	v_mul_f32_e32 v130, v179, v16
	v_cvt_pk_fp8_f32 v181, v182, v183 op_sel:[0,0,1]
	v_mul_f32_e32 v137, v179, v36
	v_cvt_pk_fp8_f32 v182, v130, v137
	v_mul_f32_e32 v183, v179, v32
	v_mul_f32_e32 v130, v179, v40
	v_mul_f32_e32 v137, v179, v56
	v_cvt_pk_fp8_f32 v182, v183, v184 op_sel:[0,0,1]
	v_cvt_pk_fp8_f32 v183, v130, v137
	v_mul_f32_e32 v184, v179, v52
	v_mul_f32_e32 v130, v179, v65
	v_mul_f32_e32 v137, v179, v9
	v_cvt_pk_fp8_f32 v183, v184, v185 op_sel:[0,0,1]
	v_mul_f32_e32 v184, v179, v49
	v_mul_f32_e32 v185, v179, v61
	s_cmpk_gt_i32 s55, 0x50f
	ds_write_b128 v160, v[180:183] offset:512
	v_cvt_pk_fp8_f32 v180, v130, v137
	v_mul_f32_e32 v181, v179, v5
	v_mul_f32_e32 v182, v179, v21
	v_mul_f32_e32 v130, v179, v13
	v_cvt_pk_fp8_f32 v180, v181, v182 op_sel:[0,0,1]
	v_mul_f32_e32 v137, v179, v29
	v_cvt_pk_fp8_f32 v181, v130, v137
	v_mul_f32_e32 v182, v179, v25
	v_mul_f32_e32 v183, v179, v45
	v_mul_f32_e32 v130, v179, v17
	v_cvt_pk_fp8_f32 v181, v182, v183 op_sel:[0,0,1]
	v_mul_f32_e32 v137, v179, v37
	v_cvt_pk_fp8_f32 v182, v130, v137
	v_mul_f32_e32 v183, v179, v33
	v_mul_f32_e32 v130, v179, v41
	v_mul_f32_e32 v137, v179, v57
	v_cvt_pk_fp8_f32 v182, v183, v184 op_sel:[0,0,1]
	v_cvt_pk_fp8_f32 v183, v130, v137
	v_mul_f32_e32 v184, v179, v53
	s_cselect_b64 s[2:3], -1, 0
	s_and_b64 vcc, exec, s[2:3]
	v_cvt_pk_fp8_f32 v183, v184, v185 op_sel:[0,0,1]
	ds_write_b128 v160, v[180:183] offset:768
	s_cbranch_vccnz .LBB0_1448
; __device__ __forceinline__ CvtItem cvt_moe_item(int it, const float* wg, const float* wu, const float* wd, unsigned char* WGU, unsigned char* WDN, int lane) {
;     const int which = it >> 11, r = it & 2047, e = r >> 7, q = r & 127; CvtItem c; c.which = which;
;     if (which < 2) { const int nb = q & 31, k0 = (q >> 5) * 256; c.nb = nb;
;         c.N = DFF; c.K = DM; c.wscale = which ? 64.f / LOG2E : 64.f * LOG2E; c.src = (which ? wu : wg) + (size_t)e * DM * DFF + (size_t)(k0 + 16 * (lane >> 4)) * DFF + nb * 64 + 4 * (lane & 15);
;         c.dst = WGU + (size_t)e * 4096 * DM + k0; }
;     else { const int nb = q & 15, k0 = (q >> 4) * 256; c.nb = nb;
;         c.N = DM; c.K = DFF; c.wscale = 64.f; c.src = wd + (size_t)e * DFF * DM + (size_t)(k0 + 16 * (lane >> 4)) * DM + nb * 64 + 4 * (lane & 15);
;         c.dst = WDN + (size_t)e * DM * DFF + k0; }
;     return c;
; }
	s_add_i32 s4, s55, 0x510
	s_ashr_i32 s53, s4, 11
	s_and_b32 s54, s4, 31
	s_and_b32 s33, s25, 0x300
	v_readlane_b32 s60, v254, 30
	s_cmpk_lt_u32 s4, 0x800
	v_readlane_b32 s61, v254, 31
	v_readlane_b32 s62, v254, 32
	v_readlane_b32 s63, v254, 33
	v_readlane_b32 s72, v254, 42
	v_readlane_b32 s73, v254, 43
	s_cselect_b64 vcc, -1, 0
	v_readlane_b32 s74, v254, 44
	v_readlane_b32 s75, v254, 45
	s_mov_b64 s[60:61], s[72:73]
	s_and_b64 s[8:9], vcc, exec
	s_mov_b64 s[62:63], s[74:75]
	s_cselect_b32 s9, s61, s63
	s_cselect_b32 s8, s60, s62
	s_bfe_u32 s58, s4, 0x40007
	s_lshl_b32 s4, s58, 23
	s_add_u32 s8, s8, s4
	v_or_b32_e32 v2, s33, v141
	s_addc_u32 s9, s9, 0
	v_lshlrev_b32_e32 v130, 13, v2
	v_lshl_add_u64 v[2:3], s[8:9], 0, v[130:131]
	s_lshl_b32 s4, s54, 8
	v_lshl_add_u64 v[2:3], v[2:3], 0, s[4:5]
	v_mov_b32_e32 v137, v131
	v_lshl_add_u64 v[132:133], v[2:3], 0, v[136:137]
	v_cndmask_b32_e32 v178, v139, v140, vcc
	v_add_co_u32_e32 v2, vcc, s24, v132
	s_lshl_b32 s4, s58, 22
	s_nop 0
	v_addc_co_u32_e32 v3, vcc, 0, v133, vcc
	v_add_co_u32_e32 v4, vcc, s23, v132
	v_readlane_b32 s8, v255, 1
	s_nop 0
	v_addc_co_u32_e32 v5, vcc, 0, v133, vcc
	v_add_co_u32_e32 v10, vcc, s22, v132
	global_load_dwordx4 v[6:9], v[2:3], off nt
	s_nop 0
	global_load_dwordx4 v[2:5], v[4:5], off nt
	v_addc_co_u32_e32 v11, vcc, 0, v133, vcc
	v_add_co_u32_e32 v12, vcc, s21, v132
	v_readlane_b32 s9, v255, 2
	s_nop 0
	v_addc_co_u32_e32 v13, vcc, 0, v133, vcc
	v_add_co_u32_e32 v14, vcc, s20, v132
	global_load_dwordx4 v[18:21], v[10:11], off nt
	s_nop 0
	global_load_dwordx4 v[10:13], v[12:13], off nt
	v_addc_co_u32_e32 v15, vcc, 0, v133, vcc
	v_add_co_u32_e32 v16, vcc, s19, v132
	s_add_u32 s4, s8, s4
	s_nop 0
	v_addc_co_u32_e32 v17, vcc, 0, v133, vcc
	global_load_dwordx4 v[26:29], v[14:15], off nt
	global_load_dwordx4 v[22:25], v[16:17], off nt
	v_add_co_u32_e32 v14, vcc, s18, v132
	s_addc_u32 s9, s9, 0
	s_nop 0
	v_addc_co_u32_e32 v15, vcc, 0, v133, vcc
	v_add_co_u32_e32 v16, vcc, s17, v132
	s_add_u32 s8, s4, s33
	s_nop 0
	v_addc_co_u32_e32 v17, vcc, 0, v133, vcc
	v_add_co_u32_e32 v30, vcc, s16, v132
	global_load_dwordx4 v[42:45], v[14:15], off nt
	s_nop 0
	global_load_dwordx4 v[14:17], v[16:17], off nt
	v_addc_co_u32_e32 v31, vcc, 0, v133, vcc
	v_add_co_u32_e32 v32, vcc, s15, v132
	s_addc_u32 s9, s9, 0
	s_nop 0
	v_addc_co_u32_e32 v33, vcc, 0, v133, vcc
	v_add_co_u32_e32 v38, vcc, s14, v132
	global_load_dwordx4 v[34:37], v[30:31], off nt
	s_nop 0
	global_load_dwordx4 v[30:33], v[32:33], off nt
	v_addc_co_u32_e32 v39, vcc, 0, v133, vcc
	v_add_co_u32_e32 v40, vcc, s13, v132
	v_readlane_b32 s64, v254, 34
	s_nop 0
	v_addc_co_u32_e32 v41, vcc, 0, v133, vcc
	v_add_co_u32_e32 v50, vcc, s12, v132
	global_load_dwordx4 v[46:49], v[38:39], off nt
	s_nop 0
	global_load_dwordx4 v[38:41], v[40:41], off nt
	v_addc_co_u32_e32 v51, vcc, 0, v133, vcc
	v_add_co_u32_e32 v52, vcc, s11, v132
	v_readlane_b32 s65, v254, 35
	s_nop 0
	v_addc_co_u32_e32 v53, vcc, 0, v133, vcc
	v_add_co_u32_e32 v58, vcc, s10, v132
	global_load_dwordx4 v[54:57], v[50:51], off nt
	s_nop 0
	global_load_dwordx4 v[50:53], v[52:53], off nt
	v_addc_co_u32_e32 v59, vcc, 0, v133, vcc
	global_load_dwordx4 v[62:65], v[132:133], off nt
	s_nop 0
	global_load_dwordx4 v[58:61], v[58:59], off nt
	v_readlane_b32 s66, v254, 36
	v_readlane_b32 s67, v254, 37
	v_readlane_b32 s68, v254, 38
	v_readlane_b32 s69, v254, 39
	v_readlane_b32 s70, v254, 40
	v_readlane_b32 s71, v254, 41
	s_branch .LBB0_1448

; __device__ __forceinline__ unsigned pk4_fp8(float a, float b, float c, float d) { unsigned w = 0u; w = __builtin_amdgcn_cvt_pk_fp8_f32(a, b, w, false); w = __builtin_amdgcn_cvt_pk_fp8_f32(c, d, w, true); return w; }
; #define LAS __attribute__((address_space(3)))
; #define LDS_WAIT() asm volatile("s_waitcnt lgkmcnt(0)" ::: "memory")
; __device__ __forceinline__ void cvt_pack8(const f32x4 (&v)[16], const CvtItem& c, LAS unsigned char* blk, int s4, int lane) {
;     const float w = c.wscale; const int cb = lane & 15, j = 4 * s4 + (lane >> 4);
; #pragma unroll
;     for (int jn = 0; jn < 4; ++jn) {
;         v4u o; o.x = pg8::pk4_fp8(v[0][jn] * w, v[1][jn] * w, v[2][jn] * w, v[3][jn] * w); o.y = pg8::pk4_fp8(v[4][jn] * w, v[5][jn] * w, v[6][jn] * w, v[7][jn] * w);
;         o.z = pg8::pk4_fp8(v[8][jn] * w, v[9][jn] * w, v[10][jn] * w, v[11][jn] * w); o.w = pg8::pk4_fp8(v[12][jn] * w, v[13][jn] * w, v[14][jn] * w, v[15][jn] * w);
;         *(LAS v4u*)(blk + (4 * cb + jn) * 256 + ((j ^ cb) * 16)) = o; }
; }
; __device__ __forceinline__ void cvt_flush8(const CvtItem& c, const LAS unsigned char* blk, int lane) {
;     LDS_WAIT();
; #pragma unroll
;     for (int t = 0; t < 16; ++t) { const int idx = 64 * t + lane, n = idx >> 4, pc = idx & 15, nn = c.nb * 64 + n;
;         const size_t row = (c.which < 2) ? (size_t)((nn >> 7) * 256 + (nn & 127) + c.which * 128) : (size_t)nn;
;         *(v4u*)(c.dst + row * c.K + 16 * pc) = *(const LAS v4u*)(blk + n * 256 + ((pc ^ ((n >> 2) & 15)) * 16)); }
;     LDS_WAIT();
; }
.LBB0_1455:
	s_waitcnt vmcnt(7)
	v_mul_f32_e32 v66, v177, v66
	s_waitcnt vmcnt(6)
	v_mul_f32_e32 v70, v177, v70
	v_cvt_pk_fp8_f32 v178, v66, v70
	v_mul_f32_e32 v66, v177, v78
	v_mul_f32_e32 v70, v177, v90
	v_cvt_pk_fp8_f32 v179, v66, v70
	s_waitcnt vmcnt(5)
	v_mul_f32_e32 v66, v177, v82
	s_waitcnt vmcnt(4)
	v_mul_f32_e32 v70, v177, v98
	v_cvt_pk_fp8_f32 v180, v66, v70
	s_waitcnt vmcnt(3)
	v_mul_f32_e32 v66, v177, v106
	s_waitcnt vmcnt(2)
	v_mul_f32_e32 v70, v177, v118
	v_mul_f32_e32 v74, v177, v74
	v_mul_f32_e32 v86, v177, v86
	v_cvt_pk_fp8_f32 v181, v66, v70
	v_cvt_pk_fp8_f32 v178, v74, v86 op_sel:[0,0,1]
	v_mul_f32_e32 v74, v177, v94
	v_mul_f32_e32 v78, v177, v110
	v_cvt_pk_fp8_f32 v179, v74, v78 op_sel:[0,0,1]
	v_mul_f32_e32 v74, v177, v102
	v_mul_f32_e32 v78, v177, v114
	v_cvt_pk_fp8_f32 v180, v74, v78 op_sel:[0,0,1]
	s_waitcnt vmcnt(1)
	v_mul_f32_e32 v74, v177, v122
	s_waitcnt vmcnt(0)
	v_mul_f32_e32 v78, v177, v126
	v_cvt_pk_fp8_f32 v181, v74, v78 op_sel:[0,0,1]
	v_mul_f32_e32 v66, v177, v67
	v_mul_f32_e32 v67, v177, v71
	v_mul_f32_e32 v70, v177, v75
	ds_write_b128 v159, v[178:181]
	v_cvt_pk_fp8_f32 v178, v66, v67
	v_mul_f32_e32 v66, v177, v79
	v_mul_f32_e32 v67, v177, v91
	v_cvt_pk_fp8_f32 v179, v66, v67
	v_mul_f32_e32 v66, v177, v83
	v_mul_f32_e32 v67, v177, v99
	v_cvt_pk_fp8_f32 v180, v66, v67
	v_mul_f32_e32 v66, v177, v107
	v_mul_f32_e32 v67, v177, v119
	v_mul_f32_e32 v71, v177, v87
	v_cvt_pk_fp8_f32 v181, v66, v67
	v_cvt_pk_fp8_f32 v178, v70, v71 op_sel:[0,0,1]
	v_mul_f32_e32 v70, v177, v95
	v_mul_f32_e32 v71, v177, v111
	v_cvt_pk_fp8_f32 v179, v70, v71 op_sel:[0,0,1]
	v_mul_f32_e32 v70, v177, v103
	v_mul_f32_e32 v71, v177, v115
	v_cvt_pk_fp8_f32 v180, v70, v71 op_sel:[0,0,1]
	v_mul_f32_e32 v70, v177, v123
	v_mul_f32_e32 v71, v177, v127
	v_cvt_pk_fp8_f32 v181, v70, v71 op_sel:[0,0,1]
	v_mul_f32_e32 v66, v177, v68
	v_mul_f32_e32 v67, v177, v72
	v_mul_f32_e32 v68, v177, v76
	ds_write_b128 v159, v[178:181] offset:256
	v_cvt_pk_fp8_f32 v178, v66, v67
	v_mul_f32_e32 v66, v177, v80
	v_mul_f32_e32 v67, v177, v92
	v_cvt_pk_fp8_f32 v179, v66, v67
	v_mul_f32_e32 v66, v177, v84
	v_mul_f32_e32 v67, v177, v100
	v_cvt_pk_fp8_f32 v180, v66, v67
	v_mul_f32_e32 v66, v177, v108
	v_mul_f32_e32 v67, v177, v120
	v_mul_f32_e32 v70, v177, v88
	v_cvt_pk_fp8_f32 v181, v66, v67
	v_cvt_pk_fp8_f32 v178, v68, v70 op_sel:[0,0,1]
	v_mul_f32_e32 v68, v177, v96
	v_mul_f32_e32 v70, v177, v112
	v_cvt_pk_fp8_f32 v179, v68, v70 op_sel:[0,0,1]
	v_mul_f32_e32 v68, v177, v104
	v_mul_f32_e32 v70, v177, v116
	v_cvt_pk_fp8_f32 v180, v68, v70 op_sel:[0,0,1]
	v_mul_f32_e32 v68, v177, v124
	v_mul_f32_e32 v70, v177, v128
	v_cvt_pk_fp8_f32 v181, v68, v70 op_sel:[0,0,1]
	v_mul_f32_e32 v67, v177, v69
	v_mul_f32_e32 v68, v177, v73
	v_cvt_pk_fp8_f32 v66, v67, v68
	v_mul_f32_e32 v69, v177, v77
	v_mul_f32_e32 v70, v177, v89
	v_mul_f32_e32 v68, v177, v81
	v_cvt_pk_fp8_f32 v66, v69, v70 op_sel:[0,0,1]
	v_mul_f32_e32 v69, v177, v93
	v_cvt_pk_fp8_f32 v67, v68, v69
	v_mul_f32_e32 v70, v177, v97
	v_mul_f32_e32 v71, v177, v113
	v_mul_f32_e32 v69, v177, v85
	v_cvt_pk_fp8_f32 v67, v70, v71 op_sel:[0,0,1]
	v_mul_f32_e32 v70, v177, v101
	v_cvt_pk_fp8_f32 v68, v69, v70
	v_mul_f32_e32 v71, v177, v105
	v_mul_f32_e32 v72, v177, v117
	v_mul_f32_e32 v70, v177, v109
	v_cvt_pk_fp8_f32 v68, v71, v72 op_sel:[0,0,1]
	v_mul_f32_e32 v71, v177, v121
	v_cvt_pk_fp8_f32 v69, v70, v71
	v_mul_f32_e32 v72, v177, v125
	v_mul_f32_e32 v73, v177, v129
	s_lshl_b32 s4, s57, 6
	v_cvt_pk_fp8_f32 v69, v72, v73 op_sel:[0,0,1]
	s_and_b32 s33, s57, 0x1fffffe
	ds_write_b128 v159, v[178:181] offset:512
	s_and_b32 s4, s4, 64
	ds_write_b128 v159, v[66:69] offset:768
	s_add_i32 s33, s33, s56
	s_waitcnt lgkmcnt(0)
	v_or_b32_e32 v66, s4, v138
	s_lshl_b32 s33, s33, 7
	v_or_b32_e32 v70, s33, v66
	ds_read_b128 v[66:69], v160
	v_ashrrev_i32_e32 v71, 31, v70
	v_lshlrev_b64 v[70:71], 10, v[70:71]
	v_lshl_add_u64 v[70:71], s[6:7], 0, v[70:71]
	v_lshl_add_u64 v[70:71], v[70:71], 0, v[134:135]
	s_waitcnt lgkmcnt(0)
	global_store_dwordx4 v[70:71], v[66:69], off nt
	s_add_i32 s2, s2, s3
	s_add_i32 s25, s25, s26
	v_or_b32_e32 v66, s4, v1
	v_or_b32_e32 v70, s33, v66
	ds_read_b128 v[66:69], v161
	v_ashrrev_i32_e32 v71, 31, v70
	v_lshlrev_b64 v[70:71], 10, v[70:71]
	v_lshl_add_u64 v[70:71], s[6:7], 0, v[70:71]
	v_lshl_add_u64 v[70:71], v[70:71], 0, v[134:135]
	s_waitcnt lgkmcnt(0)
	global_store_dwordx4 v[70:71], v[66:69], off nt
	s_mov_b32 s56, s54
	s_mov_b32 s57, s55
	v_or_b32_e32 v66, s4, v142
	v_or_b32_e32 v70, s33, v66
	ds_read_b128 v[66:69], v162
	v_ashrrev_i32_e32 v71, 31, v70
	v_lshlrev_b64 v[70:71], 10, v[70:71]
	v_lshl_add_u64 v[70:71], s[6:7], 0, v[70:71]
	v_lshl_add_u64 v[70:71], v[70:71], 0, v[134:135]
	s_waitcnt lgkmcnt(0)
	global_store_dwordx4 v[70:71], v[66:69], off nt
	v_mov_b32_e32 v177, v176
	s_nop 0
	v_or_b32_e32 v66, s4, v143
	v_or_b32_e32 v70, s33, v66
	ds_read_b128 v[66:69], v163
	v_ashrrev_i32_e32 v71, 31, v70
	v_lshlrev_b64 v[70:71], 10, v[70:71]
	v_lshl_add_u64 v[70:71], s[6:7], 0, v[70:71]
	v_lshl_add_u64 v[70:71], v[70:71], 0, v[134:135]
	s_waitcnt lgkmcnt(0)
	global_store_dwordx4 v[70:71], v[66:69], off nt
	s_nop 1
	v_or_b32_e32 v66, s4, v144
	v_or_b32_e32 v70, s33, v66
	ds_read_b128 v[66:69], v164
	v_ashrrev_i32_e32 v71, 31, v70
	v_lshlrev_b64 v[70:71], 10, v[70:71]
	v_lshl_add_u64 v[70:71], s[6:7], 0, v[70:71]
	v_lshl_add_u64 v[70:71], v[70:71], 0, v[134:135]
	s_waitcnt lgkmcnt(0)
	global_store_dwordx4 v[70:71], v[66:69], off nt
	s_nop 1
	v_or_b32_e32 v66, s4, v145
	v_or_b32_e32 v70, s33, v66
	ds_read_b128 v[66:69], v165
	v_ashrrev_i32_e32 v71, 31, v70
	v_lshlrev_b64 v[70:71], 10, v[70:71]
	v_lshl_add_u64 v[70:71], s[6:7], 0, v[70:71]
	v_lshl_add_u64 v[70:71], v[70:71], 0, v[134:135]
	s_waitcnt lgkmcnt(0)
; #define LAS __attribute__((address_space(3)))
; #define LDS_WAIT() asm volatile("s_waitcnt lgkmcnt(0)" ::: "memory")
; #define CVT_LOAD(v, c, s_) do { _Pragma("unroll") for (int i_ = 0; i_ < 16; ++i_) v[i_] = *(const f32x4*)((c).src + (size_t)(64 * (s_) + i_) * (c).N); } while (0)
; __device__ __forceinline__ void cvt_flush8(const CvtItem& c, const LAS unsigned char* blk, int lane) {
;     LDS_WAIT();
; #pragma unroll
;     for (int t = 0; t < 16; ++t) { const int idx = 64 * t + lane, n = idx >> 4, pc = idx & 15, nn = c.nb * 64 + n;
;         const size_t row = (c.which < 2) ? (size_t)((nn >> 7) * 256 + (nn & 127) + c.which * 128) : (size_t)nn;
;         *(v4u*)(c.dst + row * c.K + 16 * pc) = *(const LAS v4u*)(blk + n * 256 + ((pc ^ ((n >> 2) & 15)) * 16)); }
;     LDS_WAIT();
; }
; __device__ __forceinline__ void cvt_moe_pipe2(const CvtSrc& A, const CvtSrc& B, LAS float* scr, int gw, int NGW, int lane) {
;     LAS unsigned char* blk = (LAS unsigned char*)scr;
;     f32x4 va[16], vb[16]; CvtItem c, cn;
;     const int it1 = A.n + B.n; int it = gw;
;     if (it < it1) { c = cvt_moe_item2(it, A, B, lane); CVT_LOAD(va, c, 0); }
;     while (it < it1) {
;         const int i1 = it + NGW; const bool more = i1 < it1;
;         CVT_LOAD(vb, c, 1); cvt_pack8(va, c, blk, 0, lane);
;         CVT_LOAD(va, c, 2); cvt_pack8(vb, c, blk, 1, lane);
	global_store_dwordx4 v[70:71], v[66:69], off nt
	s_nop 1
	v_or_b32_e32 v66, s4, v146
	v_or_b32_e32 v70, s33, v66
	ds_read_b128 v[66:69], v166
	v_ashrrev_i32_e32 v71, 31, v70
	v_lshlrev_b64 v[70:71], 10, v[70:71]
	v_lshl_add_u64 v[70:71], s[6:7], 0, v[70:71]
	v_lshl_add_u64 v[70:71], v[70:71], 0, v[134:135]
	s_waitcnt lgkmcnt(0)
	global_store_dwordx4 v[70:71], v[66:69], off nt
	s_nop 1
	v_or_b32_e32 v66, s4, v147
	v_or_b32_e32 v70, s33, v66
	ds_read_b128 v[66:69], v167
	v_ashrrev_i32_e32 v71, 31, v70
	v_lshlrev_b64 v[70:71], 10, v[70:71]
	v_lshl_add_u64 v[70:71], s[6:7], 0, v[70:71]
	v_lshl_add_u64 v[70:71], v[70:71], 0, v[134:135]
	s_waitcnt lgkmcnt(0)
	global_store_dwordx4 v[70:71], v[66:69], off nt
	s_nop 1
	v_or_b32_e32 v66, s4, v148
	v_or_b32_e32 v70, s33, v66
	ds_read_b128 v[66:69], v168
	v_ashrrev_i32_e32 v71, 31, v70
	v_lshlrev_b64 v[70:71], 10, v[70:71]
	v_lshl_add_u64 v[70:71], s[6:7], 0, v[70:71]
	v_lshl_add_u64 v[70:71], v[70:71], 0, v[134:135]
	s_waitcnt lgkmcnt(0)
	global_store_dwordx4 v[70:71], v[66:69], off nt
	s_nop 1
	v_or_b32_e32 v66, s4, v149
	v_or_b32_e32 v70, s33, v66
	ds_read_b128 v[66:69], v169
	v_ashrrev_i32_e32 v71, 31, v70
	v_lshlrev_b64 v[70:71], 10, v[70:71]
	v_lshl_add_u64 v[70:71], s[6:7], 0, v[70:71]
	v_lshl_add_u64 v[70:71], v[70:71], 0, v[134:135]
	s_waitcnt lgkmcnt(0)
	global_store_dwordx4 v[70:71], v[66:69], off nt
	s_nop 1
	v_or_b32_e32 v66, s4, v150
	v_or_b32_e32 v70, s33, v66
	ds_read_b128 v[66:69], v170
	v_ashrrev_i32_e32 v71, 31, v70
	v_lshlrev_b64 v[70:71], 10, v[70:71]
	v_lshl_add_u64 v[70:71], s[6:7], 0, v[70:71]
	v_lshl_add_u64 v[70:71], v[70:71], 0, v[134:135]
	s_waitcnt lgkmcnt(0)
	global_store_dwordx4 v[70:71], v[66:69], off nt
	s_nop 1
	v_or_b32_e32 v66, s4, v151
	v_or_b32_e32 v70, s33, v66
	ds_read_b128 v[66:69], v171
	v_ashrrev_i32_e32 v71, 31, v70
	v_lshlrev_b64 v[70:71], 10, v[70:71]
	v_lshl_add_u64 v[70:71], s[6:7], 0, v[70:71]
	v_lshl_add_u64 v[70:71], v[70:71], 0, v[134:135]
	s_waitcnt lgkmcnt(0)
	global_store_dwordx4 v[70:71], v[66:69], off nt
	s_nop 1
	v_or_b32_e32 v66, s4, v152
	v_or_b32_e32 v70, s33, v66
	ds_read_b128 v[66:69], v172
	v_ashrrev_i32_e32 v71, 31, v70
	v_lshlrev_b64 v[70:71], 10, v[70:71]
	v_lshl_add_u64 v[70:71], s[6:7], 0, v[70:71]
	v_lshl_add_u64 v[70:71], v[70:71], 0, v[134:135]
	s_waitcnt lgkmcnt(0)
	global_store_dwordx4 v[70:71], v[66:69], off nt
	s_nop 1
	v_or_b32_e32 v66, s4, v153
	v_or_b32_e32 v70, s33, v66
	ds_read_b128 v[66:69], v173
	v_ashrrev_i32_e32 v71, 31, v70
	v_lshlrev_b64 v[70:71], 10, v[70:71]
	v_lshl_add_u64 v[70:71], s[6:7], 0, v[70:71]
	v_lshl_add_u64 v[70:71], v[70:71], 0, v[134:135]
	s_waitcnt lgkmcnt(0)
	global_store_dwordx4 v[70:71], v[66:69], off nt
	s_nop 1
	v_or_b32_e32 v66, s4, v154
	v_or_b32_e32 v70, s33, v66
	ds_read_b128 v[66:69], v174
	v_ashrrev_i32_e32 v71, 31, v70
	v_lshlrev_b64 v[70:71], 10, v[70:71]
	v_lshl_add_u64 v[70:71], s[6:7], 0, v[70:71]
	v_lshl_add_u64 v[70:71], v[70:71], 0, v[134:135]
	s_waitcnt lgkmcnt(0)
	global_store_dwordx4 v[70:71], v[66:69], off nt
	s_nop 1
	v_or_b32_e32 v66, s4, v155
	v_or_b32_e32 v70, s33, v66
	ds_read_b128 v[66:69], v175
	v_ashrrev_i32_e32 v71, 31, v70
	v_lshlrev_b64 v[70:71], 10, v[70:71]
	v_lshl_add_u64 v[70:71], s[6:7], 0, v[70:71]
	v_lshl_add_u64 v[70:71], v[70:71], 0, v[134:135]
	s_waitcnt lgkmcnt(0)
	global_store_dwordx4 v[70:71], v[66:69], off nt
	s_waitcnt lgkmcnt(0)
	s_add_i32 s4, s2, 0xfffffe00
	s_cmpk_lt_i32 s4, 0x510
	s_mov_b64 s[6:7], s[8:9]
	s_cbranch_scc0 .LBB0_1458
.LBB0_1456:
	s_mov_b32 s58, 0x80000
	v_add_co_u32_e32 v66, vcc, s58, v132
	s_mov_b32 s58, 0x82000
	s_nop 0
	v_addc_co_u32_e32 v67, vcc, 0, v133, vcc
	v_add_co_u32_e32 v70, vcc, s58, v132
	s_mov_b32 s58, 0x84000
	s_nop 0
	v_addc_co_u32_e32 v71, vcc, 0, v133, vcc
	v_add_co_u32_e32 v74, vcc, s58, v132
	s_mov_b32 s58, 0x86000
	s_nop 0
	v_addc_co_u32_e32 v75, vcc, 0, v133, vcc
	v_add_co_u32_e32 v78, vcc, s58, v132
	s_mov_b32 s58, 0x88000
	s_nop 0
	v_addc_co_u32_e32 v79, vcc, 0, v133, vcc
	global_load_dwordx4 v[82:85], v[78:79], off nt
	v_add_co_u32_e32 v78, vcc, s58, v132
	s_mov_b32 s58, 0x8a000
	s_nop 0
	v_addc_co_u32_e32 v79, vcc, 0, v133, vcc
	v_add_co_u32_e32 v86, vcc, s58, v132
	s_mov_b32 s58, 0x8c000
	s_nop 0
	v_addc_co_u32_e32 v87, vcc, 0, v133, vcc
	global_load_dwordx4 v[90:93], v[86:87], off nt
	v_add_co_u32_e32 v86, vcc, s58, v132
	s_mov_b32 s58, 0x8e000
	s_nop 0
	v_addc_co_u32_e32 v87, vcc, 0, v133, vcc
	global_load_dwordx4 v[94:97], v[86:87], off nt
	v_add_co_u32_e32 v86, vcc, s58, v132
	s_mov_b32 s58, 0x90000
	s_nop 0
	v_addc_co_u32_e32 v87, vcc, 0, v133, vcc
	global_load_dwordx4 v[106:109], v[86:87], off nt
	v_add_co_u32_e32 v86, vcc, s58, v132
	s_mov_b32 s58, 0x92000
	s_nop 0
	v_addc_co_u32_e32 v87, vcc, 0, v133, vcc
	v_add_co_u32_e32 v98, vcc, s58, v132
	s_mov_b32 s58, 0x94000
	s_nop 0
	v_addc_co_u32_e32 v99, vcc, 0, v133, vcc
	v_add_co_u32_e32 v102, vcc, s58, v132
	s_waitcnt vmcnt(4)
; __device__ __forceinline__ unsigned pk4_fp8(float a, float b, float c, float d) { unsigned w = 0u; w = __builtin_amdgcn_cvt_pk_fp8_f32(a, b, w, false); w = __builtin_amdgcn_cvt_pk_fp8_f32(c, d, w, true); return w; }
; #define LAS __attribute__((address_space(3)))
; __device__ __forceinline__ void cvt_pack8(const f32x4 (&v)[16], const CvtItem& c, LAS unsigned char* blk, int s4, int lane) {
;     const float w = c.wscale; const int cb = lane & 15, j = 4 * s4 + (lane >> 4);
; #pragma unroll
;     for (int jn = 0; jn < 4; ++jn) {
;         v4u o; o.x = pg8::pk4_fp8(v[0][jn] * w, v[1][jn] * w, v[2][jn] * w, v[3][jn] * w); o.y = pg8::pk4_fp8(v[4][jn] * w, v[5][jn] * w, v[6][jn] * w, v[7][jn] * w);
;         o.z = pg8::pk4_fp8(v[8][jn] * w, v[9][jn] * w, v[10][jn] * w, v[11][jn] * w); o.w = pg8::pk4_fp8(v[12][jn] * w, v[13][jn] * w, v[14][jn] * w, v[15][jn] * w);
;         *(LAS v4u*)(blk + (4 * cb + jn) * 256 + ((j ^ cb) * 16)) = o; }
; }
	v_mul_f32_e32 v62, v62, v177
	v_mul_f32_e32 v6, v6, v177
	v_addc_co_u32_e32 v103, vcc, 0, v133, vcc
	s_mov_b32 s58, 0x96000
	v_cvt_pk_fp8_f32 v178, v62, v6
	v_add_co_u32_e32 v110, vcc, s58, v132
	s_mov_b32 s58, 0x98000
	s_nop 0
	v_addc_co_u32_e32 v111, vcc, 0, v133, vcc
	global_load_dwordx4 v[102:105], v[102:103], off nt
	v_mul_f32_e32 v2, v2, v177
	global_load_dwordx4 v[114:117], v[110:111], off nt
	v_add_co_u32_e32 v110, vcc, s58, v132
	v_mul_f32_e32 v18, v18, v177
	global_load_dwordx4 v[66:69], v[66:67], off nt
	v_addc_co_u32_e32 v111, vcc, 0, v133, vcc
	global_load_dwordx4 v[70:73], v[70:71], off nt
	s_mov_b32 s58, 0x9a000
	v_cvt_pk_fp8_f32 v178, v2, v18 op_sel:[0,0,1]
	v_mul_f32_e32 v2, v10, v177
	v_mul_f32_e32 v6, v26, v177
	global_load_dwordx4 v[78:81], v[78:79], off nt
	v_add_co_u32_e32 v118, vcc, s58, v132
	v_cvt_pk_fp8_f32 v179, v2, v6
	v_mul_f32_e32 v2, v14, v177
	v_mul_f32_e32 v6, v34, v177
	global_load_dwordx4 v[86:89], v[86:87], off nt
	v_addc_co_u32_e32 v119, vcc, 0, v133, vcc
	global_load_dwordx4 v[98:101], v[98:99], off nt
	s_mov_b32 s58, 0x9c000
	v_cvt_pk_fp8_f32 v180, v2, v6
	v_mul_f32_e32 v2, v38, v177
	v_mul_f32_e32 v6, v54, v177
	global_load_dwordx4 v[110:113], v[110:111], off nt
	v_add_co_u32_e32 v122, vcc, s58, v132
	global_load_dwordx4 v[118:121], v[118:119], off nt
	v_cvt_pk_fp8_f32 v181, v2, v6
	global_load_dwordx4 v[74:77], v[74:75], off nt
	v_addc_co_u32_e32 v123, vcc, 0, v133, vcc
	s_mov_b32 s58, 0x9e000
	v_mul_f32_e32 v10, v22, v177
	v_mul_f32_e32 v18, v42, v177
	v_add_co_u32_e32 v126, vcc, s58, v132
	v_cvt_pk_fp8_f32 v179, v10, v18 op_sel:[0,0,1]
	v_mul_f32_e32 v10, v30, v177
	v_mul_f32_e32 v14, v46, v177
	v_addc_co_u32_e32 v127, vcc, 0, v133, vcc
	v_cvt_pk_fp8_f32 v180, v10, v14 op_sel:[0,0,1]
	v_mul_f32_e32 v10, v50, v177
	v_mul_f32_e32 v14, v58, v177
	global_load_dwordx4 v[122:125], v[122:123], off nt
	v_cvt_pk_fp8_f32 v181, v10, v14 op_sel:[0,0,1]
	global_load_dwordx4 v[126:129], v[126:127], off nt
	v_mul_f32_e32 v2, v63, v177
	v_mul_f32_e32 v6, v7, v177
	ds_write_b128 v156, v[178:181]
	v_cvt_pk_fp8_f32 v178, v2, v6
	v_mul_f32_e32 v3, v3, v177
	v_mul_f32_e32 v7, v19, v177
	v_mul_f32_e32 v2, v11, v177
	v_cvt_pk_fp8_f32 v178, v3, v7 op_sel:[0,0,1]
	v_mul_f32_e32 v3, v27, v177
	v_cvt_pk_fp8_f32 v179, v2, v3
	v_mul_f32_e32 v2, v15, v177
	v_mul_f32_e32 v3, v35, v177
	v_cvt_pk_fp8_f32 v180, v2, v3
	v_mul_f32_e32 v2, v39, v177
	v_mul_f32_e32 v3, v55, v177
	v_cvt_pk_fp8_f32 v181, v2, v3
	v_mul_f32_e32 v6, v23, v177
	v_mul_f32_e32 v7, v43, v177
	v_cvt_pk_fp8_f32 v179, v6, v7 op_sel:[0,0,1]
	v_mul_f32_e32 v6, v31, v177
	v_mul_f32_e32 v7, v47, v177
	v_cvt_pk_fp8_f32 v180, v6, v7 op_sel:[0,0,1]
	v_mul_f32_e32 v6, v51, v177
	v_mul_f32_e32 v7, v59, v177
	v_cvt_pk_fp8_f32 v181, v6, v7 op_sel:[0,0,1]
	v_mul_f32_e32 v2, v64, v177
	v_mul_f32_e32 v3, v8, v177
	v_mul_f32_e32 v4, v4, v177
	ds_write_b128 v156, v[178:181] offset:256
	v_cvt_pk_fp8_f32 v178, v2, v3
	v_mul_f32_e32 v2, v12, v177
	v_mul_f32_e32 v3, v28, v177
	v_cvt_pk_fp8_f32 v179, v2, v3
	v_mul_f32_e32 v2, v16, v177
	v_mul_f32_e32 v3, v36, v177
	v_cvt_pk_fp8_f32 v180, v2, v3
	v_mul_f32_e32 v2, v40, v177
	v_mul_f32_e32 v3, v56, v177
	v_mul_f32_e32 v6, v20, v177
	v_cvt_pk_fp8_f32 v181, v2, v3
	v_cvt_pk_fp8_f32 v178, v4, v6 op_sel:[0,0,1]
	v_mul_f32_e32 v4, v24, v177
	v_mul_f32_e32 v6, v44, v177
	v_cvt_pk_fp8_f32 v179, v4, v6 op_sel:[0,0,1]
	v_mul_f32_e32 v4, v32, v177
	v_mul_f32_e32 v6, v48, v177
	v_cvt_pk_fp8_f32 v180, v4, v6 op_sel:[0,0,1]
	v_mul_f32_e32 v4, v52, v177
	v_mul_f32_e32 v6, v60, v177
	v_cvt_pk_fp8_f32 v181, v4, v6 op_sel:[0,0,1]
	v_mul_f32_e32 v3, v65, v177
	v_mul_f32_e32 v4, v9, v177
	v_cvt_pk_fp8_f32 v2, v3, v4
	v_mul_f32_e32 v5, v5, v177
	v_mul_f32_e32 v6, v21, v177
	v_mul_f32_e32 v4, v13, v177
	v_cvt_pk_fp8_f32 v2, v5, v6 op_sel:[0,0,1]
	v_mul_f32_e32 v5, v29, v177
	v_cvt_pk_fp8_f32 v3, v4, v5
	v_mul_f32_e32 v6, v25, v177
	v_mul_f32_e32 v7, v45, v177
	v_mul_f32_e32 v5, v17, v177
	v_cvt_pk_fp8_f32 v3, v6, v7 op_sel:[0,0,1]
	v_mul_f32_e32 v6, v37, v177
	v_cvt_pk_fp8_f32 v4, v5, v6
	v_mul_f32_e32 v7, v33, v177
	v_mul_f32_e32 v8, v49, v177
	v_mul_f32_e32 v6, v41, v177
	v_cvt_pk_fp8_f32 v4, v7, v8 op_sel:[0,0,1]
	v_mul_f32_e32 v7, v57, v177
	v_cvt_pk_fp8_f32 v5, v6, v7
	v_mul_f32_e32 v8, v53, v177
	v_mul_f32_e32 v9, v61, v177
	s_mov_b32 s58, 0x100000
	v_cvt_pk_fp8_f32 v5, v8, v9 op_sel:[0,0,1]
	ds_write_b128 v156, v[178:181] offset:512
	ds_write_b128 v156, v[2:5] offset:768
	v_add_co_u32_e32 v2, vcc, s58, v132
	s_mov_b32 s58, 0x102000
	s_nop 0
	v_addc_co_u32_e32 v3, vcc, 0, v133, vcc
	global_load_dwordx4 v[62:65], v[2:3], off nt
	v_add_co_u32_e32 v2, vcc, s58, v132
	s_mov_b32 s58, 0x104000
	s_nop 0
	v_addc_co_u32_e32 v3, vcc, 0, v133, vcc
	global_load_dwordx4 v[6:9], v[2:3], off nt
	v_add_co_u32_e32 v2, vcc, s58, v132
	s_mov_b32 s58, 0x106000
	s_nop 0
	v_addc_co_u32_e32 v3, vcc, 0, v133, vcc
	v_add_co_u32_e32 v10, vcc, s58, v132
	s_mov_b32 s58, 0x108000
	s_nop 0
	v_addc_co_u32_e32 v11, vcc, 0, v133, vcc
	global_load_dwordx4 v[2:5], v[2:3], off nt
	s_waitcnt vmcnt(12)
	v_mul_f32_e32 v66, v177, v66
	global_load_dwordx4 v[18:21], v[10:11], off nt
	v_add_co_u32_e32 v10, vcc, s58, v132
	s_mov_b32 s58, 0x10a000
	s_nop 0
	v_addc_co_u32_e32 v11, vcc, 0, v133, vcc
	v_add_co_u32_e32 v14, vcc, s58, v132
	s_mov_b32 s58, 0x10c000
	s_nop 0
	v_addc_co_u32_e32 v15, vcc, 0, v133, vcc
	global_load_dwordx4 v[10:13], v[10:11], off nt
	s_waitcnt vmcnt(13)
; __device__ __forceinline__ unsigned pk4_fp8(float a, float b, float c, float d) { unsigned w = 0u; w = __builtin_amdgcn_cvt_pk_fp8_f32(a, b, w, false); w = __builtin_amdgcn_cvt_pk_fp8_f32(c, d, w, true); return w; }
; #define LAS __attribute__((address_space(3)))
; __device__ __forceinline__ void cvt_pack8(const f32x4 (&v)[16], const CvtItem& c, LAS unsigned char* blk, int s4, int lane) {
;     const float w = c.wscale; const int cb = lane & 15, j = 4 * s4 + (lane >> 4);
; #pragma unroll
;     for (int jn = 0; jn < 4; ++jn) {
;         v4u o; o.x = pg8::pk4_fp8(v[0][jn] * w, v[1][jn] * w, v[2][jn] * w, v[3][jn] * w); o.y = pg8::pk4_fp8(v[4][jn] * w, v[5][jn] * w, v[6][jn] * w, v[7][jn] * w);
;         o.z = pg8::pk4_fp8(v[8][jn] * w, v[9][jn] * w, v[10][jn] * w, v[11][jn] * w); o.w = pg8::pk4_fp8(v[12][jn] * w, v[13][jn] * w, v[14][jn] * w, v[15][jn] * w);
;         *(LAS v4u*)(blk + (4 * cb + jn) * 256 + ((j ^ cb) * 16)) = o; }
; }
	v_mul_f32_e32 v70, v177, v70
	global_load_dwordx4 v[26:29], v[14:15], off nt
	v_add_co_u32_e32 v14, vcc, s58, v132
	v_cvt_pk_fp8_f32 v178, v66, v70
	s_nop 0
	v_addc_co_u32_e32 v15, vcc, 0, v133, vcc
	global_load_dwordx4 v[22:25], v[14:15], off nt
	v_add_co_u32_e32 v14, vcc, s27, v132
	v_mul_f32_e32 v70, v177, v90
	s_nop 0
	v_addc_co_u32_e32 v15, vcc, 0, v133, vcc
	global_load_dwordx4 v[42:45], v[14:15], off nt
	v_add_co_u32_e32 v14, vcc, s28, v132
	s_waitcnt vmcnt(15)
	v_mul_f32_e32 v66, v177, v78
	v_addc_co_u32_e32 v15, vcc, 0, v133, vcc
	v_add_co_u32_e32 v30, vcc, s29, v132
	global_load_dwordx4 v[14:17], v[14:15], off nt
	s_nop 0
	v_addc_co_u32_e32 v31, vcc, 0, v133, vcc
	global_load_dwordx4 v[34:37], v[30:31], off nt
	v_add_co_u32_e32 v30, vcc, s30, v132
	v_cvt_pk_fp8_f32 v179, v66, v70
	s_nop 0
	v_addc_co_u32_e32 v31, vcc, 0, v133, vcc
	v_add_co_u32_e32 v38, vcc, s31, v132
	s_waitcnt vmcnt(16)
	v_mul_f32_e32 v66, v177, v86
	v_addc_co_u32_e32 v39, vcc, 0, v133, vcc
	s_waitcnt vmcnt(15)
	v_mul_f32_e32 v70, v177, v98
	global_load_dwordx4 v[30:33], v[30:31], off nt
	v_cvt_pk_fp8_f32 v180, v66, v70
	global_load_dwordx4 v[46:49], v[38:39], off nt
	v_add_co_u32_e32 v38, vcc, s34, v132
	s_waitcnt vmcnt(16)
	v_mul_f32_e32 v66, v177, v110
	s_waitcnt vmcnt(15)
	v_mul_f32_e32 v70, v177, v118
	v_addc_co_u32_e32 v39, vcc, 0, v133, vcc
	s_waitcnt vmcnt(14)
	v_mul_f32_e32 v74, v177, v74
	v_mul_f32_e32 v82, v177, v82
	v_cvt_pk_fp8_f32 v181, v66, v70
	v_add_co_u32_e32 v50, vcc, s35, v132
	v_cvt_pk_fp8_f32 v178, v74, v82 op_sel:[0,0,1]
	v_mul_f32_e32 v74, v177, v94
	v_mul_f32_e32 v78, v177, v106
	v_addc_co_u32_e32 v51, vcc, 0, v133, vcc
	v_cvt_pk_fp8_f32 v179, v74, v78 op_sel:[0,0,1]
	v_mul_f32_e32 v74, v177, v102
	v_mul_f32_e32 v78, v177, v114
	global_load_dwordx4 v[38:41], v[38:39], off nt
	v_cvt_pk_fp8_f32 v180, v74, v78 op_sel:[0,0,1]
	global_load_dwordx4 v[54:57], v[50:51], off nt
	v_add_co_u32_e32 v50, vcc, s36, v132
	s_waitcnt vmcnt(15)
	v_mul_f32_e32 v74, v177, v122
	s_waitcnt vmcnt(14)
	v_mul_f32_e32 v78, v177, v126
	v_addc_co_u32_e32 v51, vcc, 0, v133, vcc
	v_cvt_pk_fp8_f32 v181, v74, v78 op_sel:[0,0,1]
	v_add_co_u32_e32 v58, vcc, s37, v132
	global_load_dwordx4 v[50:53], v[50:51], off nt
	s_nop 0
	v_addc_co_u32_e32 v59, vcc, 0, v133, vcc
	global_load_dwordx4 v[58:61], v[58:59], off nt
	ds_write_b128 v157, v[178:181]
	v_mul_f32_e32 v66, v177, v67
	v_mul_f32_e32 v67, v177, v71
	v_cvt_pk_fp8_f32 v178, v66, v67
	v_mul_f32_e32 v66, v177, v79
	v_mul_f32_e32 v67, v177, v91
	v_cvt_pk_fp8_f32 v179, v66, v67
	v_mul_f32_e32 v66, v177, v87
	v_mul_f32_e32 v67, v177, v99
	v_cvt_pk_fp8_f32 v180, v66, v67
	v_mul_f32_e32 v66, v177, v111
	v_mul_f32_e32 v67, v177, v119
	v_mul_f32_e32 v70, v177, v75
	v_mul_f32_e32 v71, v177, v83
	v_cvt_pk_fp8_f32 v181, v66, v67
	v_cvt_pk_fp8_f32 v178, v70, v71 op_sel:[0,0,1]
	v_mul_f32_e32 v70, v177, v95
	v_mul_f32_e32 v71, v177, v107
	v_cvt_pk_fp8_f32 v179, v70, v71 op_sel:[0,0,1]
	v_mul_f32_e32 v70, v177, v103
	v_mul_f32_e32 v71, v177, v115
	v_cvt_pk_fp8_f32 v180, v70, v71 op_sel:[0,0,1]
	v_mul_f32_e32 v70, v177, v123
	v_mul_f32_e32 v71, v177, v127
	v_cvt_pk_fp8_f32 v181, v70, v71 op_sel:[0,0,1]
	v_mul_f32_e32 v66, v177, v68
	v_mul_f32_e32 v67, v177, v72
	v_mul_f32_e32 v68, v177, v76
	ds_write_b128 v157, v[178:181] offset:256
	v_cvt_pk_fp8_f32 v178, v66, v67
	v_mul_f32_e32 v66, v177, v80
	v_mul_f32_e32 v67, v177, v92
	v_cvt_pk_fp8_f32 v179, v66, v67
	v_mul_f32_e32 v66, v177, v88
	v_mul_f32_e32 v67, v177, v100
	v_cvt_pk_fp8_f32 v180, v66, v67
	v_mul_f32_e32 v66, v177, v112
	v_mul_f32_e32 v67, v177, v120
	v_mul_f32_e32 v70, v177, v84
	v_cvt_pk_fp8_f32 v181, v66, v67
	v_cvt_pk_fp8_f32 v178, v68, v70 op_sel:[0,0,1]
	v_mul_f32_e32 v68, v177, v96
	v_mul_f32_e32 v70, v177, v108
	v_cvt_pk_fp8_f32 v179, v68, v70 op_sel:[0,0,1]
	v_mul_f32_e32 v68, v177, v104
	v_mul_f32_e32 v70, v177, v116
	v_cvt_pk_fp8_f32 v180, v68, v70 op_sel:[0,0,1]
	v_mul_f32_e32 v68, v177, v124
	v_mul_f32_e32 v70, v177, v128
	v_cvt_pk_fp8_f32 v181, v68, v70 op_sel:[0,0,1]
	v_mul_f32_e32 v67, v177, v69
	v_mul_f32_e32 v68, v177, v73
	v_cvt_pk_fp8_f32 v66, v67, v68
	v_mul_f32_e32 v69, v177, v77
	v_mul_f32_e32 v70, v177, v85
	v_mul_f32_e32 v68, v177, v81
	v_cvt_pk_fp8_f32 v66, v69, v70 op_sel:[0,0,1]
	v_mul_f32_e32 v69, v177, v93
	v_cvt_pk_fp8_f32 v67, v68, v69
	v_mul_f32_e32 v70, v177, v97
	v_mul_f32_e32 v71, v177, v109
	v_mul_f32_e32 v69, v177, v89
	v_cvt_pk_fp8_f32 v67, v70, v71 op_sel:[0,0,1]
	v_mul_f32_e32 v70, v177, v101
	v_cvt_pk_fp8_f32 v68, v69, v70
	v_mul_f32_e32 v71, v177, v105
	v_mul_f32_e32 v72, v177, v117
	v_mul_f32_e32 v70, v177, v113
	v_cvt_pk_fp8_f32 v68, v71, v72 op_sel:[0,0,1]
	v_mul_f32_e32 v71, v177, v121
	v_cvt_pk_fp8_f32 v69, v70, v71
	v_mul_f32_e32 v72, v177, v125
	v_mul_f32_e32 v73, v177, v129
	ds_write_b128 v157, v[178:181] offset:512
	v_cvt_pk_fp8_f32 v69, v72, v73 op_sel:[0,0,1]
	s_waitcnt vmcnt(15)
	v_mul_f32_e32 v130, v177, v62
	s_waitcnt vmcnt(14)
	v_mul_f32_e32 v137, v177, v6
	ds_write_b128 v157, v[66:69] offset:768
	v_add_co_u32_e32 v66, vcc, s38, v132
	v_cvt_pk_fp8_f32 v178, v130, v137
	s_nop 0
	v_addc_co_u32_e32 v67, vcc, 0, v133, vcc
	v_add_co_u32_e32 v70, vcc, s39, v132
	s_waitcnt vmcnt(13)
	v_mul_f32_e32 v179, v177, v2
	v_addc_co_u32_e32 v71, vcc, 0, v133, vcc
	v_add_co_u32_e32 v74, vcc, s40, v132
	s_waitcnt vmcnt(12)
; __device__ __forceinline__ unsigned pk4_fp8(float a, float b, float c, float d) { unsigned w = 0u; w = __builtin_amdgcn_cvt_pk_fp8_f32(a, b, w, false); w = __builtin_amdgcn_cvt_pk_fp8_f32(c, d, w, true); return w; }
; #define LAS __attribute__((address_space(3)))
; #define CVT_LOAD(v, c, s_) do { _Pragma("unroll") for (int i_ = 0; i_ < 16; ++i_) v[i_] = *(const f32x4*)((c).src + (size_t)(64 * (s_) + i_) * (c).N); } while (0)
; __device__ __forceinline__ void cvt_pack8(const f32x4 (&v)[16], const CvtItem& c, LAS unsigned char* blk, int s4, int lane) {
;     const float w = c.wscale; const int cb = lane & 15, j = 4 * s4 + (lane >> 4);
; #pragma unroll
;     for (int jn = 0; jn < 4; ++jn) {
;         v4u o; o.x = pg8::pk4_fp8(v[0][jn] * w, v[1][jn] * w, v[2][jn] * w, v[3][jn] * w); o.y = pg8::pk4_fp8(v[4][jn] * w, v[5][jn] * w, v[6][jn] * w, v[7][jn] * w);
;         o.z = pg8::pk4_fp8(v[8][jn] * w, v[9][jn] * w, v[10][jn] * w, v[11][jn] * w); o.w = pg8::pk4_fp8(v[12][jn] * w, v[13][jn] * w, v[14][jn] * w, v[15][jn] * w);
;         *(LAS v4u*)(blk + (4 * cb + jn) * 256 + ((j ^ cb) * 16)) = o; }
; }
; __device__ __forceinline__ void cvt_moe_pipe2(const CvtSrc& A, const CvtSrc& B, LAS float* scr, int gw, int NGW, int lane) {
;     LAS unsigned char* blk = (LAS unsigned char*)scr;
;     f32x4 va[16], vb[16]; CvtItem c, cn;
;     const int it1 = A.n + B.n; int it = gw;
;     if (it < it1) { c = cvt_moe_item2(it, A, B, lane); CVT_LOAD(va, c, 0); }
;     while (it < it1) {
;         const int i1 = it + NGW; const bool more = i1 < it1;
;         CVT_LOAD(vb, c, 1); cvt_pack8(va, c, blk, 0, lane);
;         CVT_LOAD(va, c, 2); cvt_pack8(vb, c, blk, 1, lane);
;         CVT_LOAD(vb, c, 3); cvt_pack8(va, c, blk, 2, lane);
;         if (more) { cn = cvt_moe_item2(i1, A, B, lane); CVT_LOAD(va, cn, 0); }
;         cvt_pack8(vb, c, blk, 3, lane);
;         cvt_flush8(c, blk, lane);
;         if (more) c = cn;
;         it = i1;
	v_mul_f32_e32 v180, v177, v18
	v_addc_co_u32_e32 v75, vcc, 0, v133, vcc
	v_add_co_u32_e32 v78, vcc, s41, v132
	global_load_dwordx4 v[74:77], v[74:75], off nt
	s_nop 0
	v_addc_co_u32_e32 v79, vcc, 0, v133, vcc
	global_load_dwordx4 v[86:89], v[78:79], off nt
	v_add_co_u32_e32 v78, vcc, s42, v132
	v_cvt_pk_fp8_f32 v178, v179, v180 op_sel:[0,0,1]
	s_nop 0
	v_addc_co_u32_e32 v79, vcc, 0, v133, vcc
	v_add_co_u32_e32 v82, vcc, s43, v132
	global_load_dwordx4 v[78:81], v[78:79], off nt
	s_nop 0
	v_addc_co_u32_e32 v83, vcc, 0, v133, vcc
	global_load_dwordx4 v[90:93], v[82:83], off nt
	v_add_co_u32_e32 v82, vcc, s44, v132
	s_waitcnt vmcnt(15)
	v_mul_f32_e32 v130, v177, v10
	v_addc_co_u32_e32 v83, vcc, 0, v133, vcc
	global_load_dwordx4 v[94:97], v[82:83], off nt
	v_add_co_u32_e32 v82, vcc, s45, v132
	s_waitcnt vmcnt(15)
	v_mul_f32_e32 v137, v177, v26
	v_addc_co_u32_e32 v83, vcc, 0, v133, vcc
	global_load_dwordx4 v[110:113], v[82:83], off nt
	v_add_co_u32_e32 v82, vcc, s46, v132
	s_nop 0
	v_addc_co_u32_e32 v83, vcc, 0, v133, vcc
	v_add_co_u32_e32 v98, vcc, s47, v132
	v_cvt_pk_fp8_f32 v179, v130, v137
	s_nop 0
	v_addc_co_u32_e32 v99, vcc, 0, v133, vcc
	v_add_co_u32_e32 v102, vcc, s48, v132
	s_waitcnt vmcnt(15)
	v_mul_f32_e32 v180, v177, v22
	v_addc_co_u32_e32 v103, vcc, 0, v133, vcc
	v_add_co_u32_e32 v106, vcc, s49, v132
	global_load_dwordx4 v[102:105], v[102:103], off nt
	s_nop 0
	v_addc_co_u32_e32 v107, vcc, 0, v133, vcc
	global_load_dwordx4 v[114:117], v[106:107], off nt
	v_add_co_u32_e32 v106, vcc, s50, v132
	s_waitcnt vmcnt(16)
	v_mul_f32_e32 v181, v177, v42
	v_addc_co_u32_e32 v107, vcc, 0, v133, vcc
	v_add_co_u32_e32 v118, vcc, s51, v132
	v_cvt_pk_fp8_f32 v179, v180, v181 op_sel:[0,0,1]
	s_waitcnt vmcnt(15)
	v_mul_f32_e32 v130, v177, v14
	s_waitcnt vmcnt(14)
	v_mul_f32_e32 v137, v177, v34
	v_addc_co_u32_e32 v119, vcc, 0, v133, vcc
	v_cvt_pk_fp8_f32 v180, v130, v137
	v_add_co_u32_e32 v122, vcc, s52, v132
	s_waitcnt vmcnt(13)
	v_mul_f32_e32 v181, v177, v30
	v_addc_co_u32_e32 v123, vcc, 0, v133, vcc
	v_add_co_u32_e32 v126, vcc, s53, v132
	s_waitcnt vmcnt(12)
	v_mul_f32_e32 v182, v177, v46
	v_addc_co_u32_e32 v127, vcc, 0, v133, vcc
	v_cvt_pk_fp8_f32 v180, v181, v182 op_sel:[0,0,1]
	s_waitcnt vmcnt(11)
	v_mul_f32_e32 v130, v177, v38
	s_waitcnt vmcnt(10)
	v_mul_f32_e32 v137, v177, v54
	global_load_dwordx4 v[66:69], v[66:67], off nt
	v_cvt_pk_fp8_f32 v181, v130, v137
	global_load_dwordx4 v[70:73], v[70:71], off nt
	s_waitcnt vmcnt(11)
	v_mul_f32_e32 v182, v177, v50
	global_load_dwordx4 v[82:85], v[82:83], off nt
	s_waitcnt vmcnt(11)
	v_mul_f32_e32 v183, v177, v58
	global_load_dwordx4 v[98:101], v[98:99], off nt
	v_cvt_pk_fp8_f32 v181, v182, v183 op_sel:[0,0,1]
	global_load_dwordx4 v[106:109], v[106:107], off nt
	v_mul_f32_e32 v130, v177, v63
	global_load_dwordx4 v[118:121], v[118:119], off nt
	ds_write_b128 v158, v[178:181]
	global_load_dwordx4 v[122:125], v[122:123], off nt
	v_mul_f32_e32 v137, v177, v7
	global_load_dwordx4 v[126:129], v[126:127], off nt
	v_cvt_pk_fp8_f32 v178, v130, v137
	v_mul_f32_e32 v179, v177, v3
	v_mul_f32_e32 v180, v177, v19
	v_mul_f32_e32 v130, v177, v11
	v_cvt_pk_fp8_f32 v178, v179, v180 op_sel:[0,0,1]
	v_mul_f32_e32 v137, v177, v27
	v_cvt_pk_fp8_f32 v179, v130, v137
	v_mul_f32_e32 v180, v177, v23
	v_mul_f32_e32 v181, v177, v43
	v_mul_f32_e32 v130, v177, v15
	v_cvt_pk_fp8_f32 v179, v180, v181 op_sel:[0,0,1]
	v_mul_f32_e32 v137, v177, v35
	v_cvt_pk_fp8_f32 v180, v130, v137
	v_mul_f32_e32 v181, v177, v31
	v_mul_f32_e32 v182, v177, v47
	v_mul_f32_e32 v130, v177, v39
	v_cvt_pk_fp8_f32 v180, v181, v182 op_sel:[0,0,1]
	v_mul_f32_e32 v137, v177, v55
	v_cvt_pk_fp8_f32 v181, v130, v137
	v_mul_f32_e32 v182, v177, v51
	v_mul_f32_e32 v183, v177, v59
	v_mul_f32_e32 v130, v177, v64
	v_cvt_pk_fp8_f32 v181, v182, v183 op_sel:[0,0,1]
	v_mul_f32_e32 v137, v177, v8
	v_mul_f32_e32 v182, v177, v48
	v_mul_f32_e32 v183, v177, v60
	ds_write_b128 v158, v[178:181] offset:256
	v_cvt_pk_fp8_f32 v178, v130, v137
	v_mul_f32_e32 v179, v177, v4
	v_mul_f32_e32 v180, v177, v20
	v_mul_f32_e32 v130, v177, v12
	v_cvt_pk_fp8_f32 v178, v179, v180 op_sel:[0,0,1]
	v_mul_f32_e32 v137, v177, v28
	v_cvt_pk_fp8_f32 v179, v130, v137
	v_mul_f32_e32 v180, v177, v24
	v_mul_f32_e32 v181, v177, v44
	v_mul_f32_e32 v130, v177, v16
	v_cvt_pk_fp8_f32 v179, v180, v181 op_sel:[0,0,1]
	v_mul_f32_e32 v137, v177, v36
	v_cvt_pk_fp8_f32 v180, v130, v137
	v_mul_f32_e32 v181, v177, v32
	v_mul_f32_e32 v130, v177, v40
	v_mul_f32_e32 v137, v177, v56
	v_cvt_pk_fp8_f32 v180, v181, v182 op_sel:[0,0,1]
	v_cvt_pk_fp8_f32 v181, v130, v137
	v_mul_f32_e32 v182, v177, v52
	v_mul_f32_e32 v130, v177, v65
	v_mul_f32_e32 v137, v177, v9
	v_cvt_pk_fp8_f32 v181, v182, v183 op_sel:[0,0,1]
	v_mul_f32_e32 v182, v177, v49
	v_mul_f32_e32 v183, v177, v61
	v_readlane_b32 s4, v254, 52
	ds_write_b128 v158, v[178:181] offset:512
	v_cvt_pk_fp8_f32 v178, v130, v137
	v_mul_f32_e32 v179, v177, v5
	v_mul_f32_e32 v180, v177, v21
	v_mul_f32_e32 v130, v177, v13
	v_cvt_pk_fp8_f32 v178, v179, v180 op_sel:[0,0,1]
	v_mul_f32_e32 v137, v177, v29
	v_cvt_pk_fp8_f32 v179, v130, v137
	v_mul_f32_e32 v180, v177, v25
	v_mul_f32_e32 v181, v177, v45
	v_mul_f32_e32 v130, v177, v17
	v_cvt_pk_fp8_f32 v179, v180, v181 op_sel:[0,0,1]
	v_mul_f32_e32 v137, v177, v37
	v_cvt_pk_fp8_f32 v180, v130, v137
	v_mul_f32_e32 v181, v177, v33
	v_mul_f32_e32 v130, v177, v41
	v_mul_f32_e32 v137, v177, v57
	v_cvt_pk_fp8_f32 v180, v181, v182 op_sel:[0,0,1]
	v_cvt_pk_fp8_f32 v181, v130, v137
	v_mul_f32_e32 v182, v177, v53
	s_add_i32 s4, s4, s2
	s_add_i32 s33, s4, 0xfffffc00
	v_cvt_pk_fp8_f32 v181, v182, v183 op_sel:[0,0,1]
	s_cmpk_gt_i32 s33, 0x50f
	ds_write_b128 v158, v[178:181] offset:768
	s_cbranch_scc1 .LBB0_1455
; #define LAS __attribute__((address_space(3)))
; #define CVT_LOAD(v, c, s_) do { _Pragma("unroll") for (int i_ = 0; i_ < 16; ++i_) v[i_] = *(const f32x4*)((c).src + (size_t)(64 * (s_) + i_) * (c).N); } while (0)
; __device__ __forceinline__ CvtItem cvt_moe_item(int it, const float* wg, const float* wu, const float* wd, unsigned char* WGU, unsigned char* WDN, int lane) {
;     const int which = it >> 11, r = it & 2047, e = r >> 7, q = r & 127; CvtItem c; c.which = which;
;     if (which < 2) { const int nb = q & 31, k0 = (q >> 5) * 256; c.nb = nb;
;         c.N = DFF; c.K = DM; c.wscale = which ? 64.f / LOG2E : 64.f * LOG2E; c.src = (which ? wu : wg) + (size_t)e * DM * DFF + (size_t)(k0 + 16 * (lane >> 4)) * DFF + nb * 64 + 4 * (lane & 15);
;         c.dst = WGU + (size_t)e * 4096 * DM + k0; }
;     else { const int nb = q & 15, k0 = (q >> 4) * 256; c.nb = nb;
;         c.N = DM; c.K = DFF; c.wscale = 64.f; c.src = wd + (size_t)e * DFF * DM + (size_t)(k0 + 16 * (lane >> 4)) * DM + nb * 64 + 4 * (lane & 15);
;         c.dst = WDN + (size_t)e * DM * DFF + k0; }
;     return c;
; }
; __device__ __forceinline__ CvtItem cvt_moe_item2(int j, const CvtSrc& A, const CvtSrc& B, int lane) {
;     return (j < A.n) ? cvt_moe_item(A.it0 + j, A.wg, A.wu, A.wd, A.WGU, A.WDN, lane) : cvt_moe_item(B.it0 + (j - A.n), B.wg, B.wu, B.wd, B.WGU, B.WDN, lane);
; }
; __device__ __forceinline__ void cvt_moe_pipe2(const CvtSrc& A, const CvtSrc& B, LAS float* scr, int gw, int NGW, int lane) {
;     LAS unsigned char* blk = (LAS unsigned char*)scr;
;     f32x4 va[16], vb[16]; CvtItem c, cn;
;     const int it1 = A.n + B.n; int it = gw;
;     if (it < it1) { c = cvt_moe_item2(it, A, B, lane); CVT_LOAD(va, c, 0); }
;     while (it < it1) {
;         const int i1 = it + NGW; const bool more = i1 < it1;
;         CVT_LOAD(vb, c, 1); cvt_pack8(va, c, blk, 0, lane);
;         CVT_LOAD(va, c, 2); cvt_pack8(vb, c, blk, 1, lane);
;         CVT_LOAD(vb, c, 3); cvt_pack8(va, c, blk, 2, lane);
;         if (more) { cn = cvt_moe_item2(i1, A, B, lane); CVT_LOAD(va, cn, 0); }
	s_addk_i32 s4, 0x110
	s_ashr_i32 s54, s4, 11
	s_and_b32 s55, s4, 31
	s_and_b32 s33, s25, 0x300
	v_readlane_b32 s60, v254, 30
	s_cmpk_lt_u32 s4, 0x800
	v_readlane_b32 s61, v254, 31
	v_readlane_b32 s62, v254, 32
	v_readlane_b32 s63, v254, 33
	v_readlane_b32 s72, v254, 42
	v_readlane_b32 s73, v254, 43
	s_cselect_b64 vcc, -1, 0
	v_readlane_b32 s74, v254, 44
	v_readlane_b32 s75, v254, 45
	s_mov_b64 s[60:61], s[72:73]
	s_and_b64 s[8:9], vcc, exec
	s_mov_b64 s[62:63], s[74:75]
	s_cselect_b32 s9, s61, s63
	s_cselect_b32 s8, s60, s62
	s_bfe_u32 s58, s4, 0x40007
	s_lshl_b32 s4, s58, 23
	s_add_u32 s8, s8, s4
	v_or_b32_e32 v2, s33, v141
	s_addc_u32 s9, s9, 0
	v_lshlrev_b32_e32 v130, 13, v2
	v_lshl_add_u64 v[2:3], s[8:9], 0, v[130:131]
	s_lshl_b32 s4, s55, 8
	v_lshl_add_u64 v[2:3], v[2:3], 0, s[4:5]
	v_mov_b32_e32 v137, v131
	v_lshl_add_u64 v[132:133], v[2:3], 0, v[136:137]
	v_cndmask_b32_e32 v176, v139, v140, vcc
	v_add_co_u32_e32 v2, vcc, s24, v132
	s_lshl_b32 s4, s58, 22
	s_nop 0
	v_addc_co_u32_e32 v3, vcc, 0, v133, vcc
	v_add_co_u32_e32 v4, vcc, s23, v132
	v_readlane_b32 s8, v255, 1
	s_nop 0
	v_addc_co_u32_e32 v5, vcc, 0, v133, vcc
	v_add_co_u32_e32 v10, vcc, s22, v132
	global_load_dwordx4 v[6:9], v[2:3], off nt
	s_nop 0
	global_load_dwordx4 v[2:5], v[4:5], off nt
	v_addc_co_u32_e32 v11, vcc, 0, v133, vcc
	v_add_co_u32_e32 v12, vcc, s21, v132
	v_readlane_b32 s9, v255, 2
	s_nop 0
	v_addc_co_u32_e32 v13, vcc, 0, v133, vcc
	v_add_co_u32_e32 v14, vcc, s20, v132
	global_load_dwordx4 v[18:21], v[10:11], off nt
	s_nop 0
	global_load_dwordx4 v[10:13], v[12:13], off nt
	v_addc_co_u32_e32 v15, vcc, 0, v133, vcc
	v_add_co_u32_e32 v16, vcc, s19, v132
	s_add_u32 s4, s8, s4
	s_nop 0
	v_addc_co_u32_e32 v17, vcc, 0, v133, vcc
	global_load_dwordx4 v[26:29], v[14:15], off nt
	global_load_dwordx4 v[22:25], v[16:17], off nt
	v_add_co_u32_e32 v14, vcc, s18, v132
	s_addc_u32 s9, s9, 0
	s_nop 0
	v_addc_co_u32_e32 v15, vcc, 0, v133, vcc
	v_add_co_u32_e32 v16, vcc, s17, v132
	s_add_u32 s8, s4, s33
	s_nop 0
	v_addc_co_u32_e32 v17, vcc, 0, v133, vcc
	v_add_co_u32_e32 v30, vcc, s16, v132
	global_load_dwordx4 v[42:45], v[14:15], off nt
	s_nop 0
	global_load_dwordx4 v[14:17], v[16:17], off nt
	v_addc_co_u32_e32 v31, vcc, 0, v133, vcc
	v_add_co_u32_e32 v32, vcc, s15, v132
	s_addc_u32 s9, s9, 0
	s_nop 0
	v_addc_co_u32_e32 v33, vcc, 0, v133, vcc
	v_add_co_u32_e32 v38, vcc, s14, v132
	global_load_dwordx4 v[34:37], v[30:31], off nt
	s_nop 0
	global_load_dwordx4 v[30:33], v[32:33], off nt
	v_addc_co_u32_e32 v39, vcc, 0, v133, vcc
	v_add_co_u32_e32 v40, vcc, s13, v132
	v_readlane_b32 s64, v254, 34
	s_nop 0
	v_addc_co_u32_e32 v41, vcc, 0, v133, vcc
	v_add_co_u32_e32 v50, vcc, s12, v132
	global_load_dwordx4 v[46:49], v[38:39], off nt
	s_nop 0
	global_load_dwordx4 v[38:41], v[40:41], off nt
	v_addc_co_u32_e32 v51, vcc, 0, v133, vcc
	v_add_co_u32_e32 v52, vcc, s11, v132
	v_readlane_b32 s65, v254, 35
	s_nop 0
	v_addc_co_u32_e32 v53, vcc, 0, v133, vcc
	v_add_co_u32_e32 v58, vcc, s10, v132
	global_load_dwordx4 v[54:57], v[50:51], off nt
	s_nop 0
	global_load_dwordx4 v[50:53], v[52:53], off nt
	v_addc_co_u32_e32 v59, vcc, 0, v133, vcc
	global_load_dwordx4 v[62:65], v[132:133], off nt
	s_nop 0
	global_load_dwordx4 v[58:61], v[58:59], off nt
	v_readlane_b32 s66, v254, 36
	v_readlane_b32 s67, v254, 37
	v_readlane_b32 s68, v254, 38
	v_readlane_b32 s69, v254, 39
	v_readlane_b32 s70, v254, 40
	v_readlane_b32 s71, v254, 41
	s_branch .LBB0_1455
